# s_setprio flips removed from the ten GEMM K-loops, on top of the barrier change
# speedup vs baseline: 1.0055x; 1.0055x over previous
; #define PG8_LDA(dst, b, h) do { _Pragma("unroll") for (int m = 0; m < 4; ++m) _Pragma("unroll") for (int k = 0; k < 2; ++k) dst[m][k] = *(const PG8_LAS bf16x8*)(lds + PG8_SA(b, h) + aoff + m * 2048 + k * 1024); } while (0)
; #define PG8_LDB(dst, b, h) do { _Pragma("unroll") for (int n = 0; n < 2; ++n) _Pragma("unroll") for (int k = 0; k < 2; ++k) dst[n][k] = *(const PG8_LAS bf16x8*)(lds + PG8_SB(b, h) + boff + n * 2048 + k * 1024); } while (0)
; #define PG8_WAIT_V(n) asm volatile("s_waitcnt vmcnt(" #n ")" ::: "memory")
; #define PG8_WAIT_L(n) asm volatile("s_waitcnt lgkmcnt(" #n ")" ::: "memory")
; #define PG8_BAR __builtin_amdgcn_s_barrier()
; #define PG8_SCHED __builtin_amdgcn_sched_barrier(0)
; template <class Epi, class Sched, bool ALIGN_EPI = false, bool SP2 = false, bool F8 = false, bool I8 = false, bool PF = false>
; __device__ __forceinline__ void gemm_phase(PG8_LAS unsigned char* lds, const Gemm g, const Sched& S, const Epi& E, const int wave_) {
;     ...
;             PG8_LDB(B0, 0, 0); PG8_LDB(B1, 0, 1); PG8_SCHED; PG8_LDA(At, 0, 0); PG8_STAGE(PG8_SA(1, 1), a1 + hstep, voffA);
;             PG8_WAIT_V(8); PG8_WAIT_L(0); PG8_BAR; PG8_MMA(0, 0, At, B0); PG8_MMA(0, 1, At, B1); PG8_BAR; PG8_SCHED;
;             PG8_LDA(At, 0, 1); PG8_STAGE(PG8_SB(0, 0), b2, voffB); PG8_STAGE(PG8_SB(0, 1), b2 + hstep, voffB); PG8_STAGE(PG8_SA(0, 0), a2, voffA);
;             PG8_WAIT_V(8); PG8_WAIT_L(0); PG8_BAR; PG8_MMA(1, 0, At, B0); PG8_MMA(1, 1, At, B1); PG8_BAR; PG8_SCHED;
.LBB0_242:
	ds_read_b128 v[128:131], v180
	ds_read_b128 v[132:135], v180 offset:1024
	ds_read_b128 v[150:153], v180 offset:2048
	ds_read_b128 v[154:157], v180 offset:3072
	ds_read_b128 v[158:161], v181
	ds_read_b128 v[162:165], v181 offset:1024
	ds_read_b128 v[166:169], v181 offset:2048
	ds_read_b128 v[170:173], v181 offset:3072
	s_add_u32 s50, s48, 0xfffe0080
	s_addc_u32 s51, s49, -1
	s_cmp_eq_u32 s79, 4
	s_cselect_b32 s53, s1, s51
	s_cselect_b32 s52, s5, s50
	s_cselect_b32 s51, s39, s78
	s_cselect_b32 s50, s41, s75
	v_lshl_add_u64 v[212:213], s[48:49], 0, v[144:145]
	s_add_i32 m0, s35, 0xc000
	ds_read_b128 v[174:177], v182
	ds_read_b128 v[184:187], v182 offset:1024
	ds_read_b128 v[188:191], v182 offset:2048
	ds_read_b128 v[192:195], v182 offset:3072
	ds_read_b128 v[196:199], v182 offset:4096
	ds_read_b128 v[200:203], v182 offset:5120
	ds_read_b128 v[204:207], v182 offset:6144
	ds_read_b128 v[208:211], v182 offset:7168
	global_load_lds_dwordx4 v[212:213], off
	v_lshl_add_u64 v[212:213], s[48:49], 0, v[146:147]
	s_add_i32 m0, s35, 0xe000
	s_nop 0
	global_load_lds_dwordx4 v[212:213], off
	s_waitcnt vmcnt(8)
	s_waitcnt lgkmcnt(0)
	s_barrier
	s_waitcnt lgkmcnt(0)
	v_mfma_i32_16x16x64_i8 v[124:127], v[128:131], v[174:177], v[124:127]
	v_mfma_i32_16x16x64_i8 v[120:123], v[150:153], v[174:177], v[120:123]
	v_mfma_i32_16x16x64_i8 v[108:111], v[128:131], v[188:191], v[108:111]
	v_mfma_i32_16x16x64_i8 v[104:107], v[150:153], v[188:191], v[104:107]
	v_mfma_i32_16x16x64_i8 v[92:95], v[128:131], v[196:199], v[92:95]
	v_mfma_i32_16x16x64_i8 v[88:91], v[150:153], v[196:199], v[88:91]
	v_mfma_i32_16x16x64_i8 v[76:79], v[128:131], v[204:207], v[76:79]
	v_mfma_i32_16x16x64_i8 v[72:75], v[150:153], v[204:207], v[72:75]
	v_mfma_i32_16x16x64_i8 v[124:127], v[132:135], v[184:187], v[124:127]
	v_mfma_i32_16x16x64_i8 v[120:123], v[154:157], v[184:187], v[120:123]
	v_mfma_i32_16x16x64_i8 v[108:111], v[132:135], v[192:195], v[108:111]
	v_mfma_i32_16x16x64_i8 v[104:107], v[154:157], v[192:195], v[104:107]
	v_mfma_i32_16x16x64_i8 v[92:95], v[132:135], v[200:203], v[92:95]
	v_mfma_i32_16x16x64_i8 v[88:91], v[154:157], v[200:203], v[88:91]
	v_mfma_i32_16x16x64_i8 v[76:79], v[132:135], v[208:211], v[76:79]
	v_mfma_i32_16x16x64_i8 v[72:75], v[154:157], v[208:211], v[72:75]
	v_mfma_i32_16x16x64_i8 v[116:119], v[158:161], v[174:177], v[116:119]
	v_mfma_i32_16x16x64_i8 v[112:115], v[166:169], v[174:177], v[112:115]
	v_mfma_i32_16x16x64_i8 v[100:103], v[158:161], v[188:191], v[100:103]
	v_mfma_i32_16x16x64_i8 v[96:99], v[166:169], v[188:191], v[96:99]
	v_mfma_i32_16x16x64_i8 v[84:87], v[158:161], v[196:199], v[84:87]
	v_mfma_i32_16x16x64_i8 v[80:83], v[166:169], v[196:199], v[80:83]
	v_mfma_i32_16x16x64_i8 v[68:71], v[158:161], v[204:207], v[68:71]
	v_mfma_i32_16x16x64_i8 v[64:67], v[166:169], v[204:207], v[64:67]
	v_mfma_i32_16x16x64_i8 v[116:119], v[162:165], v[184:187], v[116:119]
	v_mfma_i32_16x16x64_i8 v[112:115], v[170:173], v[184:187], v[112:115]
	v_mfma_i32_16x16x64_i8 v[100:103], v[162:165], v[192:195], v[100:103]
	v_mfma_i32_16x16x64_i8 v[96:99], v[170:173], v[192:195], v[96:99]
	v_mfma_i32_16x16x64_i8 v[84:87], v[162:165], v[200:203], v[84:87]
	v_mfma_i32_16x16x64_i8 v[80:83], v[170:173], v[200:203], v[80:83]
	v_mfma_i32_16x16x64_i8 v[68:71], v[162:165], v[208:211], v[68:71]
	v_mfma_i32_16x16x64_i8 v[64:67], v[170:173], v[208:211], v[64:67]
	s_barrier
	s_add_i32 s86, s66, s27
	v_lshl_add_u64 v[212:213], s[50:51], 0, v[138:139]
	s_mov_b32 m0, s86
	ds_read_b128 v[174:177], v182 offset:16384
	ds_read_b128 v[184:187], v182 offset:17408
	ds_read_b128 v[188:191], v182 offset:18432
	ds_read_b128 v[192:195], v182 offset:19456
	ds_read_b128 v[196:199], v182 offset:20480
	ds_read_b128 v[200:203], v182 offset:21504
	ds_read_b128 v[204:207], v182 offset:22528
	ds_read_b128 v[208:211], v182 offset:23552
	global_load_lds_dwordx4 v[212:213], off
	s_add_i32 m0, s86, 0x2000
	s_add_u32 s86, s50, 0x20000
	v_lshl_add_u64 v[214:215], s[50:51], 0, v[142:143]
	s_addc_u32 s87, s51, 0
	s_add_i32 vcc_lo, s67, s27
	global_load_lds_dwordx4 v[214:215], off
	v_lshl_add_u64 v[216:217], s[86:87], 0, v[138:139]
	s_mov_b32 m0, vcc_lo
	v_lshl_add_u64 v[218:219], s[52:53], 0, v[140:141]
	global_load_lds_dwordx4 v[216:217], off
	v_lshl_add_u64 v[216:217], s[86:87], 0, v[142:143]
	s_add_i32 m0, vcc_lo, 0x2000
	s_nop 0
	global_load_lds_dwordx4 v[216:217], off
	v_lshl_add_u64 v[216:217], s[52:53], 0, v[136:137]
	s_mov_b32 m0, s35
	s_nop 0
	global_load_lds_dwordx4 v[216:217], off
	s_mov_b32 m0, s37
	s_nop 0
	global_load_lds_dwordx4 v[218:219], off
	s_waitcnt vmcnt(8)
	s_waitcnt lgkmcnt(0)
	s_barrier
; #define PG8_LDA(dst, b, h) do { _Pragma("unroll") for (int m = 0; m < 4; ++m) _Pragma("unroll") for (int k = 0; k < 2; ++k) dst[m][k] = *(const PG8_LAS bf16x8*)(lds + PG8_SA(b, h) + aoff + m * 2048 + k * 1024); } while (0)
; #define PG8_LDB(dst, b, h) do { _Pragma("unroll") for (int n = 0; n < 2; ++n) _Pragma("unroll") for (int k = 0; k < 2; ++k) dst[n][k] = *(const PG8_LAS bf16x8*)(lds + PG8_SB(b, h) + boff + n * 2048 + k * 1024); } while (0)
; #define PG8_WAIT_V(n) asm volatile("s_waitcnt vmcnt(" #n ")" ::: "memory")
; #define PG8_WAIT_L(n) asm volatile("s_waitcnt lgkmcnt(" #n ")" ::: "memory")
; #define PG8_BAR __builtin_amdgcn_s_barrier()
; #define PG8_SCHED __builtin_amdgcn_sched_barrier(0)
; template <class Epi, class Sched, bool ALIGN_EPI = false, bool SP2 = false, bool F8 = false, bool I8 = false, bool PF = false>
; __device__ __forceinline__ void gemm_phase(PG8_LAS unsigned char* lds, const Gemm g, const Sched& S, const Epi& E, const int wave_) {
;     ...
;             PG8_WAIT_V(8); PG8_WAIT_L(0); PG8_BAR; PG8_MMA(1, 0, At, B0); PG8_MMA(1, 1, At, B1); PG8_BAR; PG8_SCHED;
;             PG8_LDB(B0, 1, 0); PG8_LDB(B1, 1, 1); PG8_SCHED; PG8_LDA(At, 1, 0); PG8_STAGE(PG8_SA(0, 1), a2 + hstep, voffA);
;             PG8_WAIT_V(8); PG8_WAIT_L(0); PG8_BAR; PG8_MMA(0, 0, At, B0); PG8_MMA(0, 1, At, B1); PG8_BAR; PG8_SCHED;
	s_waitcnt lgkmcnt(0)
	v_mfma_i32_16x16x64_i8 v[60:63], v[128:131], v[174:177], v[60:63]
	v_mfma_i32_16x16x64_i8 v[56:59], v[150:153], v[174:177], v[56:59]
	v_mfma_i32_16x16x64_i8 v[44:47], v[128:131], v[188:191], v[44:47]
	v_mfma_i32_16x16x64_i8 v[40:43], v[150:153], v[188:191], v[40:43]
	v_mfma_i32_16x16x64_i8 v[28:31], v[128:131], v[196:199], v[28:31]
	v_mfma_i32_16x16x64_i8 v[24:27], v[150:153], v[196:199], v[24:27]
	v_mfma_i32_16x16x64_i8 v[12:15], v[128:131], v[204:207], v[12:15]
	v_mfma_i32_16x16x64_i8 v[8:11], v[150:153], v[204:207], v[8:11]
	v_mfma_i32_16x16x64_i8 v[60:63], v[132:135], v[184:187], v[60:63]
	v_mfma_i32_16x16x64_i8 v[56:59], v[154:157], v[184:187], v[56:59]
	v_mfma_i32_16x16x64_i8 v[44:47], v[132:135], v[192:195], v[44:47]
	v_mfma_i32_16x16x64_i8 v[40:43], v[154:157], v[192:195], v[40:43]
	v_mfma_i32_16x16x64_i8 v[28:31], v[132:135], v[200:203], v[28:31]
	v_mfma_i32_16x16x64_i8 v[24:27], v[154:157], v[200:203], v[24:27]
	v_mfma_i32_16x16x64_i8 v[12:15], v[132:135], v[208:211], v[12:15]
	v_mfma_i32_16x16x64_i8 v[8:11], v[154:157], v[208:211], v[8:11]
	v_mfma_i32_16x16x64_i8 v[52:55], v[158:161], v[174:177], v[52:55]
	v_mfma_i32_16x16x64_i8 v[48:51], v[166:169], v[174:177], v[48:51]
	v_mfma_i32_16x16x64_i8 v[36:39], v[158:161], v[188:191], v[36:39]
	v_mfma_i32_16x16x64_i8 v[32:35], v[166:169], v[188:191], v[32:35]
	v_mfma_i32_16x16x64_i8 v[20:23], v[158:161], v[196:199], v[20:23]
	v_mfma_i32_16x16x64_i8 v[16:19], v[166:169], v[196:199], v[16:19]
	v_mfma_i32_16x16x64_i8 v[4:7], v[158:161], v[204:207], v[4:7]
	v_mfma_i32_16x16x64_i8 v[0:3], v[166:169], v[204:207], v[0:3]
	v_mfma_i32_16x16x64_i8 v[52:55], v[162:165], v[184:187], v[52:55]
	v_mfma_i32_16x16x64_i8 v[48:51], v[170:173], v[184:187], v[48:51]
	v_mfma_i32_16x16x64_i8 v[36:39], v[162:165], v[192:195], v[36:39]
	v_mfma_i32_16x16x64_i8 v[32:35], v[170:173], v[192:195], v[32:35]
	v_mfma_i32_16x16x64_i8 v[20:23], v[162:165], v[200:203], v[20:23]
	v_mfma_i32_16x16x64_i8 v[16:19], v[170:173], v[200:203], v[16:19]
	v_mfma_i32_16x16x64_i8 v[4:7], v[162:165], v[208:211], v[4:7]
	v_mfma_i32_16x16x64_i8 v[0:3], v[170:173], v[208:211], v[0:3]
	s_barrier
	s_add_i32 s86, 0, 0x18000
	s_add_i32 s87, 0, 0x1c000
	v_add_u32_e32 v154, s86, v179
	v_add_u32_e32 v170, s87, v179
	ds_read_b128 v[128:131], v154
	ds_read_b128 v[132:135], v154 offset:1024
	ds_read_b128 v[150:153], v154 offset:2048
	ds_read_b128 v[154:157], v154 offset:3072
	ds_read_b128 v[158:161], v170
	ds_read_b128 v[162:165], v170 offset:1024
	ds_read_b128 v[166:169], v170 offset:2048
	ds_read_b128 v[170:173], v170 offset:3072
	s_add_u32 s52, s52, 0x20000
	s_addc_u32 s53, s53, 0
	s_mov_b32 m0, s54
	v_lshl_add_u64 v[220:221], s[52:53], 0, v[136:137]
	ds_read_b128 v[174:177], v182 offset:32768
	ds_read_b128 v[184:187], v182 offset:33792
	ds_read_b128 v[188:191], v182 offset:34816
	ds_read_b128 v[192:195], v182 offset:35840
	ds_read_b128 v[196:199], v182 offset:36864
	ds_read_b128 v[200:203], v182 offset:37888
	ds_read_b128 v[204:207], v182 offset:38912
	ds_read_b128 v[208:211], v182 offset:39936
	global_load_lds_dwordx4 v[220:221], off
	v_lshl_add_u64 v[220:221], s[52:53], 0, v[140:141]
	s_mov_b32 m0, s55
	s_nop 0
	global_load_lds_dwordx4 v[220:221], off
	s_waitcnt vmcnt(8)
	s_waitcnt lgkmcnt(0)
	s_barrier
	s_waitcnt lgkmcnt(0)
	v_mfma_i32_16x16x64_i8 v[124:127], v[128:131], v[174:177], v[124:127]
	v_mfma_i32_16x16x64_i8 v[120:123], v[150:153], v[174:177], v[120:123]
	v_mfma_i32_16x16x64_i8 v[108:111], v[128:131], v[188:191], v[108:111]
	v_mfma_i32_16x16x64_i8 v[104:107], v[150:153], v[188:191], v[104:107]
	v_mfma_i32_16x16x64_i8 v[92:95], v[128:131], v[196:199], v[92:95]
	v_mfma_i32_16x16x64_i8 v[88:91], v[150:153], v[196:199], v[88:91]
	v_mfma_i32_16x16x64_i8 v[76:79], v[128:131], v[204:207], v[76:79]
	v_mfma_i32_16x16x64_i8 v[72:75], v[150:153], v[204:207], v[72:75]
	v_mfma_i32_16x16x64_i8 v[124:127], v[132:135], v[184:187], v[124:127]
	v_mfma_i32_16x16x64_i8 v[120:123], v[154:157], v[184:187], v[120:123]
	v_mfma_i32_16x16x64_i8 v[108:111], v[132:135], v[192:195], v[108:111]
	v_mfma_i32_16x16x64_i8 v[104:107], v[154:157], v[192:195], v[104:107]
	v_mfma_i32_16x16x64_i8 v[92:95], v[132:135], v[200:203], v[92:95]
	v_mfma_i32_16x16x64_i8 v[88:91], v[154:157], v[200:203], v[88:91]
	v_mfma_i32_16x16x64_i8 v[76:79], v[132:135], v[208:211], v[76:79]
	v_mfma_i32_16x16x64_i8 v[72:75], v[154:157], v[208:211], v[72:75]
	v_mfma_i32_16x16x64_i8 v[116:119], v[158:161], v[174:177], v[116:119]
	v_mfma_i32_16x16x64_i8 v[112:115], v[166:169], v[174:177], v[112:115]
	v_mfma_i32_16x16x64_i8 v[100:103], v[158:161], v[188:191], v[100:103]
	v_mfma_i32_16x16x64_i8 v[96:99], v[166:169], v[188:191], v[96:99]
	v_mfma_i32_16x16x64_i8 v[84:87], v[158:161], v[196:199], v[84:87]
	v_mfma_i32_16x16x64_i8 v[80:83], v[166:169], v[196:199], v[80:83]
	v_mfma_i32_16x16x64_i8 v[68:71], v[158:161], v[204:207], v[68:71]
	v_mfma_i32_16x16x64_i8 v[64:67], v[166:169], v[204:207], v[64:67]
	v_mfma_i32_16x16x64_i8 v[116:119], v[162:165], v[184:187], v[116:119]
	v_mfma_i32_16x16x64_i8 v[112:115], v[170:173], v[184:187], v[112:115]
	v_mfma_i32_16x16x64_i8 v[100:103], v[162:165], v[192:195], v[100:103]
	v_mfma_i32_16x16x64_i8 v[96:99], v[170:173], v[192:195], v[96:99]
	v_mfma_i32_16x16x64_i8 v[84:87], v[162:165], v[200:203], v[84:87]
	v_mfma_i32_16x16x64_i8 v[80:83], v[170:173], v[200:203], v[80:83]
	v_mfma_i32_16x16x64_i8 v[68:71], v[162:165], v[208:211], v[68:71]
	v_mfma_i32_16x16x64_i8 v[64:67], v[170:173], v[208:211], v[64:67]
	s_barrier
; #define PG8_LDA(dst, b, h) do { _Pragma("unroll") for (int m = 0; m < 4; ++m) _Pragma("unroll") for (int k = 0; k < 2; ++k) dst[m][k] = *(const PG8_LAS bf16x8*)(lds + PG8_SA(b, h) + aoff + m * 2048 + k * 1024); } while (0)
; #define PG8_WAIT_V(n) asm volatile("s_waitcnt vmcnt(" #n ")" ::: "memory")
; #define PG8_WAIT_L(n) asm volatile("s_waitcnt lgkmcnt(" #n ")" ::: "memory")
; #define PG8_BAR __builtin_amdgcn_s_barrier()
; #define PG8_SCHED __builtin_amdgcn_sched_barrier(0)
; template <class Epi, class Sched, bool ALIGN_EPI = false, bool SP2 = false, bool F8 = false, bool I8 = false, bool PF = false>
; __device__ __forceinline__ void gemm_phase(PG8_LAS unsigned char* lds, const Gemm g, const Sched& S, const Epi& E, const int wave_) {
;     ...
;             PG8_LDA(At, 1, 1); PG8_STAGE(PG8_SB(1, 0), b3, voffB); PG8_STAGE(PG8_SB(1, 1), b3 + hstep, voffB); PG8_STAGE(PG8_SA(1, 0), a3, voffA);
;             PG8_WAIT_V(8); PG8_WAIT_L(0); PG8_BAR; PG8_MMA(1, 0, At, B0); PG8_MMA(1, 1, At, B1); PG8_BAR; PG8_SCHED;
	s_add_i32 s52, s86, s27
	v_lshl_add_u64 v[212:213], v[212:213], 0, s[14:15]
	s_mov_b32 m0, s52
	ds_read_b128 v[174:177], v182 offset:49152
	ds_read_b128 v[184:187], v182 offset:50176
	ds_read_b128 v[188:191], v182 offset:51200
	ds_read_b128 v[192:195], v182 offset:52224
	ds_read_b128 v[196:199], v182 offset:53248
	ds_read_b128 v[200:203], v182 offset:54272
	ds_read_b128 v[204:207], v182 offset:55296
	ds_read_b128 v[208:211], v182 offset:56320
	global_load_lds_dwordx4 v[212:213], off
	s_add_i32 m0, s52, 0x2000
	s_add_u32 s50, s50, 0x20080
	v_lshl_add_u64 v[212:213], v[214:215], 0, s[14:15]
	s_addc_u32 s51, s51, 0
	s_add_i32 s52, s87, s27
	global_load_lds_dwordx4 v[212:213], off
	v_lshl_add_u64 v[212:213], s[50:51], 0, v[138:139]
	s_mov_b32 m0, s52
	s_nop 0
	global_load_lds_dwordx4 v[212:213], off
	v_lshl_add_u64 v[212:213], s[50:51], 0, v[142:143]
	s_add_i32 m0, s52, 0x2000
	s_nop 0
	global_load_lds_dwordx4 v[212:213], off
	v_lshl_add_u64 v[212:213], v[216:217], 0, s[14:15]
	s_mov_b32 m0, s63
	s_nop 0
	global_load_lds_dwordx4 v[212:213], off
	v_lshl_add_u64 v[212:213], v[218:219], 0, s[14:15]
	s_mov_b32 m0, s64
	s_nop 0
	global_load_lds_dwordx4 v[212:213], off
	s_waitcnt vmcnt(8)
	s_waitcnt lgkmcnt(0)
	s_barrier
	s_waitcnt lgkmcnt(0)
	v_mfma_i32_16x16x64_i8 v[60:63], v[128:131], v[174:177], v[60:63]
	v_mfma_i32_16x16x64_i8 v[56:59], v[150:153], v[174:177], v[56:59]
	v_mfma_i32_16x16x64_i8 v[44:47], v[128:131], v[188:191], v[44:47]
	v_mfma_i32_16x16x64_i8 v[40:43], v[150:153], v[188:191], v[40:43]
	v_mfma_i32_16x16x64_i8 v[28:31], v[128:131], v[196:199], v[28:31]
	v_mfma_i32_16x16x64_i8 v[24:27], v[150:153], v[196:199], v[24:27]
	v_mfma_i32_16x16x64_i8 v[12:15], v[128:131], v[204:207], v[12:15]
	v_mfma_i32_16x16x64_i8 v[8:11], v[150:153], v[204:207], v[8:11]
	v_mfma_i32_16x16x64_i8 v[60:63], v[132:135], v[184:187], v[60:63]
	v_mfma_i32_16x16x64_i8 v[56:59], v[154:157], v[184:187], v[56:59]
	v_mfma_i32_16x16x64_i8 v[44:47], v[132:135], v[192:195], v[44:47]
	v_mfma_i32_16x16x64_i8 v[40:43], v[154:157], v[192:195], v[40:43]
	v_mfma_i32_16x16x64_i8 v[28:31], v[132:135], v[200:203], v[28:31]
	v_mfma_i32_16x16x64_i8 v[24:27], v[154:157], v[200:203], v[24:27]
	v_mfma_i32_16x16x64_i8 v[12:15], v[132:135], v[208:211], v[12:15]
	v_mfma_i32_16x16x64_i8 v[8:11], v[154:157], v[208:211], v[8:11]
	v_mfma_i32_16x16x64_i8 v[52:55], v[158:161], v[174:177], v[52:55]
	v_mfma_i32_16x16x64_i8 v[48:51], v[166:169], v[174:177], v[48:51]
	v_mfma_i32_16x16x64_i8 v[36:39], v[158:161], v[188:191], v[36:39]
	v_mfma_i32_16x16x64_i8 v[32:35], v[166:169], v[188:191], v[32:35]
	v_mfma_i32_16x16x64_i8 v[20:23], v[158:161], v[196:199], v[20:23]
	v_mfma_i32_16x16x64_i8 v[16:19], v[166:169], v[196:199], v[16:19]
	v_mfma_i32_16x16x64_i8 v[4:7], v[158:161], v[204:207], v[4:7]
	v_mfma_i32_16x16x64_i8 v[0:3], v[166:169], v[204:207], v[0:3]
	v_mfma_i32_16x16x64_i8 v[52:55], v[162:165], v[184:187], v[52:55]
	v_mfma_i32_16x16x64_i8 v[48:51], v[170:173], v[184:187], v[48:51]
	v_mfma_i32_16x16x64_i8 v[36:39], v[162:165], v[192:195], v[36:39]
	v_mfma_i32_16x16x64_i8 v[32:35], v[170:173], v[192:195], v[32:35]
	v_mfma_i32_16x16x64_i8 v[20:23], v[162:165], v[200:203], v[20:23]
	v_mfma_i32_16x16x64_i8 v[16:19], v[170:173], v[200:203], v[16:19]
	v_mfma_i32_16x16x64_i8 v[4:7], v[162:165], v[208:211], v[4:7]
	v_mfma_i32_16x16x64_i8 v[0:3], v[170:173], v[208:211], v[0:3]
	s_barrier
	s_add_i32 s79, s79, 2
	s_add_u32 s48, s48, 0x100
	s_addc_u32 s49, s49, 0
	s_add_u32 s75, s75, 0x100
	s_addc_u32 s78, s78, 0
	s_cmp_gt_u32 s79, 5
	s_cbranch_scc0 .LBB0_242
	s_and_b64 vcc, exec, s[16:17]
	s_cbranch_vccz .LBB0_245
	s_barrier

; #define PG8_LDA(dst, b, h) do { _Pragma("unroll") for (int m = 0; m < 4; ++m) _Pragma("unroll") for (int k = 0; k < 2; ++k) dst[m][k] = *(const PG8_LAS bf16x8*)(lds + PG8_SA(b, h) + aoff + m * 2048 + k * 1024); } while (0)
; #define PG8_LDB(dst, b, h) do { _Pragma("unroll") for (int n = 0; n < 2; ++n) _Pragma("unroll") for (int k = 0; k < 2; ++k) dst[n][k] = *(const PG8_LAS bf16x8*)(lds + PG8_SB(b, h) + boff + n * 2048 + k * 1024); } while (0)
; #define PG8_WAIT_V(n) asm volatile("s_waitcnt vmcnt(" #n ")" ::: "memory")
; #define PG8_WAIT_L(n) asm volatile("s_waitcnt lgkmcnt(" #n ")" ::: "memory")
; #define PG8_BAR __builtin_amdgcn_s_barrier()
; #define PG8_SCHED __builtin_amdgcn_sched_barrier(0)
; template <class Epi, class Sched, bool ALIGN_EPI = false, bool SP2 = false, bool F8 = false, bool I8 = false, bool PF = false>
; __device__ __forceinline__ void gemm_phase(PG8_LAS unsigned char* lds, const Gemm g, const Sched& S, const Epi& E, const int wave_) {
;     ...
;             PG8_LDB(B0, 0, 0); PG8_LDB(B1, 0, 1); PG8_SCHED; PG8_LDA(At, 0, 0); PG8_STAGE(PG8_SA(1, 1), a1 + hstep, voffA);
;             PG8_WAIT_V(8); PG8_WAIT_L(0); PG8_BAR; PG8_MMA(0, 0, At, B0); PG8_MMA(0, 1, At, B1); PG8_BAR; PG8_SCHED;
;             PG8_LDA(At, 0, 1); PG8_STAGE(PG8_SB(0, 0), b2, voffB); PG8_STAGE(PG8_SB(0, 1), b2 + hstep, voffB); PG8_STAGE(PG8_SA(0, 0), a2, voffA);
;             PG8_WAIT_V(8); PG8_WAIT_L(0); PG8_BAR; PG8_MMA(1, 0, At, B0); PG8_MMA(1, 1, At, B1); PG8_BAR; PG8_SCHED;
.LBB0_453:
	ds_read_b128 v[128:131], v175
	ds_read_b128 v[132:135], v175 offset:1024
	ds_read_b128 v[136:139], v175 offset:2048
	ds_read_b128 v[140:143], v175 offset:3072
	ds_read_b128 v[144:147], v176
	ds_read_b128 v[148:151], v176 offset:1024
	ds_read_b128 v[166:169], v176 offset:2048
	ds_read_b128 v[170:173], v176 offset:3072
	s_add_u32 s28, s22, 0xfffc0080
	s_addc_u32 s29, s23, -1
	s_cmp_eq_u32 s62, 12
	s_cselect_b32 s31, s13, s29
	s_cselect_b32 s30, s52, s28
	s_cselect_b32 s29, s11, s55
	s_cselect_b32 s28, s53, s54
	v_lshl_add_u64 v[210:211], s[22:23], 0, v[160:161]
	s_add_i32 m0, s21, 0xc000
	ds_read_b128 v[178:181], v177
	ds_read_b128 v[182:185], v177 offset:1024
	ds_read_b128 v[186:189], v177 offset:2048
	ds_read_b128 v[190:193], v177 offset:3072
	ds_read_b128 v[194:197], v177 offset:4096
	ds_read_b128 v[198:201], v177 offset:5120
	ds_read_b128 v[202:205], v177 offset:6144
	ds_read_b128 v[206:209], v177 offset:7168
	global_load_lds_dwordx4 v[210:211], off
	v_lshl_add_u64 v[210:211], s[22:23], 0, v[162:163]
	s_add_i32 m0, s21, 0xe000
	s_nop 0
	global_load_lds_dwordx4 v[210:211], off
	s_waitcnt vmcnt(8)
	s_waitcnt lgkmcnt(0)
	s_barrier
	s_waitcnt lgkmcnt(0)
	v_mfma_f32_16x16x32_bf16 v[124:127], v[128:131], v[178:181], v[124:127]
	v_mfma_f32_16x16x32_bf16 v[120:123], v[136:139], v[178:181], v[120:123]
	v_mfma_f32_16x16x32_bf16 v[116:119], v[128:131], v[186:189], v[116:119]
	v_mfma_f32_16x16x32_bf16 v[112:115], v[136:139], v[186:189], v[112:115]
	v_mfma_f32_16x16x32_bf16 v[96:99], v[128:131], v[194:197], v[96:99]
	v_mfma_f32_16x16x32_bf16 v[88:91], v[136:139], v[194:197], v[88:91]
	v_mfma_f32_16x16x32_bf16 v[80:83], v[128:131], v[202:205], v[80:83]
	v_mfma_f32_16x16x32_bf16 v[72:75], v[136:139], v[202:205], v[72:75]
	v_mfma_f32_16x16x32_bf16 v[124:127], v[132:135], v[182:185], v[124:127]
	v_mfma_f32_16x16x32_bf16 v[120:123], v[140:143], v[182:185], v[120:123]
	v_mfma_f32_16x16x32_bf16 v[116:119], v[132:135], v[190:193], v[116:119]
	v_mfma_f32_16x16x32_bf16 v[112:115], v[140:143], v[190:193], v[112:115]
	v_mfma_f32_16x16x32_bf16 v[96:99], v[132:135], v[198:201], v[96:99]
	v_mfma_f32_16x16x32_bf16 v[88:91], v[140:143], v[198:201], v[88:91]
	v_mfma_f32_16x16x32_bf16 v[80:83], v[132:135], v[206:209], v[80:83]
	v_mfma_f32_16x16x32_bf16 v[72:75], v[140:143], v[206:209], v[72:75]
	v_mfma_f32_16x16x32_bf16 v[108:111], v[144:147], v[178:181], v[108:111]
	v_mfma_f32_16x16x32_bf16 v[104:107], v[166:169], v[178:181], v[104:107]
	v_mfma_f32_16x16x32_bf16 v[100:103], v[144:147], v[186:189], v[100:103]
	v_mfma_f32_16x16x32_bf16 v[92:95], v[166:169], v[186:189], v[92:95]
	v_mfma_f32_16x16x32_bf16 v[84:87], v[144:147], v[194:197], v[84:87]
	v_mfma_f32_16x16x32_bf16 v[76:79], v[166:169], v[194:197], v[76:79]
	v_mfma_f32_16x16x32_bf16 v[68:71], v[144:147], v[202:205], v[68:71]
	v_mfma_f32_16x16x32_bf16 v[64:67], v[166:169], v[202:205], v[64:67]
	v_mfma_f32_16x16x32_bf16 v[108:111], v[148:151], v[182:185], v[108:111]
	v_mfma_f32_16x16x32_bf16 v[104:107], v[170:173], v[182:185], v[104:107]
	v_mfma_f32_16x16x32_bf16 v[100:103], v[148:151], v[190:193], v[100:103]
	v_mfma_f32_16x16x32_bf16 v[92:95], v[170:173], v[190:193], v[92:95]
	v_mfma_f32_16x16x32_bf16 v[84:87], v[148:151], v[198:201], v[84:87]
	v_mfma_f32_16x16x32_bf16 v[76:79], v[170:173], v[198:201], v[76:79]
	v_mfma_f32_16x16x32_bf16 v[68:71], v[148:151], v[206:209], v[68:71]
	v_mfma_f32_16x16x32_bf16 v[64:67], v[170:173], v[206:209], v[64:67]
	s_barrier
	s_add_i32 s63, s49, s36
	v_lshl_add_u64 v[210:211], s[28:29], 0, v[156:157]
	s_mov_b32 m0, s63
	ds_read_b128 v[178:181], v177 offset:16384
	ds_read_b128 v[182:185], v177 offset:17408
	ds_read_b128 v[186:189], v177 offset:18432
	ds_read_b128 v[190:193], v177 offset:19456
	ds_read_b128 v[194:197], v177 offset:20480
	ds_read_b128 v[198:201], v177 offset:21504
	ds_read_b128 v[202:205], v177 offset:22528
	ds_read_b128 v[206:209], v177 offset:23552
	global_load_lds_dwordx4 v[210:211], off
	s_add_i32 m0, s63, 0x2000
	s_add_u32 s64, s28, 0x40000
	v_lshl_add_u64 v[212:213], s[28:29], 0, v[152:153]
	s_addc_u32 s65, s29, 0
	s_add_i32 s63, s50, s36
	global_load_lds_dwordx4 v[212:213], off
	v_lshl_add_u64 v[214:215], s[64:65], 0, v[156:157]
	s_mov_b32 m0, s63
	v_lshl_add_u64 v[216:217], s[30:31], 0, v[154:155]
	global_load_lds_dwordx4 v[214:215], off
	v_lshl_add_u64 v[214:215], s[64:65], 0, v[152:153]
	s_add_i32 m0, s63, 0x2000
	s_nop 0
	global_load_lds_dwordx4 v[214:215], off
	v_lshl_add_u64 v[214:215], s[30:31], 0, v[158:159]
	s_mov_b32 m0, s21
	s_nop 0
	global_load_lds_dwordx4 v[214:215], off
	s_mov_b32 m0, s37
	s_nop 0
	global_load_lds_dwordx4 v[216:217], off
	s_waitcnt vmcnt(8)
	s_waitcnt lgkmcnt(0)
	s_barrier
; #define PG8_LDA(dst, b, h) do { _Pragma("unroll") for (int m = 0; m < 4; ++m) _Pragma("unroll") for (int k = 0; k < 2; ++k) dst[m][k] = *(const PG8_LAS bf16x8*)(lds + PG8_SA(b, h) + aoff + m * 2048 + k * 1024); } while (0)
; #define PG8_LDB(dst, b, h) do { _Pragma("unroll") for (int n = 0; n < 2; ++n) _Pragma("unroll") for (int k = 0; k < 2; ++k) dst[n][k] = *(const PG8_LAS bf16x8*)(lds + PG8_SB(b, h) + boff + n * 2048 + k * 1024); } while (0)
; #define PG8_WAIT_V(n) asm volatile("s_waitcnt vmcnt(" #n ")" ::: "memory")
; #define PG8_WAIT_L(n) asm volatile("s_waitcnt lgkmcnt(" #n ")" ::: "memory")
; #define PG8_BAR __builtin_amdgcn_s_barrier()
; #define PG8_SCHED __builtin_amdgcn_sched_barrier(0)
; template <class Epi, class Sched, bool ALIGN_EPI = false, bool SP2 = false, bool F8 = false, bool I8 = false, bool PF = false>
; __device__ __forceinline__ void gemm_phase(PG8_LAS unsigned char* lds, const Gemm g, const Sched& S, const Epi& E, const int wave_) {
;     ...
;             PG8_WAIT_V(8); PG8_WAIT_L(0); PG8_BAR; PG8_MMA(1, 0, At, B0); PG8_MMA(1, 1, At, B1); PG8_BAR; PG8_SCHED;
;             PG8_LDB(B0, 1, 0); PG8_LDB(B1, 1, 1); PG8_SCHED; PG8_LDA(At, 1, 0); PG8_STAGE(PG8_SA(0, 1), a2 + hstep, voffA);
;             PG8_WAIT_V(8); PG8_WAIT_L(0); PG8_BAR; PG8_MMA(0, 0, At, B0); PG8_MMA(0, 1, At, B1); PG8_BAR; PG8_SCHED;
	s_waitcnt lgkmcnt(0)
	v_mfma_f32_16x16x32_bf16 v[60:63], v[128:131], v[178:181], v[60:63]
	v_mfma_f32_16x16x32_bf16 v[56:59], v[136:139], v[178:181], v[56:59]
	v_mfma_f32_16x16x32_bf16 v[48:51], v[128:131], v[186:189], v[48:51]
	v_mfma_f32_16x16x32_bf16 v[40:43], v[136:139], v[186:189], v[40:43]
	v_mfma_f32_16x16x32_bf16 v[32:35], v[128:131], v[194:197], v[32:35]
	v_mfma_f32_16x16x32_bf16 v[24:27], v[136:139], v[194:197], v[24:27]
	v_mfma_f32_16x16x32_bf16 v[16:19], v[128:131], v[202:205], v[16:19]
	v_mfma_f32_16x16x32_bf16 v[8:11], v[136:139], v[202:205], v[8:11]
	v_mfma_f32_16x16x32_bf16 v[60:63], v[132:135], v[182:185], v[60:63]
	v_mfma_f32_16x16x32_bf16 v[56:59], v[140:143], v[182:185], v[56:59]
	v_mfma_f32_16x16x32_bf16 v[48:51], v[132:135], v[190:193], v[48:51]
	v_mfma_f32_16x16x32_bf16 v[40:43], v[140:143], v[190:193], v[40:43]
	v_mfma_f32_16x16x32_bf16 v[32:35], v[132:135], v[198:201], v[32:35]
	v_mfma_f32_16x16x32_bf16 v[24:27], v[140:143], v[198:201], v[24:27]
	v_mfma_f32_16x16x32_bf16 v[16:19], v[132:135], v[206:209], v[16:19]
	v_mfma_f32_16x16x32_bf16 v[8:11], v[140:143], v[206:209], v[8:11]
	v_mfma_f32_16x16x32_bf16 v[52:55], v[144:147], v[178:181], v[52:55]
	v_mfma_f32_16x16x32_bf16 v[44:47], v[166:169], v[178:181], v[44:47]
	v_mfma_f32_16x16x32_bf16 v[36:39], v[144:147], v[186:189], v[36:39]
	v_mfma_f32_16x16x32_bf16 v[28:31], v[166:169], v[186:189], v[28:31]
	v_mfma_f32_16x16x32_bf16 v[20:23], v[144:147], v[194:197], v[20:23]
	v_mfma_f32_16x16x32_bf16 v[12:15], v[166:169], v[194:197], v[12:15]
	v_mfma_f32_16x16x32_bf16 v[4:7], v[144:147], v[202:205], v[4:7]
	v_mfma_f32_16x16x32_bf16 v[0:3], v[166:169], v[202:205], v[0:3]
	v_mfma_f32_16x16x32_bf16 v[52:55], v[148:151], v[182:185], v[52:55]
	v_mfma_f32_16x16x32_bf16 v[44:47], v[170:173], v[182:185], v[44:47]
	v_mfma_f32_16x16x32_bf16 v[36:39], v[148:151], v[190:193], v[36:39]
	v_mfma_f32_16x16x32_bf16 v[28:31], v[170:173], v[190:193], v[28:31]
	v_mfma_f32_16x16x32_bf16 v[20:23], v[148:151], v[198:201], v[20:23]
	v_mfma_f32_16x16x32_bf16 v[12:15], v[170:173], v[198:201], v[12:15]
	v_mfma_f32_16x16x32_bf16 v[4:7], v[148:151], v[206:209], v[4:7]
	v_mfma_f32_16x16x32_bf16 v[0:3], v[170:173], v[206:209], v[0:3]
	s_barrier
	s_add_i32 s63, 0, 0x18000
	s_add_i32 s64, 0, 0x1c000
	v_add_u32_e32 v140, s63, v174
	v_add_u32_e32 v170, s64, v174
	ds_read_b128 v[128:131], v140
	ds_read_b128 v[132:135], v140 offset:1024
	ds_read_b128 v[136:139], v140 offset:2048
	ds_read_b128 v[140:143], v140 offset:3072
	ds_read_b128 v[144:147], v170
	ds_read_b128 v[148:151], v170 offset:1024
	ds_read_b128 v[166:169], v170 offset:2048
	ds_read_b128 v[170:173], v170 offset:3072
	s_add_u32 s30, s30, 0x40000
	s_addc_u32 s31, s31, 0
	s_mov_b32 m0, s38
	v_lshl_add_u64 v[218:219], s[30:31], 0, v[158:159]
	ds_read_b128 v[178:181], v177 offset:32768
	ds_read_b128 v[182:185], v177 offset:33792
	ds_read_b128 v[186:189], v177 offset:34816
	ds_read_b128 v[190:193], v177 offset:35840
	ds_read_b128 v[194:197], v177 offset:36864
	ds_read_b128 v[198:201], v177 offset:37888
	ds_read_b128 v[202:205], v177 offset:38912
	ds_read_b128 v[206:209], v177 offset:39936
	global_load_lds_dwordx4 v[218:219], off
	v_lshl_add_u64 v[218:219], s[30:31], 0, v[154:155]
	s_mov_b32 m0, s39
	s_nop 0
	global_load_lds_dwordx4 v[218:219], off
	s_waitcnt vmcnt(8)
	s_waitcnt lgkmcnt(0)
	s_barrier
	s_waitcnt lgkmcnt(0)
	v_mfma_f32_16x16x32_bf16 v[124:127], v[128:131], v[178:181], v[124:127]
	v_mfma_f32_16x16x32_bf16 v[120:123], v[136:139], v[178:181], v[120:123]
	v_mfma_f32_16x16x32_bf16 v[116:119], v[128:131], v[186:189], v[116:119]
	v_mfma_f32_16x16x32_bf16 v[112:115], v[136:139], v[186:189], v[112:115]
	v_mfma_f32_16x16x32_bf16 v[96:99], v[128:131], v[194:197], v[96:99]
	v_mfma_f32_16x16x32_bf16 v[88:91], v[136:139], v[194:197], v[88:91]
	v_mfma_f32_16x16x32_bf16 v[80:83], v[128:131], v[202:205], v[80:83]
	v_mfma_f32_16x16x32_bf16 v[72:75], v[136:139], v[202:205], v[72:75]
	v_mfma_f32_16x16x32_bf16 v[124:127], v[132:135], v[182:185], v[124:127]
	v_mfma_f32_16x16x32_bf16 v[120:123], v[140:143], v[182:185], v[120:123]
	v_mfma_f32_16x16x32_bf16 v[116:119], v[132:135], v[190:193], v[116:119]
	v_mfma_f32_16x16x32_bf16 v[112:115], v[140:143], v[190:193], v[112:115]
	v_mfma_f32_16x16x32_bf16 v[96:99], v[132:135], v[198:201], v[96:99]
	v_mfma_f32_16x16x32_bf16 v[88:91], v[140:143], v[198:201], v[88:91]
	v_mfma_f32_16x16x32_bf16 v[80:83], v[132:135], v[206:209], v[80:83]
	v_mfma_f32_16x16x32_bf16 v[72:75], v[140:143], v[206:209], v[72:75]
	v_mfma_f32_16x16x32_bf16 v[108:111], v[144:147], v[178:181], v[108:111]
	v_mfma_f32_16x16x32_bf16 v[104:107], v[166:169], v[178:181], v[104:107]
	v_mfma_f32_16x16x32_bf16 v[100:103], v[144:147], v[186:189], v[100:103]
	v_mfma_f32_16x16x32_bf16 v[92:95], v[166:169], v[186:189], v[92:95]
	v_mfma_f32_16x16x32_bf16 v[84:87], v[144:147], v[194:197], v[84:87]
	v_mfma_f32_16x16x32_bf16 v[76:79], v[166:169], v[194:197], v[76:79]
	v_mfma_f32_16x16x32_bf16 v[68:71], v[144:147], v[202:205], v[68:71]
	v_mfma_f32_16x16x32_bf16 v[64:67], v[166:169], v[202:205], v[64:67]
	v_mfma_f32_16x16x32_bf16 v[108:111], v[148:151], v[182:185], v[108:111]
	v_mfma_f32_16x16x32_bf16 v[104:107], v[170:173], v[182:185], v[104:107]
	v_mfma_f32_16x16x32_bf16 v[100:103], v[148:151], v[190:193], v[100:103]
	v_mfma_f32_16x16x32_bf16 v[92:95], v[170:173], v[190:193], v[92:95]
	v_mfma_f32_16x16x32_bf16 v[84:87], v[148:151], v[198:201], v[84:87]
	v_mfma_f32_16x16x32_bf16 v[76:79], v[170:173], v[198:201], v[76:79]
	v_mfma_f32_16x16x32_bf16 v[68:71], v[148:151], v[206:209], v[68:71]
	v_mfma_f32_16x16x32_bf16 v[64:67], v[170:173], v[206:209], v[64:67]
	s_barrier
; #define PG8_LDA(dst, b, h) do { _Pragma("unroll") for (int m = 0; m < 4; ++m) _Pragma("unroll") for (int k = 0; k < 2; ++k) dst[m][k] = *(const PG8_LAS bf16x8*)(lds + PG8_SA(b, h) + aoff + m * 2048 + k * 1024); } while (0)
; #define PG8_WAIT_V(n) asm volatile("s_waitcnt vmcnt(" #n ")" ::: "memory")
; #define PG8_WAIT_L(n) asm volatile("s_waitcnt lgkmcnt(" #n ")" ::: "memory")
; #define PG8_BAR __builtin_amdgcn_s_barrier()
; #define PG8_SCHED __builtin_amdgcn_sched_barrier(0)
; template <class Epi, class Sched, bool ALIGN_EPI = false, bool SP2 = false, bool F8 = false, bool I8 = false, bool PF = false>
; __device__ __forceinline__ void gemm_phase(PG8_LAS unsigned char* lds, const Gemm g, const Sched& S, const Epi& E, const int wave_) {
;     ...
;             PG8_LDA(At, 1, 1); PG8_STAGE(PG8_SB(1, 0), b3, voffB); PG8_STAGE(PG8_SB(1, 1), b3 + hstep, voffB); PG8_STAGE(PG8_SA(1, 0), a3, voffA);
;             PG8_WAIT_V(8); PG8_WAIT_L(0); PG8_BAR; PG8_MMA(1, 0, At, B0); PG8_MMA(1, 1, At, B1); PG8_BAR; PG8_SCHED;
	s_add_i32 s30, s63, s36
	v_lshl_add_u64 v[210:211], v[210:211], 0, s[6:7]
	s_mov_b32 m0, s30
	ds_read_b128 v[178:181], v177 offset:49152
	ds_read_b128 v[182:185], v177 offset:50176
	ds_read_b128 v[186:189], v177 offset:51200
	ds_read_b128 v[190:193], v177 offset:52224
	ds_read_b128 v[194:197], v177 offset:53248
	ds_read_b128 v[198:201], v177 offset:54272
	ds_read_b128 v[202:205], v177 offset:55296
	ds_read_b128 v[206:209], v177 offset:56320
	global_load_lds_dwordx4 v[210:211], off
	s_add_i32 m0, s30, 0x2000
	s_add_u32 s28, s28, 0x40080
	v_lshl_add_u64 v[210:211], v[212:213], 0, s[6:7]
	s_addc_u32 s29, s29, 0
	s_add_i32 s30, s64, s36
	global_load_lds_dwordx4 v[210:211], off
	v_lshl_add_u64 v[210:211], s[28:29], 0, v[156:157]
	s_mov_b32 m0, s30
	s_nop 0
	global_load_lds_dwordx4 v[210:211], off
	v_lshl_add_u64 v[210:211], s[28:29], 0, v[152:153]
	s_add_i32 m0, s30, 0x2000
	s_nop 0
	global_load_lds_dwordx4 v[210:211], off
	v_lshl_add_u64 v[210:211], v[214:215], 0, s[6:7]
	s_mov_b32 m0, s46
	s_nop 0
	global_load_lds_dwordx4 v[210:211], off
	v_lshl_add_u64 v[210:211], v[216:217], 0, s[6:7]
	s_mov_b32 m0, s47
	s_nop 0
	global_load_lds_dwordx4 v[210:211], off
	s_waitcnt vmcnt(8)
	s_waitcnt lgkmcnt(0)
	s_barrier
	s_waitcnt lgkmcnt(0)
	v_mfma_f32_16x16x32_bf16 v[60:63], v[128:131], v[178:181], v[60:63]
	v_mfma_f32_16x16x32_bf16 v[56:59], v[136:139], v[178:181], v[56:59]
	v_mfma_f32_16x16x32_bf16 v[48:51], v[128:131], v[186:189], v[48:51]
	v_mfma_f32_16x16x32_bf16 v[40:43], v[136:139], v[186:189], v[40:43]
	v_mfma_f32_16x16x32_bf16 v[32:35], v[128:131], v[194:197], v[32:35]
	v_mfma_f32_16x16x32_bf16 v[24:27], v[136:139], v[194:197], v[24:27]
	v_mfma_f32_16x16x32_bf16 v[16:19], v[128:131], v[202:205], v[16:19]
	v_mfma_f32_16x16x32_bf16 v[8:11], v[136:139], v[202:205], v[8:11]
	v_mfma_f32_16x16x32_bf16 v[60:63], v[132:135], v[182:185], v[60:63]
	v_mfma_f32_16x16x32_bf16 v[56:59], v[140:143], v[182:185], v[56:59]
	v_mfma_f32_16x16x32_bf16 v[48:51], v[132:135], v[190:193], v[48:51]
	v_mfma_f32_16x16x32_bf16 v[40:43], v[140:143], v[190:193], v[40:43]
	v_mfma_f32_16x16x32_bf16 v[32:35], v[132:135], v[198:201], v[32:35]
	v_mfma_f32_16x16x32_bf16 v[24:27], v[140:143], v[198:201], v[24:27]
	v_mfma_f32_16x16x32_bf16 v[16:19], v[132:135], v[206:209], v[16:19]
	v_mfma_f32_16x16x32_bf16 v[8:11], v[140:143], v[206:209], v[8:11]
	v_mfma_f32_16x16x32_bf16 v[52:55], v[144:147], v[178:181], v[52:55]
	v_mfma_f32_16x16x32_bf16 v[44:47], v[166:169], v[178:181], v[44:47]
	v_mfma_f32_16x16x32_bf16 v[36:39], v[144:147], v[186:189], v[36:39]
	v_mfma_f32_16x16x32_bf16 v[28:31], v[166:169], v[186:189], v[28:31]
	v_mfma_f32_16x16x32_bf16 v[20:23], v[144:147], v[194:197], v[20:23]
	v_mfma_f32_16x16x32_bf16 v[12:15], v[166:169], v[194:197], v[12:15]
	v_mfma_f32_16x16x32_bf16 v[4:7], v[144:147], v[202:205], v[4:7]
	v_mfma_f32_16x16x32_bf16 v[0:3], v[166:169], v[202:205], v[0:3]
	v_mfma_f32_16x16x32_bf16 v[52:55], v[148:151], v[182:185], v[52:55]
	v_mfma_f32_16x16x32_bf16 v[44:47], v[170:173], v[182:185], v[44:47]
	v_mfma_f32_16x16x32_bf16 v[36:39], v[148:151], v[190:193], v[36:39]
	v_mfma_f32_16x16x32_bf16 v[28:31], v[170:173], v[190:193], v[28:31]
	v_mfma_f32_16x16x32_bf16 v[20:23], v[148:151], v[198:201], v[20:23]
	v_mfma_f32_16x16x32_bf16 v[12:15], v[170:173], v[198:201], v[12:15]
	v_mfma_f32_16x16x32_bf16 v[4:7], v[148:151], v[206:209], v[4:7]
	v_mfma_f32_16x16x32_bf16 v[0:3], v[170:173], v[206:209], v[0:3]
	s_barrier
	s_add_i32 s62, s62, 2
	s_add_u32 s22, s22, 0x100
	s_addc_u32 s23, s23, 0
	s_add_u32 s54, s54, 0x100
	s_addc_u32 s55, s55, 0
	s_cmp_gt_u32 s62, 13
	s_cbranch_scc0 .LBB0_453
	s_and_b64 vcc, exec, s[8:9]
	s_cbranch_vccz .LBB0_456
	s_barrier

; #define PG8_LDA(dst, b, h) do { _Pragma("unroll") for (int m = 0; m < 4; ++m) _Pragma("unroll") for (int k = 0; k < 2; ++k) dst[m][k] = *(const PG8_LAS bf16x8*)(lds + PG8_SA(b, h) + aoff + m * 2048 + k * 1024); } while (0)
; #define PG8_LDB(dst, b, h) do { _Pragma("unroll") for (int n = 0; n < 2; ++n) _Pragma("unroll") for (int k = 0; k < 2; ++k) dst[n][k] = *(const PG8_LAS bf16x8*)(lds + PG8_SB(b, h) + boff + n * 2048 + k * 1024); } while (0)
; #define PG8_WAIT_V(n) asm volatile("s_waitcnt vmcnt(" #n ")" ::: "memory")
; #define PG8_WAIT_L(n) asm volatile("s_waitcnt lgkmcnt(" #n ")" ::: "memory")
; #define PG8_BAR __builtin_amdgcn_s_barrier()
; #define PG8_SCHED __builtin_amdgcn_sched_barrier(0)
; template <class Epi, class Sched, bool ALIGN_EPI = false, bool SP2 = false, bool F8 = false, bool I8 = false, bool PF = false>
; __device__ __forceinline__ void gemm_phase(PG8_LAS unsigned char* lds, const Gemm g, const Sched& S, const Epi& E, const int wave_) {
;     ...
;             PG8_LDB(B0, 0, 0); PG8_LDB(B1, 0, 1); PG8_SCHED; PG8_LDA(At, 0, 0); PG8_STAGE(PG8_SA(1, 1), a1 + hstep, voffA);
;             PG8_WAIT_V(8); PG8_WAIT_L(0); PG8_BAR; PG8_MMA(0, 0, At, B0); PG8_MMA(0, 1, At, B1); PG8_BAR; PG8_SCHED;
;             PG8_LDA(At, 0, 1); PG8_STAGE(PG8_SB(0, 0), b2, voffB); PG8_STAGE(PG8_SB(0, 1), b2 + hstep, voffB); PG8_STAGE(PG8_SA(0, 0), a2, voffA);
;             PG8_WAIT_V(8); PG8_WAIT_L(0); PG8_BAR; PG8_MMA(1, 0, At, B0); PG8_MMA(1, 1, At, B1); PG8_BAR; PG8_SCHED;
.LBB0_591:
	ds_read_b128 v[142:145], v153
	ds_read_b128 v[146:149], v153 offset:1024
	ds_read_b128 v[158:161], v153 offset:2048
	ds_read_b128 v[162:165], v153 offset:3072
	ds_read_b128 v[166:169], v154
	ds_read_b128 v[170:173], v154 offset:1024
	ds_read_b128 v[174:177], v154 offset:2048
	ds_read_b128 v[178:181], v154 offset:3072
	s_add_u32 s34, s30, 0xfffe0080
	s_addc_u32 s35, s31, -1
	s_cmp_eq_u32 s64, 4
	s_cselect_b32 s37, s19, s35
	s_cselect_b32 s36, s56, s34
	s_cselect_b32 s35, s17, s63
	s_cselect_b32 s34, s57, s62
	v_lshl_add_u64 v[150:151], s[30:31], 0, v[136:137]
	s_add_i32 m0, s29, 0xc000
	ds_read_b128 v[182:185], v155
	ds_read_b128 v[186:189], v155 offset:1024
	ds_read_b128 v[190:193], v155 offset:2048
	ds_read_b128 v[194:197], v155 offset:3072
	ds_read_b128 v[198:201], v155 offset:4096
	ds_read_b128 v[202:205], v155 offset:5120
	ds_read_b128 v[206:209], v155 offset:6144
	ds_read_b128 v[210:213], v155 offset:7168
	global_load_lds_dwordx4 v[150:151], off
	v_lshl_add_u64 v[150:151], s[30:31], 0, v[138:139]
	s_add_i32 m0, s29, 0xe000
	s_nop 0
	global_load_lds_dwordx4 v[150:151], off
	s_waitcnt vmcnt(8)
	s_waitcnt lgkmcnt(0)
	s_barrier
	s_waitcnt lgkmcnt(0)
	v_mfma_i32_16x16x64_i8 v[124:127], v[142:145], v[182:185], v[124:127]
	v_mfma_i32_16x16x64_i8 v[120:123], v[158:161], v[182:185], v[120:123]
	v_mfma_i32_16x16x64_i8 v[108:111], v[142:145], v[190:193], v[108:111]
	v_mfma_i32_16x16x64_i8 v[104:107], v[158:161], v[190:193], v[104:107]
	v_mfma_i32_16x16x64_i8 v[92:95], v[142:145], v[198:201], v[92:95]
	v_mfma_i32_16x16x64_i8 v[88:91], v[158:161], v[198:201], v[88:91]
	v_mfma_i32_16x16x64_i8 v[76:79], v[142:145], v[206:209], v[76:79]
	v_mfma_i32_16x16x64_i8 v[72:75], v[158:161], v[206:209], v[72:75]
	v_mfma_i32_16x16x64_i8 v[124:127], v[146:149], v[186:189], v[124:127]
	v_mfma_i32_16x16x64_i8 v[120:123], v[162:165], v[186:189], v[120:123]
	v_mfma_i32_16x16x64_i8 v[108:111], v[146:149], v[194:197], v[108:111]
	v_mfma_i32_16x16x64_i8 v[104:107], v[162:165], v[194:197], v[104:107]
	v_mfma_i32_16x16x64_i8 v[92:95], v[146:149], v[202:205], v[92:95]
	v_mfma_i32_16x16x64_i8 v[88:91], v[162:165], v[202:205], v[88:91]
	v_mfma_i32_16x16x64_i8 v[76:79], v[146:149], v[210:213], v[76:79]
	v_mfma_i32_16x16x64_i8 v[72:75], v[162:165], v[210:213], v[72:75]
	v_mfma_i32_16x16x64_i8 v[116:119], v[166:169], v[182:185], v[116:119]
	v_mfma_i32_16x16x64_i8 v[112:115], v[174:177], v[182:185], v[112:115]
	v_mfma_i32_16x16x64_i8 v[100:103], v[166:169], v[190:193], v[100:103]
	v_mfma_i32_16x16x64_i8 v[96:99], v[174:177], v[190:193], v[96:99]
	v_mfma_i32_16x16x64_i8 v[84:87], v[166:169], v[198:201], v[84:87]
	v_mfma_i32_16x16x64_i8 v[80:83], v[174:177], v[198:201], v[80:83]
	v_mfma_i32_16x16x64_i8 v[68:71], v[166:169], v[206:209], v[68:71]
	v_mfma_i32_16x16x64_i8 v[64:67], v[174:177], v[206:209], v[64:67]
	v_mfma_i32_16x16x64_i8 v[116:119], v[170:173], v[186:189], v[116:119]
	v_mfma_i32_16x16x64_i8 v[112:115], v[178:181], v[186:189], v[112:115]
	v_mfma_i32_16x16x64_i8 v[100:103], v[170:173], v[194:197], v[100:103]
	v_mfma_i32_16x16x64_i8 v[96:99], v[178:181], v[194:197], v[96:99]
	v_mfma_i32_16x16x64_i8 v[84:87], v[170:173], v[202:205], v[84:87]
	v_mfma_i32_16x16x64_i8 v[80:83], v[178:181], v[202:205], v[80:83]
	v_mfma_i32_16x16x64_i8 v[68:71], v[170:173], v[210:213], v[68:71]
	v_mfma_i32_16x16x64_i8 v[64:67], v[178:181], v[210:213], v[64:67]
	s_barrier
	s_add_i32 s65, s51, s39
	v_lshl_add_u64 v[150:151], s[34:35], 0, v[132:133]
	s_mov_b32 m0, s65
	ds_read_b128 v[182:185], v155 offset:16384
	ds_read_b128 v[186:189], v155 offset:17408
	ds_read_b128 v[190:193], v155 offset:18432
	ds_read_b128 v[194:197], v155 offset:19456
	ds_read_b128 v[198:201], v155 offset:20480
	ds_read_b128 v[202:205], v155 offset:21504
	ds_read_b128 v[206:209], v155 offset:22528
	ds_read_b128 v[210:213], v155 offset:23552
	global_load_lds_dwordx4 v[150:151], off
	s_add_i32 m0, s65, 0x2000
	s_add_u32 s66, s34, 0x20000
	v_lshl_add_u64 v[214:215], s[34:35], 0, v[128:129]
	s_addc_u32 s67, s35, 0
	s_add_i32 s65, s52, s39
	global_load_lds_dwordx4 v[214:215], off
	v_lshl_add_u64 v[216:217], s[66:67], 0, v[132:133]
	s_mov_b32 m0, s65
	v_lshl_add_u64 v[218:219], s[36:37], 0, v[130:131]
	global_load_lds_dwordx4 v[216:217], off
	v_lshl_add_u64 v[216:217], s[66:67], 0, v[128:129]
	s_add_i32 m0, s65, 0x2000
	s_nop 0
	global_load_lds_dwordx4 v[216:217], off
	v_lshl_add_u64 v[216:217], s[36:37], 0, v[134:135]
	s_mov_b32 m0, s29
	s_nop 0
	global_load_lds_dwordx4 v[216:217], off
	s_mov_b32 m0, s41
	s_nop 0
	global_load_lds_dwordx4 v[218:219], off
	s_waitcnt vmcnt(8)
	s_waitcnt lgkmcnt(0)
	s_barrier
; #define PG8_LDA(dst, b, h) do { _Pragma("unroll") for (int m = 0; m < 4; ++m) _Pragma("unroll") for (int k = 0; k < 2; ++k) dst[m][k] = *(const PG8_LAS bf16x8*)(lds + PG8_SA(b, h) + aoff + m * 2048 + k * 1024); } while (0)
; #define PG8_LDB(dst, b, h) do { _Pragma("unroll") for (int n = 0; n < 2; ++n) _Pragma("unroll") for (int k = 0; k < 2; ++k) dst[n][k] = *(const PG8_LAS bf16x8*)(lds + PG8_SB(b, h) + boff + n * 2048 + k * 1024); } while (0)
; #define PG8_WAIT_V(n) asm volatile("s_waitcnt vmcnt(" #n ")" ::: "memory")
; #define PG8_WAIT_L(n) asm volatile("s_waitcnt lgkmcnt(" #n ")" ::: "memory")
; #define PG8_BAR __builtin_amdgcn_s_barrier()
; #define PG8_SCHED __builtin_amdgcn_sched_barrier(0)
; template <class Epi, class Sched, bool ALIGN_EPI = false, bool SP2 = false, bool F8 = false, bool I8 = false, bool PF = false>
; __device__ __forceinline__ void gemm_phase(PG8_LAS unsigned char* lds, const Gemm g, const Sched& S, const Epi& E, const int wave_) {
;     ...
;             PG8_WAIT_V(8); PG8_WAIT_L(0); PG8_BAR; PG8_MMA(1, 0, At, B0); PG8_MMA(1, 1, At, B1); PG8_BAR; PG8_SCHED;
;             PG8_LDB(B0, 1, 0); PG8_LDB(B1, 1, 1); PG8_SCHED; PG8_LDA(At, 1, 0); PG8_STAGE(PG8_SA(0, 1), a2 + hstep, voffA);
;             PG8_WAIT_V(8); PG8_WAIT_L(0); PG8_BAR; PG8_MMA(0, 0, At, B0); PG8_MMA(0, 1, At, B1); PG8_BAR; PG8_SCHED;
	s_waitcnt lgkmcnt(0)
	v_mfma_i32_16x16x64_i8 v[60:63], v[142:145], v[182:185], v[60:63]
	v_mfma_i32_16x16x64_i8 v[56:59], v[158:161], v[182:185], v[56:59]
	v_mfma_i32_16x16x64_i8 v[44:47], v[142:145], v[190:193], v[44:47]
	v_mfma_i32_16x16x64_i8 v[40:43], v[158:161], v[190:193], v[40:43]
	v_mfma_i32_16x16x64_i8 v[28:31], v[142:145], v[198:201], v[28:31]
	v_mfma_i32_16x16x64_i8 v[24:27], v[158:161], v[198:201], v[24:27]
	v_mfma_i32_16x16x64_i8 v[12:15], v[142:145], v[206:209], v[12:15]
	v_mfma_i32_16x16x64_i8 v[8:11], v[158:161], v[206:209], v[8:11]
	v_mfma_i32_16x16x64_i8 v[60:63], v[146:149], v[186:189], v[60:63]
	v_mfma_i32_16x16x64_i8 v[56:59], v[162:165], v[186:189], v[56:59]
	v_mfma_i32_16x16x64_i8 v[44:47], v[146:149], v[194:197], v[44:47]
	v_mfma_i32_16x16x64_i8 v[40:43], v[162:165], v[194:197], v[40:43]
	v_mfma_i32_16x16x64_i8 v[28:31], v[146:149], v[202:205], v[28:31]
	v_mfma_i32_16x16x64_i8 v[24:27], v[162:165], v[202:205], v[24:27]
	v_mfma_i32_16x16x64_i8 v[12:15], v[146:149], v[210:213], v[12:15]
	v_mfma_i32_16x16x64_i8 v[8:11], v[162:165], v[210:213], v[8:11]
	v_mfma_i32_16x16x64_i8 v[52:55], v[166:169], v[182:185], v[52:55]
	v_mfma_i32_16x16x64_i8 v[48:51], v[174:177], v[182:185], v[48:51]
	v_mfma_i32_16x16x64_i8 v[36:39], v[166:169], v[190:193], v[36:39]
	v_mfma_i32_16x16x64_i8 v[32:35], v[174:177], v[190:193], v[32:35]
	v_mfma_i32_16x16x64_i8 v[20:23], v[166:169], v[198:201], v[20:23]
	v_mfma_i32_16x16x64_i8 v[16:19], v[174:177], v[198:201], v[16:19]
	v_mfma_i32_16x16x64_i8 v[4:7], v[166:169], v[206:209], v[4:7]
	v_mfma_i32_16x16x64_i8 v[0:3], v[174:177], v[206:209], v[0:3]
	v_mfma_i32_16x16x64_i8 v[52:55], v[170:173], v[186:189], v[52:55]
	v_mfma_i32_16x16x64_i8 v[48:51], v[178:181], v[186:189], v[48:51]
	v_mfma_i32_16x16x64_i8 v[36:39], v[170:173], v[194:197], v[36:39]
	v_mfma_i32_16x16x64_i8 v[32:35], v[178:181], v[194:197], v[32:35]
	v_mfma_i32_16x16x64_i8 v[20:23], v[170:173], v[202:205], v[20:23]
	v_mfma_i32_16x16x64_i8 v[16:19], v[178:181], v[202:205], v[16:19]
	v_mfma_i32_16x16x64_i8 v[4:7], v[170:173], v[210:213], v[4:7]
	v_mfma_i32_16x16x64_i8 v[0:3], v[178:181], v[210:213], v[0:3]
	s_barrier
	s_add_i32 s65, 0, 0x18000
	v_add_u32_e32 v157, s65, v152
	s_add_i32 s66, 0, 0x1c000
	ds_read_b128 v[142:145], v157
	ds_read_b128 v[146:149], v157 offset:1024
	ds_read_b128 v[158:161], v157 offset:2048
	ds_read_b128 v[162:165], v157 offset:3072
	v_add_u32_e32 v157, s66, v152
	ds_read_b128 v[166:169], v157
	ds_read_b128 v[170:173], v157 offset:1024
	ds_read_b128 v[174:177], v157 offset:2048
	ds_read_b128 v[178:181], v157 offset:3072
	s_add_u32 s36, s36, 0x20000
	s_addc_u32 s37, s37, 0
	s_mov_b32 m0, s42
	v_lshl_add_u64 v[220:221], s[36:37], 0, v[134:135]
	ds_read_b128 v[182:185], v155 offset:32768
	ds_read_b128 v[186:189], v155 offset:33792
	ds_read_b128 v[190:193], v155 offset:34816
	ds_read_b128 v[194:197], v155 offset:35840
	ds_read_b128 v[198:201], v155 offset:36864
	ds_read_b128 v[202:205], v155 offset:37888
	ds_read_b128 v[206:209], v155 offset:38912
	ds_read_b128 v[210:213], v155 offset:39936
	global_load_lds_dwordx4 v[220:221], off
	v_lshl_add_u64 v[220:221], s[36:37], 0, v[130:131]
	s_mov_b32 m0, s43
	s_nop 0
	global_load_lds_dwordx4 v[220:221], off
	s_waitcnt vmcnt(8)
	s_waitcnt lgkmcnt(0)
	s_barrier
	s_waitcnt lgkmcnt(0)
	v_mfma_i32_16x16x64_i8 v[124:127], v[142:145], v[182:185], v[124:127]
	v_mfma_i32_16x16x64_i8 v[120:123], v[158:161], v[182:185], v[120:123]
	v_mfma_i32_16x16x64_i8 v[108:111], v[142:145], v[190:193], v[108:111]
	v_mfma_i32_16x16x64_i8 v[104:107], v[158:161], v[190:193], v[104:107]
	v_mfma_i32_16x16x64_i8 v[92:95], v[142:145], v[198:201], v[92:95]
	v_mfma_i32_16x16x64_i8 v[88:91], v[158:161], v[198:201], v[88:91]
	v_mfma_i32_16x16x64_i8 v[76:79], v[142:145], v[206:209], v[76:79]
	v_mfma_i32_16x16x64_i8 v[72:75], v[158:161], v[206:209], v[72:75]
	v_mfma_i32_16x16x64_i8 v[124:127], v[146:149], v[186:189], v[124:127]
	v_mfma_i32_16x16x64_i8 v[120:123], v[162:165], v[186:189], v[120:123]
	v_mfma_i32_16x16x64_i8 v[108:111], v[146:149], v[194:197], v[108:111]
	v_mfma_i32_16x16x64_i8 v[104:107], v[162:165], v[194:197], v[104:107]
	v_mfma_i32_16x16x64_i8 v[92:95], v[146:149], v[202:205], v[92:95]
	v_mfma_i32_16x16x64_i8 v[88:91], v[162:165], v[202:205], v[88:91]
	v_mfma_i32_16x16x64_i8 v[76:79], v[146:149], v[210:213], v[76:79]
	v_mfma_i32_16x16x64_i8 v[72:75], v[162:165], v[210:213], v[72:75]
	v_mfma_i32_16x16x64_i8 v[116:119], v[166:169], v[182:185], v[116:119]
	v_mfma_i32_16x16x64_i8 v[112:115], v[174:177], v[182:185], v[112:115]
	v_mfma_i32_16x16x64_i8 v[100:103], v[166:169], v[190:193], v[100:103]
	v_mfma_i32_16x16x64_i8 v[96:99], v[174:177], v[190:193], v[96:99]
	v_mfma_i32_16x16x64_i8 v[84:87], v[166:169], v[198:201], v[84:87]
	v_mfma_i32_16x16x64_i8 v[80:83], v[174:177], v[198:201], v[80:83]
	v_mfma_i32_16x16x64_i8 v[68:71], v[166:169], v[206:209], v[68:71]
	v_mfma_i32_16x16x64_i8 v[64:67], v[174:177], v[206:209], v[64:67]
	v_mfma_i32_16x16x64_i8 v[116:119], v[170:173], v[186:189], v[116:119]
	v_mfma_i32_16x16x64_i8 v[112:115], v[178:181], v[186:189], v[112:115]
	v_mfma_i32_16x16x64_i8 v[100:103], v[170:173], v[194:197], v[100:103]
	v_mfma_i32_16x16x64_i8 v[96:99], v[178:181], v[194:197], v[96:99]
	v_mfma_i32_16x16x64_i8 v[84:87], v[170:173], v[202:205], v[84:87]
	v_mfma_i32_16x16x64_i8 v[80:83], v[178:181], v[202:205], v[80:83]
	v_mfma_i32_16x16x64_i8 v[68:71], v[170:173], v[210:213], v[68:71]
	v_mfma_i32_16x16x64_i8 v[64:67], v[178:181], v[210:213], v[64:67]
	s_barrier
; #define PG8_LDA(dst, b, h) do { _Pragma("unroll") for (int m = 0; m < 4; ++m) _Pragma("unroll") for (int k = 0; k < 2; ++k) dst[m][k] = *(const PG8_LAS bf16x8*)(lds + PG8_SA(b, h) + aoff + m * 2048 + k * 1024); } while (0)
; #define PG8_WAIT_V(n) asm volatile("s_waitcnt vmcnt(" #n ")" ::: "memory")
; #define PG8_WAIT_L(n) asm volatile("s_waitcnt lgkmcnt(" #n ")" ::: "memory")
; #define PG8_BAR __builtin_amdgcn_s_barrier()
; #define PG8_SCHED __builtin_amdgcn_sched_barrier(0)
; template <class Epi, class Sched, bool ALIGN_EPI = false, bool SP2 = false, bool F8 = false, bool I8 = false, bool PF = false>
; __device__ __forceinline__ void gemm_phase(PG8_LAS unsigned char* lds, const Gemm g, const Sched& S, const Epi& E, const int wave_) {
;     ...
;             PG8_LDA(At, 1, 1); PG8_STAGE(PG8_SB(1, 0), b3, voffB); PG8_STAGE(PG8_SB(1, 1), b3 + hstep, voffB); PG8_STAGE(PG8_SA(1, 0), a3, voffA);
;             PG8_WAIT_V(8); PG8_WAIT_L(0); PG8_BAR; PG8_MMA(1, 0, At, B0); PG8_MMA(1, 1, At, B1); PG8_BAR; PG8_SCHED;
	s_add_i32 s36, s65, s39
	v_lshl_add_u64 v[150:151], v[150:151], 0, s[10:11]
	s_mov_b32 m0, s36
	ds_read_b128 v[182:185], v155 offset:49152
	ds_read_b128 v[186:189], v155 offset:50176
	ds_read_b128 v[190:193], v155 offset:51200
	ds_read_b128 v[194:197], v155 offset:52224
	ds_read_b128 v[198:201], v155 offset:53248
	ds_read_b128 v[202:205], v155 offset:54272
	ds_read_b128 v[206:209], v155 offset:55296
	ds_read_b128 v[210:213], v155 offset:56320
	global_load_lds_dwordx4 v[150:151], off
	s_add_i32 m0, s36, 0x2000
	s_add_u32 s34, s34, 0x20080
	v_lshl_add_u64 v[150:151], v[214:215], 0, s[10:11]
	s_addc_u32 s35, s35, 0
	s_add_i32 s36, s66, s39
	global_load_lds_dwordx4 v[150:151], off
	v_lshl_add_u64 v[150:151], s[34:35], 0, v[132:133]
	s_mov_b32 m0, s36
	s_nop 0
	global_load_lds_dwordx4 v[150:151], off
	v_lshl_add_u64 v[150:151], s[34:35], 0, v[128:129]
	s_add_i32 m0, s36, 0x2000
	s_nop 0
	global_load_lds_dwordx4 v[150:151], off
	v_lshl_add_u64 v[150:151], v[216:217], 0, s[10:11]
	s_mov_b32 m0, s48
	s_nop 0
	global_load_lds_dwordx4 v[150:151], off
	v_lshl_add_u64 v[150:151], v[218:219], 0, s[10:11]
	s_mov_b32 m0, s49
	s_nop 0
	global_load_lds_dwordx4 v[150:151], off
	s_waitcnt vmcnt(8)
	s_waitcnt lgkmcnt(0)
	s_barrier
	s_waitcnt lgkmcnt(0)
	v_mfma_i32_16x16x64_i8 v[60:63], v[142:145], v[182:185], v[60:63]
	v_mfma_i32_16x16x64_i8 v[56:59], v[158:161], v[182:185], v[56:59]
	v_mfma_i32_16x16x64_i8 v[44:47], v[142:145], v[190:193], v[44:47]
	v_mfma_i32_16x16x64_i8 v[40:43], v[158:161], v[190:193], v[40:43]
	v_mfma_i32_16x16x64_i8 v[28:31], v[142:145], v[198:201], v[28:31]
	v_mfma_i32_16x16x64_i8 v[24:27], v[158:161], v[198:201], v[24:27]
	v_mfma_i32_16x16x64_i8 v[12:15], v[142:145], v[206:209], v[12:15]
	v_mfma_i32_16x16x64_i8 v[8:11], v[158:161], v[206:209], v[8:11]
	v_mfma_i32_16x16x64_i8 v[60:63], v[146:149], v[186:189], v[60:63]
	v_mfma_i32_16x16x64_i8 v[56:59], v[162:165], v[186:189], v[56:59]
	v_mfma_i32_16x16x64_i8 v[44:47], v[146:149], v[194:197], v[44:47]
	v_mfma_i32_16x16x64_i8 v[40:43], v[162:165], v[194:197], v[40:43]
	v_mfma_i32_16x16x64_i8 v[28:31], v[146:149], v[202:205], v[28:31]
	v_mfma_i32_16x16x64_i8 v[24:27], v[162:165], v[202:205], v[24:27]
	v_mfma_i32_16x16x64_i8 v[12:15], v[146:149], v[210:213], v[12:15]
	v_mfma_i32_16x16x64_i8 v[8:11], v[162:165], v[210:213], v[8:11]
	v_mfma_i32_16x16x64_i8 v[52:55], v[166:169], v[182:185], v[52:55]
	v_mfma_i32_16x16x64_i8 v[48:51], v[174:177], v[182:185], v[48:51]
	v_mfma_i32_16x16x64_i8 v[36:39], v[166:169], v[190:193], v[36:39]
	v_mfma_i32_16x16x64_i8 v[32:35], v[174:177], v[190:193], v[32:35]
	v_mfma_i32_16x16x64_i8 v[20:23], v[166:169], v[198:201], v[20:23]
	v_mfma_i32_16x16x64_i8 v[16:19], v[174:177], v[198:201], v[16:19]
	v_mfma_i32_16x16x64_i8 v[4:7], v[166:169], v[206:209], v[4:7]
	v_mfma_i32_16x16x64_i8 v[0:3], v[174:177], v[206:209], v[0:3]
	v_mfma_i32_16x16x64_i8 v[52:55], v[170:173], v[186:189], v[52:55]
	v_mfma_i32_16x16x64_i8 v[48:51], v[178:181], v[186:189], v[48:51]
	v_mfma_i32_16x16x64_i8 v[36:39], v[170:173], v[194:197], v[36:39]
	v_mfma_i32_16x16x64_i8 v[32:35], v[178:181], v[194:197], v[32:35]
	v_mfma_i32_16x16x64_i8 v[20:23], v[170:173], v[202:205], v[20:23]
	v_mfma_i32_16x16x64_i8 v[16:19], v[178:181], v[202:205], v[16:19]
	v_mfma_i32_16x16x64_i8 v[4:7], v[170:173], v[210:213], v[4:7]
	v_mfma_i32_16x16x64_i8 v[0:3], v[178:181], v[210:213], v[0:3]
	s_barrier
	s_add_i32 s64, s64, 2
	s_add_u32 s30, s30, 0x100
	s_addc_u32 s31, s31, 0
	s_add_u32 s62, s62, 0x100
	s_addc_u32 s63, s63, 0
	s_cmp_gt_u32 s64, 5
	s_cbranch_scc0 .LBB0_591
	s_and_b64 vcc, exec, s[12:13]
	s_cbranch_vccz .LBB0_594
	s_barrier

; #define PG8_LDA(dst, b, h) do { _Pragma("unroll") for (int m = 0; m < 4; ++m) _Pragma("unroll") for (int k = 0; k < 2; ++k) dst[m][k] = *(const PG8_LAS bf16x8*)(lds + PG8_SA(b, h) + aoff + m * 2048 + k * 1024); } while (0)
; #define PG8_LDB(dst, b, h) do { _Pragma("unroll") for (int n = 0; n < 2; ++n) _Pragma("unroll") for (int k = 0; k < 2; ++k) dst[n][k] = *(const PG8_LAS bf16x8*)(lds + PG8_SB(b, h) + boff + n * 2048 + k * 1024); } while (0)
; #define PG8_WAIT_V(n) asm volatile("s_waitcnt vmcnt(" #n ")" ::: "memory")
; #define PG8_WAIT_L(n) asm volatile("s_waitcnt lgkmcnt(" #n ")" ::: "memory")
; #define PG8_BAR __builtin_amdgcn_s_barrier()
; #define PG8_SCHED __builtin_amdgcn_sched_barrier(0)
; template <class Epi, class Sched, bool ALIGN_EPI = false, bool SP2 = false, bool F8 = false, bool I8 = false, bool PF = false>
; __device__ __forceinline__ void gemm_phase(PG8_LAS unsigned char* lds, const Gemm g, const Sched& S, const Epi& E, const int wave_) {
;     ...
;             PG8_LDB(B0, 0, 0); PG8_LDB(B1, 0, 1); PG8_SCHED; PG8_LDA(At, 0, 0); PG8_STAGE(PG8_SA(1, 1), a1 + hstep, voffA);
;             PG8_WAIT_V(8); PG8_WAIT_L(0); PG8_BAR; PG8_MMA(0, 0, At, B0); PG8_MMA(0, 1, At, B1); PG8_BAR; PG8_SCHED;
;             PG8_LDA(At, 0, 1); PG8_STAGE(PG8_SB(0, 0), b2, voffB); PG8_STAGE(PG8_SB(0, 1), b2 + hstep, voffB); PG8_STAGE(PG8_SA(0, 0), a2, voffA);
;             PG8_WAIT_V(8); PG8_WAIT_L(0); PG8_BAR; PG8_MMA(1, 0, At, B0); PG8_MMA(1, 1, At, B1); PG8_BAR; PG8_SCHED;
.LBB0_671:
	ds_read_b128 v[24:27], v209
	ds_read_b128 v[28:31], v209 offset:1024
	ds_read_b128 v[16:19], v209 offset:2048
	ds_read_b128 v[20:23], v209 offset:3072
	ds_read_b128 v[8:11], v210
	ds_read_b128 v[12:15], v210 offset:1024
	ds_read_b128 v[0:3], v210 offset:2048
	ds_read_b128 v[4:7], v210 offset:3072
	s_add_u32 s28, s30, 0x100
	s_addc_u32 s29, s31, 0
	s_cmp_eq_u32 s65, 18
	s_cselect_b32 s37, s23, s29
	s_cselect_b32 s36, s22, s28
	s_cselect_b32 s35, s27, s64
	s_cselect_b32 s34, s26, s63
	v_lshl_add_u64 v[160:161], s[30:31], 0, v[172:173]
	s_add_i32 m0, s40, 0xc000
	ds_read_b128 v[178:181], v211
	ds_read_b128 v[182:185], v211 offset:1024
	ds_read_b128 v[186:189], v211 offset:2048
	ds_read_b128 v[190:193], v211 offset:3072
	ds_read_b128 v[194:197], v211 offset:4096
	ds_read_b128 v[198:201], v211 offset:5120
	ds_read_b128 v[212:215], v211 offset:6144
	ds_read_b128 v[216:219], v211 offset:7168
	global_load_lds_dwordx4 v[160:161], off
	v_lshl_add_u64 v[160:161], s[30:31], 0, v[174:175]
	s_add_i32 m0, s40, 0xe000
	s_nop 0
	global_load_lds_dwordx4 v[160:161], off
	s_waitcnt vmcnt(8)
	s_waitcnt lgkmcnt(0)
	s_barrier
	s_waitcnt lgkmcnt(0)
	v_mfma_f32_16x16x128_f8f6f4 v[156:159], v[24:31], v[178:185], v[156:159]
	v_mfma_f32_16x16x128_f8f6f4 v[152:155], v[16:23], v[178:185], v[152:155]
	v_mfma_f32_16x16x128_f8f6f4 v[140:143], v[24:31], v[186:193], v[140:143]
	v_mfma_f32_16x16x128_f8f6f4 v[136:139], v[16:23], v[186:193], v[136:139]
	v_mfma_f32_16x16x128_f8f6f4 v[124:127], v[24:31], v[194:201], v[124:127]
	v_mfma_f32_16x16x128_f8f6f4 v[120:123], v[16:23], v[194:201], v[120:123]
	v_mfma_f32_16x16x128_f8f6f4 v[108:111], v[24:31], v[212:219], v[108:111]
	v_mfma_f32_16x16x128_f8f6f4 v[104:107], v[16:23], v[212:219], v[104:107]
	v_mfma_f32_16x16x128_f8f6f4 v[148:151], v[8:15], v[178:185], v[148:151]
	v_mfma_f32_16x16x128_f8f6f4 v[144:147], v[0:7], v[178:185], v[144:147]
	v_mfma_f32_16x16x128_f8f6f4 v[132:135], v[8:15], v[186:193], v[132:135]
	v_mfma_f32_16x16x128_f8f6f4 v[128:131], v[0:7], v[186:193], v[128:131]
	v_mfma_f32_16x16x128_f8f6f4 v[116:119], v[8:15], v[194:201], v[116:119]
	v_mfma_f32_16x16x128_f8f6f4 v[112:115], v[0:7], v[194:201], v[112:115]
	v_mfma_f32_16x16x128_f8f6f4 v[100:103], v[8:15], v[212:219], v[100:103]
	v_mfma_f32_16x16x128_f8f6f4 v[96:99], v[0:7], v[212:219], v[96:99]
	s_barrier
	s_add_i32 s30, s53, s39
	v_lshl_add_u64 v[160:161], s[34:35], 0, v[168:169]
	s_mov_b32 m0, s30
	ds_read_b128 v[182:185], v211 offset:16384
	ds_read_b128 v[186:189], v211 offset:17408
	ds_read_b128 v[190:193], v211 offset:18432
	ds_read_b128 v[194:197], v211 offset:19456
	ds_read_b128 v[198:201], v211 offset:20480
	ds_read_b128 v[202:205], v211 offset:21504
	ds_read_b128 v[212:215], v211 offset:22528
	ds_read_b128 v[216:219], v211 offset:23552
	global_load_lds_dwordx4 v[160:161], off
	s_add_i32 m0, s30, 0x2000
	s_add_u32 s30, s34, 0x58000
	v_lshl_add_u64 v[162:163], s[34:35], 0, v[164:165]
	s_addc_u32 s31, s35, 0
	s_add_i32 s66, s54, s39
	global_load_lds_dwordx4 v[162:163], off
	v_lshl_add_u64 v[178:179], s[30:31], 0, v[168:169]
	s_mov_b32 m0, s66
	v_lshl_add_u64 v[180:181], s[36:37], 0, v[166:167]
	global_load_lds_dwordx4 v[178:179], off
	v_lshl_add_u64 v[178:179], s[30:31], 0, v[164:165]
	s_add_i32 m0, s66, 0x2000
	s_nop 0
	global_load_lds_dwordx4 v[178:179], off
	v_lshl_add_u64 v[178:179], s[36:37], 0, v[170:171]
	s_mov_b32 m0, s40
	s_nop 0
	global_load_lds_dwordx4 v[178:179], off
	s_mov_b32 m0, s41
	s_nop 0
	global_load_lds_dwordx4 v[180:181], off
	s_waitcnt vmcnt(8)
	s_waitcnt lgkmcnt(0)
	s_barrier
	s_waitcnt lgkmcnt(0)
	v_mfma_f32_16x16x128_f8f6f4 v[92:95], v[24:31], v[182:189], v[92:95]
	v_mfma_f32_16x16x128_f8f6f4 v[88:91], v[16:23], v[182:189], v[88:91]
	v_mfma_f32_16x16x128_f8f6f4 v[76:79], v[24:31], v[190:197], v[76:79]
	v_mfma_f32_16x16x128_f8f6f4 v[72:75], v[16:23], v[190:197], v[72:75]
	v_mfma_f32_16x16x128_f8f6f4 v[60:63], v[24:31], v[198:205], v[60:63]
	v_mfma_f32_16x16x128_f8f6f4 v[56:59], v[16:23], v[198:205], v[56:59]
	v_mfma_f32_16x16x128_f8f6f4 v[44:47], v[24:31], v[212:219], v[44:47]
	v_mfma_f32_16x16x128_f8f6f4 v[40:43], v[16:23], v[212:219], v[40:43]
	v_mfma_f32_16x16x128_f8f6f4 v[84:87], v[8:15], v[182:189], v[84:87]
	v_mfma_f32_16x16x128_f8f6f4 v[80:83], v[0:7], v[182:189], v[80:83]
	v_mfma_f32_16x16x128_f8f6f4 v[68:71], v[8:15], v[190:197], v[68:71]
	v_mfma_f32_16x16x128_f8f6f4 v[64:67], v[0:7], v[190:197], v[64:67]
	v_mfma_f32_16x16x128_f8f6f4 v[52:55], v[8:15], v[198:205], v[52:55]
	v_mfma_f32_16x16x128_f8f6f4 v[48:51], v[0:7], v[198:205], v[48:51]
	v_mfma_f32_16x16x128_f8f6f4 v[36:39], v[8:15], v[212:219], v[36:39]
	v_mfma_f32_16x16x128_f8f6f4 v[32:35], v[0:7], v[212:219], v[32:35]
	s_barrier
; #define PG8_LDA(dst, b, h) do { _Pragma("unroll") for (int m = 0; m < 4; ++m) _Pragma("unroll") for (int k = 0; k < 2; ++k) dst[m][k] = *(const PG8_LAS bf16x8*)(lds + PG8_SA(b, h) + aoff + m * 2048 + k * 1024); } while (0)
; #define PG8_LDB(dst, b, h) do { _Pragma("unroll") for (int n = 0; n < 2; ++n) _Pragma("unroll") for (int k = 0; k < 2; ++k) dst[n][k] = *(const PG8_LAS bf16x8*)(lds + PG8_SB(b, h) + boff + n * 2048 + k * 1024); } while (0)
; #define PG8_WAIT_V(n) asm volatile("s_waitcnt vmcnt(" #n ")" ::: "memory")
; #define PG8_WAIT_L(n) asm volatile("s_waitcnt lgkmcnt(" #n ")" ::: "memory")
; #define PG8_BAR __builtin_amdgcn_s_barrier()
; #define PG8_SCHED __builtin_amdgcn_sched_barrier(0)
; template <class Epi, class Sched, bool ALIGN_EPI = false, bool SP2 = false, bool F8 = false, bool I8 = false, bool PF = false>
; __device__ __forceinline__ void gemm_phase(PG8_LAS unsigned char* lds, const Gemm g, const Sched& S, const Epi& E, const int wave_) {
;     ...
;             PG8_LDB(B0, 1, 0); PG8_LDB(B1, 1, 1); PG8_SCHED; PG8_LDA(At, 1, 0); PG8_STAGE(PG8_SA(0, 1), a2 + hstep, voffA);
;             PG8_WAIT_V(8); PG8_WAIT_L(0); PG8_BAR; PG8_MMA(0, 0, At, B0); PG8_MMA(0, 1, At, B1); PG8_BAR; PG8_SCHED;
;             PG8_LDA(At, 1, 1); PG8_STAGE(PG8_SB(1, 0), b3, voffB); PG8_STAGE(PG8_SB(1, 1), b3 + hstep, voffB); PG8_STAGE(PG8_SA(1, 0), a3, voffA);
;             PG8_WAIT_V(8); PG8_WAIT_L(0); PG8_BAR; PG8_MMA(1, 0, At, B0); PG8_MMA(1, 1, At, B1); PG8_BAR; PG8_SCHED;
	s_add_i32 s66, 0, 0x18000
	s_add_i32 s67, 0, 0x1c000
	v_add_u32_e32 v12, s66, v208
	v_add_u32_e32 v28, s67, v208
	ds_read_b128 v[0:3], v12
	ds_read_b128 v[4:7], v12 offset:1024
	ds_read_b128 v[8:11], v12 offset:2048
	ds_read_b128 v[12:15], v12 offset:3072
	ds_read_b128 v[16:19], v28
	ds_read_b128 v[20:23], v28 offset:1024
	ds_read_b128 v[24:27], v28 offset:2048
	ds_read_b128 v[28:31], v28 offset:3072
	s_add_u32 s30, s36, 0x58000
	s_addc_u32 s31, s37, 0
	s_mov_b32 m0, s42
	v_lshl_add_u64 v[206:207], s[30:31], 0, v[170:171]
	ds_read_b128 v[182:185], v211 offset:32768
	ds_read_b128 v[186:189], v211 offset:33792
	ds_read_b128 v[190:193], v211 offset:34816
	ds_read_b128 v[194:197], v211 offset:35840
	ds_read_b128 v[198:201], v211 offset:36864
	ds_read_b128 v[202:205], v211 offset:37888
	ds_read_b128 v[212:215], v211 offset:38912
	ds_read_b128 v[216:219], v211 offset:39936
	global_load_lds_dwordx4 v[206:207], off
	v_lshl_add_u64 v[206:207], s[30:31], 0, v[166:167]
	s_mov_b32 m0, s43
	s_nop 0
	global_load_lds_dwordx4 v[206:207], off
	s_waitcnt vmcnt(8)
	s_waitcnt lgkmcnt(0)
	s_barrier
	s_waitcnt lgkmcnt(0)
	v_mfma_f32_16x16x128_f8f6f4 v[156:159], v[0:7], v[182:189], v[156:159]
	v_mfma_f32_16x16x128_f8f6f4 v[152:155], v[8:15], v[182:189], v[152:155]
	v_mfma_f32_16x16x128_f8f6f4 v[140:143], v[0:7], v[190:197], v[140:143]
	v_mfma_f32_16x16x128_f8f6f4 v[136:139], v[8:15], v[190:197], v[136:139]
	v_mfma_f32_16x16x128_f8f6f4 v[124:127], v[0:7], v[198:205], v[124:127]
	v_mfma_f32_16x16x128_f8f6f4 v[120:123], v[8:15], v[198:205], v[120:123]
	v_mfma_f32_16x16x128_f8f6f4 v[108:111], v[0:7], v[212:219], v[108:111]
	v_mfma_f32_16x16x128_f8f6f4 v[104:107], v[8:15], v[212:219], v[104:107]
	v_mfma_f32_16x16x128_f8f6f4 v[148:151], v[16:23], v[182:189], v[148:151]
	v_mfma_f32_16x16x128_f8f6f4 v[144:147], v[24:31], v[182:189], v[144:147]
	v_mfma_f32_16x16x128_f8f6f4 v[132:135], v[16:23], v[190:197], v[132:135]
	v_mfma_f32_16x16x128_f8f6f4 v[128:131], v[24:31], v[190:197], v[128:131]
	v_mfma_f32_16x16x128_f8f6f4 v[116:119], v[16:23], v[198:205], v[116:119]
	v_mfma_f32_16x16x128_f8f6f4 v[112:115], v[24:31], v[198:205], v[112:115]
	v_mfma_f32_16x16x128_f8f6f4 v[100:103], v[16:23], v[212:219], v[100:103]
	v_mfma_f32_16x16x128_f8f6f4 v[96:99], v[24:31], v[212:219], v[96:99]
	s_barrier
	s_add_i32 s30, s66, s39
	v_lshl_add_u64 v[160:161], v[160:161], 0, s[10:11]
	s_mov_b32 m0, s30
	ds_read_b128 v[182:185], v211 offset:49152
	ds_read_b128 v[186:189], v211 offset:50176
	ds_read_b128 v[190:193], v211 offset:51200
	ds_read_b128 v[194:197], v211 offset:52224
	ds_read_b128 v[198:201], v211 offset:53248
	ds_read_b128 v[202:205], v211 offset:54272
	ds_read_b128 v[212:215], v211 offset:55296
	ds_read_b128 v[216:219], v211 offset:56320
	global_load_lds_dwordx4 v[160:161], off
	s_add_i32 m0, s30, 0x2000
	s_add_u32 s30, s34, 0x58080
	v_lshl_add_u64 v[160:161], v[162:163], 0, s[10:11]
	s_addc_u32 s31, s35, 0
	s_add_i32 s34, s67, s39
	global_load_lds_dwordx4 v[160:161], off
	v_lshl_add_u64 v[160:161], s[30:31], 0, v[168:169]
	s_mov_b32 m0, s34
	s_nop 0
	global_load_lds_dwordx4 v[160:161], off
	v_lshl_add_u64 v[160:161], s[30:31], 0, v[164:165]
	s_add_i32 m0, s34, 0x2000
	s_nop 0
	global_load_lds_dwordx4 v[160:161], off
	v_lshl_add_u64 v[160:161], v[178:179], 0, s[10:11]
	s_mov_b32 m0, s50
	s_nop 0
	global_load_lds_dwordx4 v[160:161], off
	v_lshl_add_u64 v[160:161], v[180:181], 0, s[10:11]
	s_mov_b32 m0, s51
	s_nop 0
	global_load_lds_dwordx4 v[160:161], off
	s_waitcnt vmcnt(8)
	s_waitcnt lgkmcnt(0)
	s_barrier
	s_waitcnt lgkmcnt(0)
	v_mfma_f32_16x16x128_f8f6f4 v[92:95], v[0:7], v[182:189], v[92:95]
	v_mfma_f32_16x16x128_f8f6f4 v[88:91], v[8:15], v[182:189], v[88:91]
	v_mfma_f32_16x16x128_f8f6f4 v[76:79], v[0:7], v[190:197], v[76:79]
	v_mfma_f32_16x16x128_f8f6f4 v[72:75], v[8:15], v[190:197], v[72:75]
	v_mfma_f32_16x16x128_f8f6f4 v[60:63], v[0:7], v[198:205], v[60:63]
	v_mfma_f32_16x16x128_f8f6f4 v[56:59], v[8:15], v[198:205], v[56:59]
	v_mfma_f32_16x16x128_f8f6f4 v[44:47], v[0:7], v[212:219], v[44:47]
	v_mfma_f32_16x16x128_f8f6f4 v[40:43], v[8:15], v[212:219], v[40:43]
	v_mfma_f32_16x16x128_f8f6f4 v[84:87], v[16:23], v[182:189], v[84:87]
	v_mfma_f32_16x16x128_f8f6f4 v[80:83], v[24:31], v[182:189], v[80:83]
	v_mfma_f32_16x16x128_f8f6f4 v[68:71], v[16:23], v[190:197], v[68:71]
	v_mfma_f32_16x16x128_f8f6f4 v[64:67], v[24:31], v[190:197], v[64:67]
	v_mfma_f32_16x16x128_f8f6f4 v[52:55], v[16:23], v[198:205], v[52:55]
	v_mfma_f32_16x16x128_f8f6f4 v[48:51], v[24:31], v[198:205], v[48:51]
	v_mfma_f32_16x16x128_f8f6f4 v[36:39], v[16:23], v[212:219], v[36:39]
	v_mfma_f32_16x16x128_f8f6f4 v[32:35], v[24:31], v[212:219], v[32:35]
	s_barrier
	s_add_i32 s65, s65, 2
	s_add_u32 s63, s63, 0x100
	s_addc_u32 s64, s64, 0
	s_cmp_gt_u32 s65, 19
	s_mov_b64 s[30:31], s[28:29]
	s_cbranch_scc0 .LBB0_671
	s_and_b64 vcc, exec, s[12:13]
	s_cbranch_vccz .LBB0_674
	s_barrier

; #define PG8_LDA(dst, b, h) do { _Pragma("unroll") for (int m = 0; m < 4; ++m) _Pragma("unroll") for (int k = 0; k < 2; ++k) dst[m][k] = *(const PG8_LAS bf16x8*)(lds + PG8_SA(b, h) + aoff + m * 2048 + k * 1024); } while (0)
; #define PG8_LDB(dst, b, h) do { _Pragma("unroll") for (int n = 0; n < 2; ++n) _Pragma("unroll") for (int k = 0; k < 2; ++k) dst[n][k] = *(const PG8_LAS bf16x8*)(lds + PG8_SB(b, h) + boff + n * 2048 + k * 1024); } while (0)
; #define PG8_WAIT_V(n) asm volatile("s_waitcnt vmcnt(" #n ")" ::: "memory")
; #define PG8_WAIT_L(n) asm volatile("s_waitcnt lgkmcnt(" #n ")" ::: "memory")
; #define PG8_BAR __builtin_amdgcn_s_barrier()
; #define PG8_SCHED __builtin_amdgcn_sched_barrier(0)
; template <class Epi, class Sched, bool ALIGN_EPI = false, bool SP2 = false, bool F8 = false, bool I8 = false, bool PF = false>
; __device__ __forceinline__ void gemm_phase(PG8_LAS unsigned char* lds, const Gemm g, const Sched& S, const Epi& E, const int wave_) {
;     ...
;             PG8_LDB(B0, 0, 0); PG8_LDB(B1, 0, 1); PG8_SCHED; PG8_LDA(At, 0, 0); PG8_STAGE(PG8_SA(1, 1), a1 + hstep, voffA);
;             PG8_WAIT_V(8); PG8_WAIT_L(0); PG8_BAR; PG8_MMA(0, 0, At, B0); PG8_MMA(0, 1, At, B1); PG8_BAR; PG8_SCHED;
;             PG8_LDA(At, 0, 1); PG8_STAGE(PG8_SB(0, 0), b2, voffB); PG8_STAGE(PG8_SB(0, 1), b2 + hstep, voffB); PG8_STAGE(PG8_SA(0, 0), a2, voffA);
;             PG8_WAIT_V(8); PG8_WAIT_L(0); PG8_BAR; PG8_MMA(1, 0, At, B0); PG8_MMA(1, 1, At, B1); PG8_BAR; PG8_SCHED;
.LBB0_809:
	ds_read_b128 v[142:145], v151
	ds_read_b128 v[156:159], v151 offset:1024
	ds_read_b128 v[160:163], v151 offset:2048
	ds_read_b128 v[164:167], v151 offset:3072
	ds_read_b128 v[168:171], v153
	ds_read_b128 v[172:175], v153 offset:1024
	ds_read_b128 v[176:179], v153 offset:2048
	ds_read_b128 v[180:183], v153 offset:3072
	s_add_u32 s34, s30, 0xfffe0080
	s_addc_u32 s35, s31, -1
	s_cmp_eq_u32 s63, 4
	s_cselect_b32 s37, s19, s35
	s_cselect_b32 s36, s55, s34
	s_cselect_b32 s35, s17, s62
	s_cselect_b32 s34, s56, s57
	v_lshl_add_u64 v[146:147], s[30:31], 0, v[136:137]
	s_add_i32 m0, s29, 0xc000
	ds_read_b128 v[184:187], v155
	ds_read_b128 v[188:191], v155 offset:1024
	ds_read_b128 v[192:195], v155 offset:2048
	ds_read_b128 v[196:199], v155 offset:3072
	ds_read_b128 v[200:203], v155 offset:4096
	ds_read_b128 v[204:207], v155 offset:5120
	ds_read_b128 v[208:211], v155 offset:6144
	ds_read_b128 v[212:215], v155 offset:7168
	global_load_lds_dwordx4 v[146:147], off
	v_lshl_add_u64 v[146:147], s[30:31], 0, v[138:139]
	s_add_i32 m0, s29, 0xe000
	s_nop 0
	global_load_lds_dwordx4 v[146:147], off
	s_waitcnt vmcnt(8)
	s_waitcnt lgkmcnt(0)
	s_barrier
	s_waitcnt lgkmcnt(0)
	v_mfma_i32_16x16x64_i8 v[124:127], v[142:145], v[184:187], v[124:127]
	v_mfma_i32_16x16x64_i8 v[120:123], v[160:163], v[184:187], v[120:123]
	v_mfma_i32_16x16x64_i8 v[108:111], v[142:145], v[192:195], v[108:111]
	v_mfma_i32_16x16x64_i8 v[104:107], v[160:163], v[192:195], v[104:107]
	v_mfma_i32_16x16x64_i8 v[92:95], v[142:145], v[200:203], v[92:95]
	v_mfma_i32_16x16x64_i8 v[88:91], v[160:163], v[200:203], v[88:91]
	v_mfma_i32_16x16x64_i8 v[76:79], v[142:145], v[208:211], v[76:79]
	v_mfma_i32_16x16x64_i8 v[72:75], v[160:163], v[208:211], v[72:75]
	v_mfma_i32_16x16x64_i8 v[124:127], v[156:159], v[188:191], v[124:127]
	v_mfma_i32_16x16x64_i8 v[120:123], v[164:167], v[188:191], v[120:123]
	v_mfma_i32_16x16x64_i8 v[108:111], v[156:159], v[196:199], v[108:111]
	v_mfma_i32_16x16x64_i8 v[104:107], v[164:167], v[196:199], v[104:107]
	v_mfma_i32_16x16x64_i8 v[92:95], v[156:159], v[204:207], v[92:95]
	v_mfma_i32_16x16x64_i8 v[88:91], v[164:167], v[204:207], v[88:91]
	v_mfma_i32_16x16x64_i8 v[76:79], v[156:159], v[212:215], v[76:79]
	v_mfma_i32_16x16x64_i8 v[72:75], v[164:167], v[212:215], v[72:75]
	v_mfma_i32_16x16x64_i8 v[116:119], v[168:171], v[184:187], v[116:119]
	v_mfma_i32_16x16x64_i8 v[112:115], v[176:179], v[184:187], v[112:115]
	v_mfma_i32_16x16x64_i8 v[100:103], v[168:171], v[192:195], v[100:103]
	v_mfma_i32_16x16x64_i8 v[96:99], v[176:179], v[192:195], v[96:99]
	v_mfma_i32_16x16x64_i8 v[84:87], v[168:171], v[200:203], v[84:87]
	v_mfma_i32_16x16x64_i8 v[80:83], v[176:179], v[200:203], v[80:83]
	v_mfma_i32_16x16x64_i8 v[68:71], v[168:171], v[208:211], v[68:71]
	v_mfma_i32_16x16x64_i8 v[64:67], v[176:179], v[208:211], v[64:67]
	v_mfma_i32_16x16x64_i8 v[116:119], v[172:175], v[188:191], v[116:119]
	v_mfma_i32_16x16x64_i8 v[112:115], v[180:183], v[188:191], v[112:115]
	v_mfma_i32_16x16x64_i8 v[100:103], v[172:175], v[196:199], v[100:103]
	v_mfma_i32_16x16x64_i8 v[96:99], v[180:183], v[196:199], v[96:99]
	v_mfma_i32_16x16x64_i8 v[84:87], v[172:175], v[204:207], v[84:87]
	v_mfma_i32_16x16x64_i8 v[80:83], v[180:183], v[204:207], v[80:83]
	v_mfma_i32_16x16x64_i8 v[68:71], v[172:175], v[212:215], v[68:71]
	v_mfma_i32_16x16x64_i8 v[64:67], v[180:183], v[212:215], v[64:67]
	s_barrier
	s_add_i32 s64, s51, s39
	v_lshl_add_u64 v[146:147], s[34:35], 0, v[132:133]
	s_mov_b32 m0, s64
	ds_read_b128 v[184:187], v155 offset:16384
	ds_read_b128 v[188:191], v155 offset:17408
	ds_read_b128 v[192:195], v155 offset:18432
	ds_read_b128 v[196:199], v155 offset:19456
	ds_read_b128 v[200:203], v155 offset:20480
	ds_read_b128 v[204:207], v155 offset:21504
	ds_read_b128 v[208:211], v155 offset:22528
	ds_read_b128 v[212:215], v155 offset:23552
	global_load_lds_dwordx4 v[146:147], off
	s_add_i32 m0, s64, 0x2000
	s_add_u32 s64, s34, 0x20000
	v_lshl_add_u64 v[216:217], s[34:35], 0, v[128:129]
	s_addc_u32 s65, s35, 0
	s_add_i32 s66, s52, s39
	global_load_lds_dwordx4 v[216:217], off
	v_lshl_add_u64 v[218:219], s[64:65], 0, v[132:133]
	s_mov_b32 m0, s66
	v_lshl_add_u64 v[220:221], s[36:37], 0, v[130:131]
	global_load_lds_dwordx4 v[218:219], off
	v_lshl_add_u64 v[218:219], s[64:65], 0, v[128:129]
	s_add_i32 m0, s66, 0x2000
	s_nop 0
	global_load_lds_dwordx4 v[218:219], off
	v_lshl_add_u64 v[218:219], s[36:37], 0, v[134:135]
	s_mov_b32 m0, s29
	s_nop 0
	global_load_lds_dwordx4 v[218:219], off
	s_mov_b32 m0, s41
	s_nop 0
	global_load_lds_dwordx4 v[220:221], off
	s_waitcnt vmcnt(8)
	s_waitcnt lgkmcnt(0)
	s_barrier
; #define PG8_LDA(dst, b, h) do { _Pragma("unroll") for (int m = 0; m < 4; ++m) _Pragma("unroll") for (int k = 0; k < 2; ++k) dst[m][k] = *(const PG8_LAS bf16x8*)(lds + PG8_SA(b, h) + aoff + m * 2048 + k * 1024); } while (0)
; #define PG8_LDB(dst, b, h) do { _Pragma("unroll") for (int n = 0; n < 2; ++n) _Pragma("unroll") for (int k = 0; k < 2; ++k) dst[n][k] = *(const PG8_LAS bf16x8*)(lds + PG8_SB(b, h) + boff + n * 2048 + k * 1024); } while (0)
; #define PG8_WAIT_V(n) asm volatile("s_waitcnt vmcnt(" #n ")" ::: "memory")
; #define PG8_WAIT_L(n) asm volatile("s_waitcnt lgkmcnt(" #n ")" ::: "memory")
; #define PG8_BAR __builtin_amdgcn_s_barrier()
; #define PG8_SCHED __builtin_amdgcn_sched_barrier(0)
; template <class Epi, class Sched, bool ALIGN_EPI = false, bool SP2 = false, bool F8 = false, bool I8 = false, bool PF = false>
; __device__ __forceinline__ void gemm_phase(PG8_LAS unsigned char* lds, const Gemm g, const Sched& S, const Epi& E, const int wave_) {
;     ...
;             PG8_WAIT_V(8); PG8_WAIT_L(0); PG8_BAR; PG8_MMA(1, 0, At, B0); PG8_MMA(1, 1, At, B1); PG8_BAR; PG8_SCHED;
;             PG8_LDB(B0, 1, 0); PG8_LDB(B1, 1, 1); PG8_SCHED; PG8_LDA(At, 1, 0); PG8_STAGE(PG8_SA(0, 1), a2 + hstep, voffA);
;             PG8_WAIT_V(8); PG8_WAIT_L(0); PG8_BAR; PG8_MMA(0, 0, At, B0); PG8_MMA(0, 1, At, B1); PG8_BAR; PG8_SCHED;
	s_waitcnt lgkmcnt(0)
	v_mfma_i32_16x16x64_i8 v[60:63], v[142:145], v[184:187], v[60:63]
	v_mfma_i32_16x16x64_i8 v[56:59], v[160:163], v[184:187], v[56:59]
	v_mfma_i32_16x16x64_i8 v[44:47], v[142:145], v[192:195], v[44:47]
	v_mfma_i32_16x16x64_i8 v[40:43], v[160:163], v[192:195], v[40:43]
	v_mfma_i32_16x16x64_i8 v[28:31], v[142:145], v[200:203], v[28:31]
	v_mfma_i32_16x16x64_i8 v[24:27], v[160:163], v[200:203], v[24:27]
	v_mfma_i32_16x16x64_i8 v[12:15], v[142:145], v[208:211], v[12:15]
	v_mfma_i32_16x16x64_i8 v[8:11], v[160:163], v[208:211], v[8:11]
	v_mfma_i32_16x16x64_i8 v[60:63], v[156:159], v[188:191], v[60:63]
	v_mfma_i32_16x16x64_i8 v[56:59], v[164:167], v[188:191], v[56:59]
	v_mfma_i32_16x16x64_i8 v[44:47], v[156:159], v[196:199], v[44:47]
	v_mfma_i32_16x16x64_i8 v[40:43], v[164:167], v[196:199], v[40:43]
	v_mfma_i32_16x16x64_i8 v[28:31], v[156:159], v[204:207], v[28:31]
	v_mfma_i32_16x16x64_i8 v[24:27], v[164:167], v[204:207], v[24:27]
	v_mfma_i32_16x16x64_i8 v[12:15], v[156:159], v[212:215], v[12:15]
	v_mfma_i32_16x16x64_i8 v[8:11], v[164:167], v[212:215], v[8:11]
	v_mfma_i32_16x16x64_i8 v[52:55], v[168:171], v[184:187], v[52:55]
	v_mfma_i32_16x16x64_i8 v[48:51], v[176:179], v[184:187], v[48:51]
	v_mfma_i32_16x16x64_i8 v[36:39], v[168:171], v[192:195], v[36:39]
	v_mfma_i32_16x16x64_i8 v[32:35], v[176:179], v[192:195], v[32:35]
	v_mfma_i32_16x16x64_i8 v[20:23], v[168:171], v[200:203], v[20:23]
	v_mfma_i32_16x16x64_i8 v[16:19], v[176:179], v[200:203], v[16:19]
	v_mfma_i32_16x16x64_i8 v[4:7], v[168:171], v[208:211], v[4:7]
	v_mfma_i32_16x16x64_i8 v[0:3], v[176:179], v[208:211], v[0:3]
	v_mfma_i32_16x16x64_i8 v[52:55], v[172:175], v[188:191], v[52:55]
	v_mfma_i32_16x16x64_i8 v[48:51], v[180:183], v[188:191], v[48:51]
	v_mfma_i32_16x16x64_i8 v[36:39], v[172:175], v[196:199], v[36:39]
	v_mfma_i32_16x16x64_i8 v[32:35], v[180:183], v[196:199], v[32:35]
	v_mfma_i32_16x16x64_i8 v[20:23], v[172:175], v[204:207], v[20:23]
	v_mfma_i32_16x16x64_i8 v[16:19], v[180:183], v[204:207], v[16:19]
	v_mfma_i32_16x16x64_i8 v[4:7], v[172:175], v[212:215], v[4:7]
	v_mfma_i32_16x16x64_i8 v[0:3], v[180:183], v[212:215], v[0:3]
	s_barrier
	s_add_i32 s64, 0, 0x18000
	v_add_u32_e32 v148, s64, v149
	s_add_i32 s65, 0, 0x1c000
	ds_read_b128 v[142:145], v148
	ds_read_b128 v[156:159], v148 offset:1024
	ds_read_b128 v[160:163], v148 offset:2048
	ds_read_b128 v[164:167], v148 offset:3072
	v_add_u32_e32 v148, s65, v149
	ds_read_b128 v[168:171], v148
	ds_read_b128 v[172:175], v148 offset:1024
	ds_read_b128 v[176:179], v148 offset:2048
	ds_read_b128 v[180:183], v148 offset:3072
	s_add_u32 s36, s36, 0x20000
	s_addc_u32 s37, s37, 0
	s_mov_b32 m0, s42
	v_lshl_add_u64 v[222:223], s[36:37], 0, v[134:135]
	ds_read_b128 v[184:187], v155 offset:32768
	ds_read_b128 v[188:191], v155 offset:33792
	ds_read_b128 v[192:195], v155 offset:34816
	ds_read_b128 v[196:199], v155 offset:35840
	ds_read_b128 v[200:203], v155 offset:36864
	ds_read_b128 v[204:207], v155 offset:37888
	ds_read_b128 v[208:211], v155 offset:38912
	ds_read_b128 v[212:215], v155 offset:39936
	global_load_lds_dwordx4 v[222:223], off
	v_lshl_add_u64 v[222:223], s[36:37], 0, v[130:131]
	s_mov_b32 m0, s43
	s_nop 0
	global_load_lds_dwordx4 v[222:223], off
	s_waitcnt vmcnt(8)
	s_waitcnt lgkmcnt(0)
	s_barrier
	s_waitcnt lgkmcnt(0)
	v_mfma_i32_16x16x64_i8 v[124:127], v[142:145], v[184:187], v[124:127]
	v_mfma_i32_16x16x64_i8 v[120:123], v[160:163], v[184:187], v[120:123]
	v_mfma_i32_16x16x64_i8 v[108:111], v[142:145], v[192:195], v[108:111]
	v_mfma_i32_16x16x64_i8 v[104:107], v[160:163], v[192:195], v[104:107]
	v_mfma_i32_16x16x64_i8 v[92:95], v[142:145], v[200:203], v[92:95]
	v_mfma_i32_16x16x64_i8 v[88:91], v[160:163], v[200:203], v[88:91]
	v_mfma_i32_16x16x64_i8 v[76:79], v[142:145], v[208:211], v[76:79]
	v_mfma_i32_16x16x64_i8 v[72:75], v[160:163], v[208:211], v[72:75]
	v_mfma_i32_16x16x64_i8 v[124:127], v[156:159], v[188:191], v[124:127]
	v_mfma_i32_16x16x64_i8 v[120:123], v[164:167], v[188:191], v[120:123]
	v_mfma_i32_16x16x64_i8 v[108:111], v[156:159], v[196:199], v[108:111]
	v_mfma_i32_16x16x64_i8 v[104:107], v[164:167], v[196:199], v[104:107]
	v_mfma_i32_16x16x64_i8 v[92:95], v[156:159], v[204:207], v[92:95]
	v_mfma_i32_16x16x64_i8 v[88:91], v[164:167], v[204:207], v[88:91]
	v_mfma_i32_16x16x64_i8 v[76:79], v[156:159], v[212:215], v[76:79]
	v_mfma_i32_16x16x64_i8 v[72:75], v[164:167], v[212:215], v[72:75]
	v_mfma_i32_16x16x64_i8 v[116:119], v[168:171], v[184:187], v[116:119]
	v_mfma_i32_16x16x64_i8 v[112:115], v[176:179], v[184:187], v[112:115]
	v_mfma_i32_16x16x64_i8 v[100:103], v[168:171], v[192:195], v[100:103]
	v_mfma_i32_16x16x64_i8 v[96:99], v[176:179], v[192:195], v[96:99]
	v_mfma_i32_16x16x64_i8 v[84:87], v[168:171], v[200:203], v[84:87]
	v_mfma_i32_16x16x64_i8 v[80:83], v[176:179], v[200:203], v[80:83]
	v_mfma_i32_16x16x64_i8 v[68:71], v[168:171], v[208:211], v[68:71]
	v_mfma_i32_16x16x64_i8 v[64:67], v[176:179], v[208:211], v[64:67]
	v_mfma_i32_16x16x64_i8 v[116:119], v[172:175], v[188:191], v[116:119]
	v_mfma_i32_16x16x64_i8 v[112:115], v[180:183], v[188:191], v[112:115]
	v_mfma_i32_16x16x64_i8 v[100:103], v[172:175], v[196:199], v[100:103]
	v_mfma_i32_16x16x64_i8 v[96:99], v[180:183], v[196:199], v[96:99]
	v_mfma_i32_16x16x64_i8 v[84:87], v[172:175], v[204:207], v[84:87]
	v_mfma_i32_16x16x64_i8 v[80:83], v[180:183], v[204:207], v[80:83]
	v_mfma_i32_16x16x64_i8 v[68:71], v[172:175], v[212:215], v[68:71]
	v_mfma_i32_16x16x64_i8 v[64:67], v[180:183], v[212:215], v[64:67]
	s_barrier
; #define PG8_LDA(dst, b, h) do { _Pragma("unroll") for (int m = 0; m < 4; ++m) _Pragma("unroll") for (int k = 0; k < 2; ++k) dst[m][k] = *(const PG8_LAS bf16x8*)(lds + PG8_SA(b, h) + aoff + m * 2048 + k * 1024); } while (0)
; #define PG8_WAIT_V(n) asm volatile("s_waitcnt vmcnt(" #n ")" ::: "memory")
; #define PG8_WAIT_L(n) asm volatile("s_waitcnt lgkmcnt(" #n ")" ::: "memory")
; #define PG8_BAR __builtin_amdgcn_s_barrier()
; #define PG8_SCHED __builtin_amdgcn_sched_barrier(0)
; template <class Epi, class Sched, bool ALIGN_EPI = false, bool SP2 = false, bool F8 = false, bool I8 = false, bool PF = false>
; __device__ __forceinline__ void gemm_phase(PG8_LAS unsigned char* lds, const Gemm g, const Sched& S, const Epi& E, const int wave_) {
;     ...
;             PG8_LDA(At, 1, 1); PG8_STAGE(PG8_SB(1, 0), b3, voffB); PG8_STAGE(PG8_SB(1, 1), b3 + hstep, voffB); PG8_STAGE(PG8_SA(1, 0), a3, voffA);
;             PG8_WAIT_V(8); PG8_WAIT_L(0); PG8_BAR; PG8_MMA(1, 0, At, B0); PG8_MMA(1, 1, At, B1); PG8_BAR; PG8_SCHED;
	s_add_i32 s36, s64, s39
	v_lshl_add_u64 v[146:147], v[146:147], 0, s[10:11]
	s_mov_b32 m0, s36
	ds_read_b128 v[184:187], v155 offset:49152
	ds_read_b128 v[188:191], v155 offset:50176
	ds_read_b128 v[192:195], v155 offset:51200
	ds_read_b128 v[196:199], v155 offset:52224
	ds_read_b128 v[200:203], v155 offset:53248
	ds_read_b128 v[204:207], v155 offset:54272
	ds_read_b128 v[208:211], v155 offset:55296
	ds_read_b128 v[212:215], v155 offset:56320
	global_load_lds_dwordx4 v[146:147], off
	s_add_i32 m0, s36, 0x2000
	s_add_u32 s34, s34, 0x20080
	v_lshl_add_u64 v[146:147], v[216:217], 0, s[10:11]
	s_addc_u32 s35, s35, 0
	s_add_i32 s36, s65, s39
	global_load_lds_dwordx4 v[146:147], off
	v_lshl_add_u64 v[146:147], s[34:35], 0, v[132:133]
	s_mov_b32 m0, s36
	s_nop 0
	global_load_lds_dwordx4 v[146:147], off
	v_lshl_add_u64 v[146:147], s[34:35], 0, v[128:129]
	s_add_i32 m0, s36, 0x2000
	s_nop 0
	global_load_lds_dwordx4 v[146:147], off
	v_lshl_add_u64 v[146:147], v[218:219], 0, s[10:11]
	s_mov_b32 m0, s48
	s_nop 0
	global_load_lds_dwordx4 v[146:147], off
	v_lshl_add_u64 v[146:147], v[220:221], 0, s[10:11]
	s_mov_b32 m0, s49
	s_nop 0
	global_load_lds_dwordx4 v[146:147], off
	s_waitcnt vmcnt(8)
	s_waitcnt lgkmcnt(0)
	s_barrier
	s_waitcnt lgkmcnt(0)
	v_mfma_i32_16x16x64_i8 v[60:63], v[142:145], v[184:187], v[60:63]
	v_mfma_i32_16x16x64_i8 v[56:59], v[160:163], v[184:187], v[56:59]
	v_mfma_i32_16x16x64_i8 v[44:47], v[142:145], v[192:195], v[44:47]
	v_mfma_i32_16x16x64_i8 v[40:43], v[160:163], v[192:195], v[40:43]
	v_mfma_i32_16x16x64_i8 v[28:31], v[142:145], v[200:203], v[28:31]
	v_mfma_i32_16x16x64_i8 v[24:27], v[160:163], v[200:203], v[24:27]
	v_mfma_i32_16x16x64_i8 v[12:15], v[142:145], v[208:211], v[12:15]
	v_mfma_i32_16x16x64_i8 v[8:11], v[160:163], v[208:211], v[8:11]
	v_mfma_i32_16x16x64_i8 v[60:63], v[156:159], v[188:191], v[60:63]
	v_mfma_i32_16x16x64_i8 v[56:59], v[164:167], v[188:191], v[56:59]
	v_mfma_i32_16x16x64_i8 v[44:47], v[156:159], v[196:199], v[44:47]
	v_mfma_i32_16x16x64_i8 v[40:43], v[164:167], v[196:199], v[40:43]
	v_mfma_i32_16x16x64_i8 v[28:31], v[156:159], v[204:207], v[28:31]
	v_mfma_i32_16x16x64_i8 v[24:27], v[164:167], v[204:207], v[24:27]
	v_mfma_i32_16x16x64_i8 v[12:15], v[156:159], v[212:215], v[12:15]
	v_mfma_i32_16x16x64_i8 v[8:11], v[164:167], v[212:215], v[8:11]
	v_mfma_i32_16x16x64_i8 v[52:55], v[168:171], v[184:187], v[52:55]
	v_mfma_i32_16x16x64_i8 v[48:51], v[176:179], v[184:187], v[48:51]
	v_mfma_i32_16x16x64_i8 v[36:39], v[168:171], v[192:195], v[36:39]
	v_mfma_i32_16x16x64_i8 v[32:35], v[176:179], v[192:195], v[32:35]
	v_mfma_i32_16x16x64_i8 v[20:23], v[168:171], v[200:203], v[20:23]
	v_mfma_i32_16x16x64_i8 v[16:19], v[176:179], v[200:203], v[16:19]
	v_mfma_i32_16x16x64_i8 v[4:7], v[168:171], v[208:211], v[4:7]
	v_mfma_i32_16x16x64_i8 v[0:3], v[176:179], v[208:211], v[0:3]
	v_mfma_i32_16x16x64_i8 v[52:55], v[172:175], v[188:191], v[52:55]
	v_mfma_i32_16x16x64_i8 v[48:51], v[180:183], v[188:191], v[48:51]
	v_mfma_i32_16x16x64_i8 v[36:39], v[172:175], v[196:199], v[36:39]
	v_mfma_i32_16x16x64_i8 v[32:35], v[180:183], v[196:199], v[32:35]
	v_mfma_i32_16x16x64_i8 v[20:23], v[172:175], v[204:207], v[20:23]
	v_mfma_i32_16x16x64_i8 v[16:19], v[180:183], v[204:207], v[16:19]
	v_mfma_i32_16x16x64_i8 v[4:7], v[172:175], v[212:215], v[4:7]
	v_mfma_i32_16x16x64_i8 v[0:3], v[180:183], v[212:215], v[0:3]
	s_barrier
	s_add_i32 s63, s63, 2
	s_add_u32 s30, s30, 0x100
	s_addc_u32 s31, s31, 0
	s_add_u32 s57, s57, 0x100
	s_addc_u32 s62, s62, 0
	s_cmp_gt_u32 s63, 5
	s_cbranch_scc0 .LBB0_809
	s_and_b64 vcc, exec, s[12:13]
	s_cbranch_vccz .LBB0_812
	s_barrier

; #define PG8_LDA(dst, b, h) do { _Pragma("unroll") for (int m = 0; m < 4; ++m) _Pragma("unroll") for (int k = 0; k < 2; ++k) dst[m][k] = *(const PG8_LAS bf16x8*)(lds + PG8_SA(b, h) + aoff + m * 2048 + k * 1024); } while (0)
; #define PG8_LDB(dst, b, h) do { _Pragma("unroll") for (int n = 0; n < 2; ++n) _Pragma("unroll") for (int k = 0; k < 2; ++k) dst[n][k] = *(const PG8_LAS bf16x8*)(lds + PG8_SB(b, h) + boff + n * 2048 + k * 1024); } while (0)
; #define PG8_WAIT_V(n) asm volatile("s_waitcnt vmcnt(" #n ")" ::: "memory")
; #define PG8_WAIT_L(n) asm volatile("s_waitcnt lgkmcnt(" #n ")" ::: "memory")
; #define PG8_BAR __builtin_amdgcn_s_barrier()
; #define PG8_SCHED __builtin_amdgcn_sched_barrier(0)
; template <class Epi, class Sched, bool ALIGN_EPI = false, bool SP2 = false, bool F8 = false, bool I8 = false, bool PF = false>
; __device__ __forceinline__ void gemm_phase(PG8_LAS unsigned char* lds, const Gemm g, const Sched& S, const Epi& E, const int wave_) {
;     ...
;             PG8_LDB(B0, 0, 0); PG8_LDB(B1, 0, 1); PG8_SCHED; PG8_LDA(At, 0, 0); PG8_STAGE(PG8_SA(1, 1), a1 + hstep, voffA);
;             PG8_WAIT_V(8); PG8_WAIT_L(0); PG8_BAR; PG8_MMA(0, 0, At, B0); PG8_MMA(0, 1, At, B1); PG8_BAR; PG8_SCHED;
;             PG8_LDA(At, 0, 1); PG8_STAGE(PG8_SB(0, 0), b2, voffB); PG8_STAGE(PG8_SB(0, 1), b2 + hstep, voffB); PG8_STAGE(PG8_SA(0, 0), a2, voffA);
;             PG8_WAIT_V(8); PG8_WAIT_L(0); PG8_BAR; PG8_MMA(1, 0, At, B0); PG8_MMA(1, 1, At, B1); PG8_BAR; PG8_SCHED;
.LBB0_967:
	ds_read_b128 v[144:147], v151
	ds_read_b128 v[154:157], v151 offset:1024
	ds_read_b128 v[158:161], v151 offset:2048
	ds_read_b128 v[162:165], v151 offset:3072
	ds_read_b128 v[166:169], v152
	ds_read_b128 v[170:173], v152 offset:1024
	ds_read_b128 v[174:177], v152 offset:2048
	ds_read_b128 v[178:181], v152 offset:3072
	s_add_u32 s40, s38, 0xfffe0080
	s_addc_u32 s41, s39, -1
	s_cmp_eq_u32 s72, 4
	s_cselect_b32 s43, s5, s41
	s_cselect_b32 s42, s27, s40
	s_cselect_b32 s41, s23, s71
	s_cselect_b32 s40, s37, s70
	v_lshl_add_u64 v[148:149], s[38:39], 0, v[138:139]
	s_add_i32 m0, s51, 0xc000
	ds_read_b128 v[182:185], v153
	ds_read_b128 v[186:189], v153 offset:1024
	ds_read_b128 v[190:193], v153 offset:2048
	ds_read_b128 v[194:197], v153 offset:3072
	ds_read_b128 v[198:201], v153 offset:4096
	ds_read_b128 v[202:205], v153 offset:5120
	ds_read_b128 v[206:209], v153 offset:6144
	ds_read_b128 v[210:213], v153 offset:7168
	global_load_lds_dwordx4 v[148:149], off
	v_lshl_add_u64 v[148:149], s[38:39], 0, v[140:141]
	s_add_i32 m0, s51, 0xe000
	s_nop 0
	global_load_lds_dwordx4 v[148:149], off
	s_waitcnt vmcnt(8)
	s_waitcnt lgkmcnt(0)
	s_barrier
	s_waitcnt lgkmcnt(0)
	v_mfma_f32_16x16x32_bf16 v[124:127], v[144:147], v[182:185], v[124:127]
	v_mfma_f32_16x16x32_bf16 v[120:123], v[158:161], v[182:185], v[120:123]
	v_mfma_f32_16x16x32_bf16 v[108:111], v[144:147], v[190:193], v[108:111]
	v_mfma_f32_16x16x32_bf16 v[104:107], v[158:161], v[190:193], v[104:107]
	v_mfma_f32_16x16x32_bf16 v[92:95], v[144:147], v[198:201], v[92:95]
	v_mfma_f32_16x16x32_bf16 v[88:91], v[158:161], v[198:201], v[88:91]
	v_mfma_f32_16x16x32_bf16 v[76:79], v[144:147], v[206:209], v[76:79]
	v_mfma_f32_16x16x32_bf16 v[72:75], v[158:161], v[206:209], v[72:75]
	v_mfma_f32_16x16x32_bf16 v[124:127], v[154:157], v[186:189], v[124:127]
	v_mfma_f32_16x16x32_bf16 v[120:123], v[162:165], v[186:189], v[120:123]
	v_mfma_f32_16x16x32_bf16 v[108:111], v[154:157], v[194:197], v[108:111]
	v_mfma_f32_16x16x32_bf16 v[104:107], v[162:165], v[194:197], v[104:107]
	v_mfma_f32_16x16x32_bf16 v[92:95], v[154:157], v[202:205], v[92:95]
	v_mfma_f32_16x16x32_bf16 v[88:91], v[162:165], v[202:205], v[88:91]
	v_mfma_f32_16x16x32_bf16 v[76:79], v[154:157], v[210:213], v[76:79]
	v_mfma_f32_16x16x32_bf16 v[72:75], v[162:165], v[210:213], v[72:75]
	v_mfma_f32_16x16x32_bf16 v[116:119], v[166:169], v[182:185], v[116:119]
	v_mfma_f32_16x16x32_bf16 v[112:115], v[174:177], v[182:185], v[112:115]
	v_mfma_f32_16x16x32_bf16 v[100:103], v[166:169], v[190:193], v[100:103]
	v_mfma_f32_16x16x32_bf16 v[96:99], v[174:177], v[190:193], v[96:99]
	v_mfma_f32_16x16x32_bf16 v[84:87], v[166:169], v[198:201], v[84:87]
	v_mfma_f32_16x16x32_bf16 v[80:83], v[174:177], v[198:201], v[80:83]
	v_mfma_f32_16x16x32_bf16 v[68:71], v[166:169], v[206:209], v[68:71]
	v_mfma_f32_16x16x32_bf16 v[64:67], v[174:177], v[206:209], v[64:67]
	v_mfma_f32_16x16x32_bf16 v[116:119], v[170:173], v[186:189], v[116:119]
	v_mfma_f32_16x16x32_bf16 v[112:115], v[178:181], v[186:189], v[112:115]
	v_mfma_f32_16x16x32_bf16 v[100:103], v[170:173], v[194:197], v[100:103]
	v_mfma_f32_16x16x32_bf16 v[96:99], v[178:181], v[194:197], v[96:99]
	v_mfma_f32_16x16x32_bf16 v[84:87], v[170:173], v[202:205], v[84:87]
	v_mfma_f32_16x16x32_bf16 v[80:83], v[178:181], v[202:205], v[80:83]
	v_mfma_f32_16x16x32_bf16 v[68:71], v[170:173], v[210:213], v[68:71]
	v_mfma_f32_16x16x32_bf16 v[64:67], v[178:181], v[210:213], v[64:67]
	s_barrier
	s_add_i32 s73, s67, s48
	v_lshl_add_u64 v[148:149], s[40:41], 0, v[130:131]
	s_mov_b32 m0, s73
	ds_read_b128 v[182:185], v153 offset:16384
	ds_read_b128 v[186:189], v153 offset:17408
	ds_read_b128 v[190:193], v153 offset:18432
	ds_read_b128 v[194:197], v153 offset:19456
	ds_read_b128 v[198:201], v153 offset:20480
	ds_read_b128 v[202:205], v153 offset:21504
	ds_read_b128 v[206:209], v153 offset:22528
	ds_read_b128 v[210:213], v153 offset:23552
	global_load_lds_dwordx4 v[148:149], off
	s_add_i32 m0, s73, 0x2000
	s_add_u32 s74, s40, 0x20000
	v_lshl_add_u64 v[214:215], s[40:41], 0, v[134:135]
	s_addc_u32 s75, s41, 0
	s_add_i32 s73, s68, s48
	global_load_lds_dwordx4 v[214:215], off
	v_lshl_add_u64 v[216:217], s[74:75], 0, v[130:131]
	s_mov_b32 m0, s73
	v_lshl_add_u64 v[218:219], s[42:43], 0, v[132:133]
	global_load_lds_dwordx4 v[216:217], off
	v_lshl_add_u64 v[216:217], s[74:75], 0, v[134:135]
	s_add_i32 m0, s73, 0x2000
	s_nop 0
	global_load_lds_dwordx4 v[216:217], off
	v_lshl_add_u64 v[216:217], s[42:43], 0, v[128:129]
	s_mov_b32 m0, s51
	s_nop 0
	global_load_lds_dwordx4 v[216:217], off
	s_mov_b32 m0, s52
	s_nop 0
	global_load_lds_dwordx4 v[218:219], off
	s_waitcnt vmcnt(8)
	s_waitcnt lgkmcnt(0)
	s_barrier
; #define PG8_LDA(dst, b, h) do { _Pragma("unroll") for (int m = 0; m < 4; ++m) _Pragma("unroll") for (int k = 0; k < 2; ++k) dst[m][k] = *(const PG8_LAS bf16x8*)(lds + PG8_SA(b, h) + aoff + m * 2048 + k * 1024); } while (0)
; #define PG8_LDB(dst, b, h) do { _Pragma("unroll") for (int n = 0; n < 2; ++n) _Pragma("unroll") for (int k = 0; k < 2; ++k) dst[n][k] = *(const PG8_LAS bf16x8*)(lds + PG8_SB(b, h) + boff + n * 2048 + k * 1024); } while (0)
; #define PG8_WAIT_V(n) asm volatile("s_waitcnt vmcnt(" #n ")" ::: "memory")
; #define PG8_WAIT_L(n) asm volatile("s_waitcnt lgkmcnt(" #n ")" ::: "memory")
; #define PG8_BAR __builtin_amdgcn_s_barrier()
; #define PG8_SCHED __builtin_amdgcn_sched_barrier(0)
; template <class Epi, class Sched, bool ALIGN_EPI = false, bool SP2 = false, bool F8 = false, bool I8 = false, bool PF = false>
; __device__ __forceinline__ void gemm_phase(PG8_LAS unsigned char* lds, const Gemm g, const Sched& S, const Epi& E, const int wave_) {
;     ...
;             PG8_WAIT_V(8); PG8_WAIT_L(0); PG8_BAR; PG8_MMA(1, 0, At, B0); PG8_MMA(1, 1, At, B1); PG8_BAR; PG8_SCHED;
;             PG8_LDB(B0, 1, 0); PG8_LDB(B1, 1, 1); PG8_SCHED; PG8_LDA(At, 1, 0); PG8_STAGE(PG8_SA(0, 1), a2 + hstep, voffA);
;             PG8_WAIT_V(8); PG8_WAIT_L(0); PG8_BAR; PG8_MMA(0, 0, At, B0); PG8_MMA(0, 1, At, B1); PG8_BAR; PG8_SCHED;
	s_waitcnt lgkmcnt(0)
	v_mfma_f32_16x16x32_bf16 v[60:63], v[144:147], v[182:185], v[60:63]
	v_mfma_f32_16x16x32_bf16 v[56:59], v[158:161], v[182:185], v[56:59]
	v_mfma_f32_16x16x32_bf16 v[44:47], v[144:147], v[190:193], v[44:47]
	v_mfma_f32_16x16x32_bf16 v[40:43], v[158:161], v[190:193], v[40:43]
	v_mfma_f32_16x16x32_bf16 v[28:31], v[144:147], v[198:201], v[28:31]
	v_mfma_f32_16x16x32_bf16 v[24:27], v[158:161], v[198:201], v[24:27]
	v_mfma_f32_16x16x32_bf16 v[12:15], v[144:147], v[206:209], v[12:15]
	v_mfma_f32_16x16x32_bf16 v[8:11], v[158:161], v[206:209], v[8:11]
	v_mfma_f32_16x16x32_bf16 v[60:63], v[154:157], v[186:189], v[60:63]
	v_mfma_f32_16x16x32_bf16 v[56:59], v[162:165], v[186:189], v[56:59]
	v_mfma_f32_16x16x32_bf16 v[44:47], v[154:157], v[194:197], v[44:47]
	v_mfma_f32_16x16x32_bf16 v[40:43], v[162:165], v[194:197], v[40:43]
	v_mfma_f32_16x16x32_bf16 v[28:31], v[154:157], v[202:205], v[28:31]
	v_mfma_f32_16x16x32_bf16 v[24:27], v[162:165], v[202:205], v[24:27]
	v_mfma_f32_16x16x32_bf16 v[12:15], v[154:157], v[210:213], v[12:15]
	v_mfma_f32_16x16x32_bf16 v[8:11], v[162:165], v[210:213], v[8:11]
	v_mfma_f32_16x16x32_bf16 v[52:55], v[166:169], v[182:185], v[52:55]
	v_mfma_f32_16x16x32_bf16 v[48:51], v[174:177], v[182:185], v[48:51]
	v_mfma_f32_16x16x32_bf16 v[36:39], v[166:169], v[190:193], v[36:39]
	v_mfma_f32_16x16x32_bf16 v[32:35], v[174:177], v[190:193], v[32:35]
	v_mfma_f32_16x16x32_bf16 v[20:23], v[166:169], v[198:201], v[20:23]
	v_mfma_f32_16x16x32_bf16 v[16:19], v[174:177], v[198:201], v[16:19]
	v_mfma_f32_16x16x32_bf16 v[4:7], v[166:169], v[206:209], v[4:7]
	v_mfma_f32_16x16x32_bf16 v[0:3], v[174:177], v[206:209], v[0:3]
	v_mfma_f32_16x16x32_bf16 v[52:55], v[170:173], v[186:189], v[52:55]
	v_mfma_f32_16x16x32_bf16 v[48:51], v[178:181], v[186:189], v[48:51]
	v_mfma_f32_16x16x32_bf16 v[36:39], v[170:173], v[194:197], v[36:39]
	v_mfma_f32_16x16x32_bf16 v[32:35], v[178:181], v[194:197], v[32:35]
	v_mfma_f32_16x16x32_bf16 v[20:23], v[170:173], v[202:205], v[20:23]
	v_mfma_f32_16x16x32_bf16 v[16:19], v[178:181], v[202:205], v[16:19]
	v_mfma_f32_16x16x32_bf16 v[4:7], v[170:173], v[210:213], v[4:7]
	v_mfma_f32_16x16x32_bf16 v[0:3], v[178:181], v[210:213], v[0:3]
	s_barrier
	s_add_i32 s73, 0, 0x18000
	v_add_u32_e32 v136, s73, v150
	s_add_i32 s74, 0, 0x1c000
	ds_read_b128 v[144:147], v136
	ds_read_b128 v[154:157], v136 offset:1024
	ds_read_b128 v[158:161], v136 offset:2048
	ds_read_b128 v[162:165], v136 offset:3072
	v_add_u32_e32 v136, s74, v150
	ds_read_b128 v[166:169], v136
	ds_read_b128 v[170:173], v136 offset:1024
	ds_read_b128 v[174:177], v136 offset:2048
	ds_read_b128 v[178:181], v136 offset:3072
	s_add_u32 s42, s42, 0x20000
	s_addc_u32 s43, s43, 0
	s_mov_b32 m0, s53
	v_lshl_add_u64 v[220:221], s[42:43], 0, v[128:129]
	ds_read_b128 v[182:185], v153 offset:32768
	ds_read_b128 v[186:189], v153 offset:33792
	ds_read_b128 v[190:193], v153 offset:34816
	ds_read_b128 v[194:197], v153 offset:35840
	ds_read_b128 v[198:201], v153 offset:36864
	ds_read_b128 v[202:205], v153 offset:37888
	ds_read_b128 v[206:209], v153 offset:38912
	ds_read_b128 v[210:213], v153 offset:39936
	global_load_lds_dwordx4 v[220:221], off
	v_lshl_add_u64 v[220:221], s[42:43], 0, v[132:133]
	s_mov_b32 m0, s54
	s_nop 0
	global_load_lds_dwordx4 v[220:221], off
	s_waitcnt vmcnt(8)
	s_waitcnt lgkmcnt(0)
	s_barrier
	s_waitcnt lgkmcnt(0)
	v_mfma_f32_16x16x32_bf16 v[124:127], v[144:147], v[182:185], v[124:127]
	v_mfma_f32_16x16x32_bf16 v[120:123], v[158:161], v[182:185], v[120:123]
	v_mfma_f32_16x16x32_bf16 v[108:111], v[144:147], v[190:193], v[108:111]
	v_mfma_f32_16x16x32_bf16 v[104:107], v[158:161], v[190:193], v[104:107]
	v_mfma_f32_16x16x32_bf16 v[92:95], v[144:147], v[198:201], v[92:95]
	v_mfma_f32_16x16x32_bf16 v[88:91], v[158:161], v[198:201], v[88:91]
	v_mfma_f32_16x16x32_bf16 v[76:79], v[144:147], v[206:209], v[76:79]
	v_mfma_f32_16x16x32_bf16 v[72:75], v[158:161], v[206:209], v[72:75]
	v_mfma_f32_16x16x32_bf16 v[124:127], v[154:157], v[186:189], v[124:127]
	v_mfma_f32_16x16x32_bf16 v[120:123], v[162:165], v[186:189], v[120:123]
	v_mfma_f32_16x16x32_bf16 v[108:111], v[154:157], v[194:197], v[108:111]
	v_mfma_f32_16x16x32_bf16 v[104:107], v[162:165], v[194:197], v[104:107]
	v_mfma_f32_16x16x32_bf16 v[92:95], v[154:157], v[202:205], v[92:95]
	v_mfma_f32_16x16x32_bf16 v[88:91], v[162:165], v[202:205], v[88:91]
	v_mfma_f32_16x16x32_bf16 v[76:79], v[154:157], v[210:213], v[76:79]
	v_mfma_f32_16x16x32_bf16 v[72:75], v[162:165], v[210:213], v[72:75]
	v_mfma_f32_16x16x32_bf16 v[116:119], v[166:169], v[182:185], v[116:119]
	v_mfma_f32_16x16x32_bf16 v[112:115], v[174:177], v[182:185], v[112:115]
	v_mfma_f32_16x16x32_bf16 v[100:103], v[166:169], v[190:193], v[100:103]
	v_mfma_f32_16x16x32_bf16 v[96:99], v[174:177], v[190:193], v[96:99]
	v_mfma_f32_16x16x32_bf16 v[84:87], v[166:169], v[198:201], v[84:87]
	v_mfma_f32_16x16x32_bf16 v[80:83], v[174:177], v[198:201], v[80:83]
	v_mfma_f32_16x16x32_bf16 v[68:71], v[166:169], v[206:209], v[68:71]
	v_mfma_f32_16x16x32_bf16 v[64:67], v[174:177], v[206:209], v[64:67]
	v_mfma_f32_16x16x32_bf16 v[116:119], v[170:173], v[186:189], v[116:119]
	v_mfma_f32_16x16x32_bf16 v[112:115], v[178:181], v[186:189], v[112:115]
	v_mfma_f32_16x16x32_bf16 v[100:103], v[170:173], v[194:197], v[100:103]
	v_mfma_f32_16x16x32_bf16 v[96:99], v[178:181], v[194:197], v[96:99]
	v_mfma_f32_16x16x32_bf16 v[84:87], v[170:173], v[202:205], v[84:87]
	v_mfma_f32_16x16x32_bf16 v[80:83], v[178:181], v[202:205], v[80:83]
	v_mfma_f32_16x16x32_bf16 v[68:71], v[170:173], v[210:213], v[68:71]
	v_mfma_f32_16x16x32_bf16 v[64:67], v[178:181], v[210:213], v[64:67]
	s_barrier
; #define PG8_LDA(dst, b, h) do { _Pragma("unroll") for (int m = 0; m < 4; ++m) _Pragma("unroll") for (int k = 0; k < 2; ++k) dst[m][k] = *(const PG8_LAS bf16x8*)(lds + PG8_SA(b, h) + aoff + m * 2048 + k * 1024); } while (0)
; #define PG8_WAIT_V(n) asm volatile("s_waitcnt vmcnt(" #n ")" ::: "memory")
; #define PG8_WAIT_L(n) asm volatile("s_waitcnt lgkmcnt(" #n ")" ::: "memory")
; #define PG8_BAR __builtin_amdgcn_s_barrier()
; #define PG8_SCHED __builtin_amdgcn_sched_barrier(0)
; template <class Epi, class Sched, bool ALIGN_EPI = false, bool SP2 = false, bool F8 = false, bool I8 = false, bool PF = false>
; __device__ __forceinline__ void gemm_phase(PG8_LAS unsigned char* lds, const Gemm g, const Sched& S, const Epi& E, const int wave_) {
;     ...
;             PG8_LDA(At, 1, 1); PG8_STAGE(PG8_SB(1, 0), b3, voffB); PG8_STAGE(PG8_SB(1, 1), b3 + hstep, voffB); PG8_STAGE(PG8_SA(1, 0), a3, voffA);
;             PG8_WAIT_V(8); PG8_WAIT_L(0); PG8_BAR; PG8_MMA(1, 0, At, B0); PG8_MMA(1, 1, At, B1); PG8_BAR; PG8_SCHED;
	s_add_i32 s42, s73, s48
	v_lshl_add_u64 v[148:149], v[148:149], 0, s[16:17]
	s_mov_b32 m0, s42
	ds_read_b128 v[182:185], v153 offset:49152
	ds_read_b128 v[186:189], v153 offset:50176
	ds_read_b128 v[190:193], v153 offset:51200
	ds_read_b128 v[194:197], v153 offset:52224
	ds_read_b128 v[198:201], v153 offset:53248
	ds_read_b128 v[202:205], v153 offset:54272
	ds_read_b128 v[206:209], v153 offset:55296
	ds_read_b128 v[210:213], v153 offset:56320
	global_load_lds_dwordx4 v[148:149], off
	s_add_i32 m0, s42, 0x2000
	s_add_u32 s40, s40, 0x20080
	v_lshl_add_u64 v[148:149], v[214:215], 0, s[16:17]
	s_addc_u32 s41, s41, 0
	s_add_i32 s42, s74, s48
	global_load_lds_dwordx4 v[148:149], off
	v_lshl_add_u64 v[148:149], s[40:41], 0, v[130:131]
	s_mov_b32 m0, s42
	s_nop 0
	global_load_lds_dwordx4 v[148:149], off
	v_lshl_add_u64 v[148:149], s[40:41], 0, v[134:135]
	s_add_i32 m0, s42, 0x2000
	s_nop 0
	global_load_lds_dwordx4 v[148:149], off
	v_lshl_add_u64 v[148:149], v[216:217], 0, s[16:17]
	s_mov_b32 m0, s62
	s_nop 0
	global_load_lds_dwordx4 v[148:149], off
	v_lshl_add_u64 v[148:149], v[218:219], 0, s[16:17]
	s_mov_b32 m0, s63
	s_nop 0
	global_load_lds_dwordx4 v[148:149], off
	s_waitcnt vmcnt(8)
	s_waitcnt lgkmcnt(0)
	s_barrier
	s_waitcnt lgkmcnt(0)
	v_mfma_f32_16x16x32_bf16 v[60:63], v[144:147], v[182:185], v[60:63]
	v_mfma_f32_16x16x32_bf16 v[56:59], v[158:161], v[182:185], v[56:59]
	v_mfma_f32_16x16x32_bf16 v[44:47], v[144:147], v[190:193], v[44:47]
	v_mfma_f32_16x16x32_bf16 v[40:43], v[158:161], v[190:193], v[40:43]
	v_mfma_f32_16x16x32_bf16 v[28:31], v[144:147], v[198:201], v[28:31]
	v_mfma_f32_16x16x32_bf16 v[24:27], v[158:161], v[198:201], v[24:27]
	v_mfma_f32_16x16x32_bf16 v[12:15], v[144:147], v[206:209], v[12:15]
	v_mfma_f32_16x16x32_bf16 v[8:11], v[158:161], v[206:209], v[8:11]
	v_mfma_f32_16x16x32_bf16 v[60:63], v[154:157], v[186:189], v[60:63]
	v_mfma_f32_16x16x32_bf16 v[56:59], v[162:165], v[186:189], v[56:59]
	v_mfma_f32_16x16x32_bf16 v[44:47], v[154:157], v[194:197], v[44:47]
	v_mfma_f32_16x16x32_bf16 v[40:43], v[162:165], v[194:197], v[40:43]
	v_mfma_f32_16x16x32_bf16 v[28:31], v[154:157], v[202:205], v[28:31]
	v_mfma_f32_16x16x32_bf16 v[24:27], v[162:165], v[202:205], v[24:27]
	v_mfma_f32_16x16x32_bf16 v[12:15], v[154:157], v[210:213], v[12:15]
	v_mfma_f32_16x16x32_bf16 v[8:11], v[162:165], v[210:213], v[8:11]
	v_mfma_f32_16x16x32_bf16 v[52:55], v[166:169], v[182:185], v[52:55]
	v_mfma_f32_16x16x32_bf16 v[48:51], v[174:177], v[182:185], v[48:51]
	v_mfma_f32_16x16x32_bf16 v[36:39], v[166:169], v[190:193], v[36:39]
	v_mfma_f32_16x16x32_bf16 v[32:35], v[174:177], v[190:193], v[32:35]
	v_mfma_f32_16x16x32_bf16 v[20:23], v[166:169], v[198:201], v[20:23]
	v_mfma_f32_16x16x32_bf16 v[16:19], v[174:177], v[198:201], v[16:19]
	v_mfma_f32_16x16x32_bf16 v[4:7], v[166:169], v[206:209], v[4:7]
	v_mfma_f32_16x16x32_bf16 v[0:3], v[174:177], v[206:209], v[0:3]
	v_mfma_f32_16x16x32_bf16 v[52:55], v[170:173], v[186:189], v[52:55]
	v_mfma_f32_16x16x32_bf16 v[48:51], v[178:181], v[186:189], v[48:51]
	v_mfma_f32_16x16x32_bf16 v[36:39], v[170:173], v[194:197], v[36:39]
	v_mfma_f32_16x16x32_bf16 v[32:35], v[178:181], v[194:197], v[32:35]
	v_mfma_f32_16x16x32_bf16 v[20:23], v[170:173], v[202:205], v[20:23]
	v_mfma_f32_16x16x32_bf16 v[16:19], v[178:181], v[202:205], v[16:19]
	v_mfma_f32_16x16x32_bf16 v[4:7], v[170:173], v[210:213], v[4:7]
	v_mfma_f32_16x16x32_bf16 v[0:3], v[178:181], v[210:213], v[0:3]
	s_barrier
	s_add_i32 s72, s72, 2
	s_add_u32 s38, s38, 0x100
	s_addc_u32 s39, s39, 0
	s_add_u32 s70, s70, 0x100
	s_addc_u32 s71, s71, 0
	s_cmp_gt_u32 s72, 5
	s_cbranch_scc0 .LBB0_967
	s_and_b64 vcc, exec, s[18:19]
	s_cbranch_vccz .LBB0_970
	s_barrier

; #define PG8_LDA(dst, b, h) do { _Pragma("unroll") for (int m = 0; m < 4; ++m) _Pragma("unroll") for (int k = 0; k < 2; ++k) dst[m][k] = *(const PG8_LAS bf16x8*)(lds + PG8_SA(b, h) + aoff + m * 2048 + k * 1024); } while (0)
; #define PG8_LDB(dst, b, h) do { _Pragma("unroll") for (int n = 0; n < 2; ++n) _Pragma("unroll") for (int k = 0; k < 2; ++k) dst[n][k] = *(const PG8_LAS bf16x8*)(lds + PG8_SB(b, h) + boff + n * 2048 + k * 1024); } while (0)
; #define PG8_WAIT_V(n) asm volatile("s_waitcnt vmcnt(" #n ")" ::: "memory")
; #define PG8_WAIT_L(n) asm volatile("s_waitcnt lgkmcnt(" #n ")" ::: "memory")
; #define PG8_BAR __builtin_amdgcn_s_barrier()
; #define PG8_SCHED __builtin_amdgcn_sched_barrier(0)
; template <class Epi, class Sched, bool ALIGN_EPI = false, bool SP2 = false, bool F8 = false, bool I8 = false, bool PF = false>
; __device__ __forceinline__ void gemm_phase(PG8_LAS unsigned char* lds, const Gemm g, const Sched& S, const Epi& E, const int wave_) {
;     ...
;             PG8_LDB(B0, 0, 0); PG8_LDB(B1, 0, 1); PG8_SCHED; PG8_LDA(At, 0, 0); PG8_STAGE(PG8_SA(1, 1), a1 + hstep, voffA);
;             PG8_WAIT_V(8); PG8_WAIT_L(0); PG8_BAR; PG8_MMA(0, 0, At, B0); PG8_MMA(0, 1, At, B1); PG8_BAR; PG8_SCHED;
;             PG8_LDA(At, 0, 1); PG8_STAGE(PG8_SB(0, 0), b2, voffB); PG8_STAGE(PG8_SB(0, 1), b2 + hstep, voffB); PG8_STAGE(PG8_SA(0, 0), a2, voffA);
;             PG8_WAIT_V(8); PG8_WAIT_L(0); PG8_BAR; PG8_MMA(1, 0, At, B0); PG8_MMA(1, 1, At, B1); PG8_BAR; PG8_SCHED;
.LBB0_1304:
	ds_read_b128 v[128:131], v209
	ds_read_b128 v[132:135], v209 offset:1024
	ds_read_b128 v[136:139], v209 offset:2048
	ds_read_b128 v[140:143], v209 offset:3072
	ds_read_b128 v[144:147], v210
	ds_read_b128 v[148:151], v210 offset:1024
	ds_read_b128 v[152:155], v210 offset:2048
	ds_read_b128 v[156:159], v210 offset:3072
	s_add_u32 s34, s30, 0xfffc0080
	s_addc_u32 s35, s31, -1
	s_cmp_eq_u32 s66, 12
	s_cselect_b32 s37, s21, s35
	s_cselect_b32 s36, s62, s34
	s_cselect_b32 s35, s19, s65
	s_cselect_b32 s34, s63, s64
	v_lshl_add_u64 v[206:207], s[30:31], 0, v[188:189]
	s_add_i32 m0, s29, 0xc000
	ds_read_b128 v[160:163], v211
	ds_read_b128 v[164:167], v211 offset:1024
	ds_read_b128 v[168:171], v211 offset:2048
	ds_read_b128 v[172:175], v211 offset:3072
	ds_read_b128 v[176:179], v211 offset:4096
	ds_read_b128 v[194:197], v211 offset:5120
	ds_read_b128 v[198:201], v211 offset:6144
	ds_read_b128 v[202:205], v211 offset:7168
	global_load_lds_dwordx4 v[206:207], off
	v_lshl_add_u64 v[206:207], s[30:31], 0, v[190:191]
	s_add_i32 m0, s29, 0xe000
	s_nop 0
	global_load_lds_dwordx4 v[206:207], off
	s_waitcnt vmcnt(8)
	s_waitcnt lgkmcnt(0)
	s_barrier
	s_waitcnt lgkmcnt(0)
	v_mfma_f32_16x16x32_bf16 v[124:127], v[128:131], v[160:163], v[124:127]
	v_mfma_f32_16x16x32_bf16 v[120:123], v[136:139], v[160:163], v[120:123]
	v_mfma_f32_16x16x32_bf16 v[108:111], v[128:131], v[168:171], v[108:111]
	v_mfma_f32_16x16x32_bf16 v[104:107], v[136:139], v[168:171], v[104:107]
	v_mfma_f32_16x16x32_bf16 v[92:95], v[128:131], v[176:179], v[92:95]
	v_mfma_f32_16x16x32_bf16 v[88:91], v[136:139], v[176:179], v[88:91]
	v_mfma_f32_16x16x32_bf16 v[76:79], v[128:131], v[198:201], v[76:79]
	v_mfma_f32_16x16x32_bf16 v[72:75], v[136:139], v[198:201], v[72:75]
	v_mfma_f32_16x16x32_bf16 v[124:127], v[132:135], v[164:167], v[124:127]
	v_mfma_f32_16x16x32_bf16 v[120:123], v[140:143], v[164:167], v[120:123]
	v_mfma_f32_16x16x32_bf16 v[108:111], v[132:135], v[172:175], v[108:111]
	v_mfma_f32_16x16x32_bf16 v[104:107], v[140:143], v[172:175], v[104:107]
	v_mfma_f32_16x16x32_bf16 v[92:95], v[132:135], v[194:197], v[92:95]
	v_mfma_f32_16x16x32_bf16 v[88:91], v[140:143], v[194:197], v[88:91]
	v_mfma_f32_16x16x32_bf16 v[76:79], v[132:135], v[202:205], v[76:79]
	v_mfma_f32_16x16x32_bf16 v[72:75], v[140:143], v[202:205], v[72:75]
	v_mfma_f32_16x16x32_bf16 v[116:119], v[144:147], v[160:163], v[116:119]
	v_mfma_f32_16x16x32_bf16 v[112:115], v[152:155], v[160:163], v[112:115]
	v_mfma_f32_16x16x32_bf16 v[100:103], v[144:147], v[168:171], v[100:103]
	v_mfma_f32_16x16x32_bf16 v[96:99], v[152:155], v[168:171], v[96:99]
	v_mfma_f32_16x16x32_bf16 v[84:87], v[144:147], v[176:179], v[84:87]
	v_mfma_f32_16x16x32_bf16 v[80:83], v[152:155], v[176:179], v[80:83]
	v_mfma_f32_16x16x32_bf16 v[68:71], v[144:147], v[198:201], v[68:71]
	v_mfma_f32_16x16x32_bf16 v[64:67], v[152:155], v[198:201], v[64:67]
	v_mfma_f32_16x16x32_bf16 v[116:119], v[148:151], v[164:167], v[116:119]
	v_mfma_f32_16x16x32_bf16 v[112:115], v[156:159], v[164:167], v[112:115]
	v_mfma_f32_16x16x32_bf16 v[100:103], v[148:151], v[172:175], v[100:103]
	v_mfma_f32_16x16x32_bf16 v[96:99], v[156:159], v[172:175], v[96:99]
	v_mfma_f32_16x16x32_bf16 v[84:87], v[148:151], v[194:197], v[84:87]
	v_mfma_f32_16x16x32_bf16 v[80:83], v[156:159], v[194:197], v[80:83]
	v_mfma_f32_16x16x32_bf16 v[68:71], v[148:151], v[202:205], v[68:71]
	v_mfma_f32_16x16x32_bf16 v[64:67], v[156:159], v[202:205], v[64:67]
	s_barrier
	s_add_i32 s67, s55, s40
	v_lshl_add_u64 v[206:207], s[34:35], 0, v[184:185]
	s_mov_b32 m0, s67
	ds_read_b128 v[160:163], v211 offset:16384
	ds_read_b128 v[164:167], v211 offset:17408
	ds_read_b128 v[168:171], v211 offset:18432
	ds_read_b128 v[172:175], v211 offset:19456
	ds_read_b128 v[176:179], v211 offset:20480
	ds_read_b128 v[194:197], v211 offset:21504
	ds_read_b128 v[198:201], v211 offset:22528
	ds_read_b128 v[202:205], v211 offset:23552
	global_load_lds_dwordx4 v[206:207], off
	s_add_i32 m0, s67, 0x2000
	s_add_u32 s68, s34, 0x40000
	v_lshl_add_u64 v[212:213], s[34:35], 0, v[180:181]
	s_addc_u32 s69, s35, 0
	s_add_i32 s67, s56, s40
	global_load_lds_dwordx4 v[212:213], off
	v_lshl_add_u64 v[214:215], s[68:69], 0, v[184:185]
	s_mov_b32 m0, s67
	v_lshl_add_u64 v[216:217], s[36:37], 0, v[182:183]
	global_load_lds_dwordx4 v[214:215], off
	v_lshl_add_u64 v[214:215], s[68:69], 0, v[180:181]
	s_add_i32 m0, s67, 0x2000
	s_nop 0
	global_load_lds_dwordx4 v[214:215], off
	v_lshl_add_u64 v[214:215], s[36:37], 0, v[186:187]
	s_mov_b32 m0, s29
	s_nop 0
	global_load_lds_dwordx4 v[214:215], off
	s_mov_b32 m0, s41
	s_nop 0
	global_load_lds_dwordx4 v[216:217], off
	s_waitcnt vmcnt(8)
	s_waitcnt lgkmcnt(0)
	s_barrier
; #define PG8_LDA(dst, b, h) do { _Pragma("unroll") for (int m = 0; m < 4; ++m) _Pragma("unroll") for (int k = 0; k < 2; ++k) dst[m][k] = *(const PG8_LAS bf16x8*)(lds + PG8_SA(b, h) + aoff + m * 2048 + k * 1024); } while (0)
; #define PG8_LDB(dst, b, h) do { _Pragma("unroll") for (int n = 0; n < 2; ++n) _Pragma("unroll") for (int k = 0; k < 2; ++k) dst[n][k] = *(const PG8_LAS bf16x8*)(lds + PG8_SB(b, h) + boff + n * 2048 + k * 1024); } while (0)
; #define PG8_WAIT_V(n) asm volatile("s_waitcnt vmcnt(" #n ")" ::: "memory")
; #define PG8_WAIT_L(n) asm volatile("s_waitcnt lgkmcnt(" #n ")" ::: "memory")
; #define PG8_BAR __builtin_amdgcn_s_barrier()
; #define PG8_SCHED __builtin_amdgcn_sched_barrier(0)
; template <class Epi, class Sched, bool ALIGN_EPI = false, bool SP2 = false, bool F8 = false, bool I8 = false, bool PF = false>
; __device__ __forceinline__ void gemm_phase(PG8_LAS unsigned char* lds, const Gemm g, const Sched& S, const Epi& E, const int wave_) {
;     ...
;             PG8_WAIT_V(8); PG8_WAIT_L(0); PG8_BAR; PG8_MMA(1, 0, At, B0); PG8_MMA(1, 1, At, B1); PG8_BAR; PG8_SCHED;
;             PG8_LDB(B0, 1, 0); PG8_LDB(B1, 1, 1); PG8_SCHED; PG8_LDA(At, 1, 0); PG8_STAGE(PG8_SA(0, 1), a2 + hstep, voffA);
;             PG8_WAIT_V(8); PG8_WAIT_L(0); PG8_BAR; PG8_MMA(0, 0, At, B0); PG8_MMA(0, 1, At, B1); PG8_BAR; PG8_SCHED;
	s_waitcnt lgkmcnt(0)
	v_mfma_f32_16x16x32_bf16 v[60:63], v[128:131], v[160:163], v[60:63]
	v_mfma_f32_16x16x32_bf16 v[56:59], v[136:139], v[160:163], v[56:59]
	v_mfma_f32_16x16x32_bf16 v[44:47], v[128:131], v[168:171], v[44:47]
	v_mfma_f32_16x16x32_bf16 v[40:43], v[136:139], v[168:171], v[40:43]
	v_mfma_f32_16x16x32_bf16 v[28:31], v[128:131], v[176:179], v[28:31]
	v_mfma_f32_16x16x32_bf16 v[24:27], v[136:139], v[176:179], v[24:27]
	v_mfma_f32_16x16x32_bf16 v[12:15], v[128:131], v[198:201], v[12:15]
	v_mfma_f32_16x16x32_bf16 v[8:11], v[136:139], v[198:201], v[8:11]
	v_mfma_f32_16x16x32_bf16 v[60:63], v[132:135], v[164:167], v[60:63]
	v_mfma_f32_16x16x32_bf16 v[56:59], v[140:143], v[164:167], v[56:59]
	v_mfma_f32_16x16x32_bf16 v[44:47], v[132:135], v[172:175], v[44:47]
	v_mfma_f32_16x16x32_bf16 v[40:43], v[140:143], v[172:175], v[40:43]
	v_mfma_f32_16x16x32_bf16 v[28:31], v[132:135], v[194:197], v[28:31]
	v_mfma_f32_16x16x32_bf16 v[24:27], v[140:143], v[194:197], v[24:27]
	v_mfma_f32_16x16x32_bf16 v[12:15], v[132:135], v[202:205], v[12:15]
	v_mfma_f32_16x16x32_bf16 v[8:11], v[140:143], v[202:205], v[8:11]
	v_mfma_f32_16x16x32_bf16 v[52:55], v[144:147], v[160:163], v[52:55]
	v_mfma_f32_16x16x32_bf16 v[48:51], v[152:155], v[160:163], v[48:51]
	v_mfma_f32_16x16x32_bf16 v[36:39], v[144:147], v[168:171], v[36:39]
	v_mfma_f32_16x16x32_bf16 v[32:35], v[152:155], v[168:171], v[32:35]
	v_mfma_f32_16x16x32_bf16 v[20:23], v[144:147], v[176:179], v[20:23]
	v_mfma_f32_16x16x32_bf16 v[16:19], v[152:155], v[176:179], v[16:19]
	v_mfma_f32_16x16x32_bf16 v[4:7], v[144:147], v[198:201], v[4:7]
	v_mfma_f32_16x16x32_bf16 v[0:3], v[152:155], v[198:201], v[0:3]
	v_mfma_f32_16x16x32_bf16 v[52:55], v[148:151], v[164:167], v[52:55]
	v_mfma_f32_16x16x32_bf16 v[48:51], v[156:159], v[164:167], v[48:51]
	v_mfma_f32_16x16x32_bf16 v[36:39], v[148:151], v[172:175], v[36:39]
	v_mfma_f32_16x16x32_bf16 v[32:35], v[156:159], v[172:175], v[32:35]
	v_mfma_f32_16x16x32_bf16 v[20:23], v[148:151], v[194:197], v[20:23]
	v_mfma_f32_16x16x32_bf16 v[16:19], v[156:159], v[194:197], v[16:19]
	v_mfma_f32_16x16x32_bf16 v[4:7], v[148:151], v[202:205], v[4:7]
	v_mfma_f32_16x16x32_bf16 v[0:3], v[156:159], v[202:205], v[0:3]
	s_barrier
	s_add_i32 s67, 0, 0x18000
	s_add_i32 s68, 0, 0x1c000
	v_add_u32_e32 v140, s67, v208
	v_add_u32_e32 v156, s68, v208
	ds_read_b128 v[128:131], v140
	ds_read_b128 v[132:135], v140 offset:1024
	ds_read_b128 v[136:139], v140 offset:2048
	ds_read_b128 v[140:143], v140 offset:3072
	ds_read_b128 v[144:147], v156
	ds_read_b128 v[148:151], v156 offset:1024
	ds_read_b128 v[152:155], v156 offset:2048
	ds_read_b128 v[156:159], v156 offset:3072
	s_add_u32 s36, s36, 0x40000
	s_addc_u32 s37, s37, 0
	s_mov_b32 m0, s42
	v_lshl_add_u64 v[218:219], s[36:37], 0, v[186:187]
	ds_read_b128 v[160:163], v211 offset:32768
	ds_read_b128 v[164:167], v211 offset:33792
	ds_read_b128 v[168:171], v211 offset:34816
	ds_read_b128 v[172:175], v211 offset:35840
	ds_read_b128 v[176:179], v211 offset:36864
	ds_read_b128 v[194:197], v211 offset:37888
	ds_read_b128 v[198:201], v211 offset:38912
	ds_read_b128 v[202:205], v211 offset:39936
	global_load_lds_dwordx4 v[218:219], off
	v_lshl_add_u64 v[218:219], s[36:37], 0, v[182:183]
	s_mov_b32 m0, s43
	s_nop 0
	global_load_lds_dwordx4 v[218:219], off
	s_waitcnt vmcnt(8)
	s_waitcnt lgkmcnt(0)
	s_barrier
	s_waitcnt lgkmcnt(0)
	v_mfma_f32_16x16x32_bf16 v[124:127], v[128:131], v[160:163], v[124:127]
	v_mfma_f32_16x16x32_bf16 v[120:123], v[136:139], v[160:163], v[120:123]
	v_mfma_f32_16x16x32_bf16 v[108:111], v[128:131], v[168:171], v[108:111]
	v_mfma_f32_16x16x32_bf16 v[104:107], v[136:139], v[168:171], v[104:107]
	v_mfma_f32_16x16x32_bf16 v[92:95], v[128:131], v[176:179], v[92:95]
	v_mfma_f32_16x16x32_bf16 v[88:91], v[136:139], v[176:179], v[88:91]
	v_mfma_f32_16x16x32_bf16 v[76:79], v[128:131], v[198:201], v[76:79]
	v_mfma_f32_16x16x32_bf16 v[72:75], v[136:139], v[198:201], v[72:75]
	v_mfma_f32_16x16x32_bf16 v[124:127], v[132:135], v[164:167], v[124:127]
	v_mfma_f32_16x16x32_bf16 v[120:123], v[140:143], v[164:167], v[120:123]
	v_mfma_f32_16x16x32_bf16 v[108:111], v[132:135], v[172:175], v[108:111]
	v_mfma_f32_16x16x32_bf16 v[104:107], v[140:143], v[172:175], v[104:107]
	v_mfma_f32_16x16x32_bf16 v[92:95], v[132:135], v[194:197], v[92:95]
	v_mfma_f32_16x16x32_bf16 v[88:91], v[140:143], v[194:197], v[88:91]
	v_mfma_f32_16x16x32_bf16 v[76:79], v[132:135], v[202:205], v[76:79]
	v_mfma_f32_16x16x32_bf16 v[72:75], v[140:143], v[202:205], v[72:75]
	v_mfma_f32_16x16x32_bf16 v[116:119], v[144:147], v[160:163], v[116:119]
	v_mfma_f32_16x16x32_bf16 v[112:115], v[152:155], v[160:163], v[112:115]
	v_mfma_f32_16x16x32_bf16 v[100:103], v[144:147], v[168:171], v[100:103]
	v_mfma_f32_16x16x32_bf16 v[96:99], v[152:155], v[168:171], v[96:99]
	v_mfma_f32_16x16x32_bf16 v[84:87], v[144:147], v[176:179], v[84:87]
	v_mfma_f32_16x16x32_bf16 v[80:83], v[152:155], v[176:179], v[80:83]
	v_mfma_f32_16x16x32_bf16 v[68:71], v[144:147], v[198:201], v[68:71]
	v_mfma_f32_16x16x32_bf16 v[64:67], v[152:155], v[198:201], v[64:67]
	v_mfma_f32_16x16x32_bf16 v[116:119], v[148:151], v[164:167], v[116:119]
	v_mfma_f32_16x16x32_bf16 v[112:115], v[156:159], v[164:167], v[112:115]
	v_mfma_f32_16x16x32_bf16 v[100:103], v[148:151], v[172:175], v[100:103]
	v_mfma_f32_16x16x32_bf16 v[96:99], v[156:159], v[172:175], v[96:99]
	v_mfma_f32_16x16x32_bf16 v[84:87], v[148:151], v[194:197], v[84:87]
	v_mfma_f32_16x16x32_bf16 v[80:83], v[156:159], v[194:197], v[80:83]
	v_mfma_f32_16x16x32_bf16 v[68:71], v[148:151], v[202:205], v[68:71]
	v_mfma_f32_16x16x32_bf16 v[64:67], v[156:159], v[202:205], v[64:67]
	s_barrier
; #define PG8_LDA(dst, b, h) do { _Pragma("unroll") for (int m = 0; m < 4; ++m) _Pragma("unroll") for (int k = 0; k < 2; ++k) dst[m][k] = *(const PG8_LAS bf16x8*)(lds + PG8_SA(b, h) + aoff + m * 2048 + k * 1024); } while (0)
; #define PG8_WAIT_V(n) asm volatile("s_waitcnt vmcnt(" #n ")" ::: "memory")
; #define PG8_WAIT_L(n) asm volatile("s_waitcnt lgkmcnt(" #n ")" ::: "memory")
; #define PG8_BAR __builtin_amdgcn_s_barrier()
; #define PG8_SCHED __builtin_amdgcn_sched_barrier(0)
; template <class Epi, class Sched, bool ALIGN_EPI = false, bool SP2 = false, bool F8 = false, bool I8 = false, bool PF = false>
; __device__ __forceinline__ void gemm_phase(PG8_LAS unsigned char* lds, const Gemm g, const Sched& S, const Epi& E, const int wave_) {
;     ...
;             PG8_LDA(At, 1, 1); PG8_STAGE(PG8_SB(1, 0), b3, voffB); PG8_STAGE(PG8_SB(1, 1), b3 + hstep, voffB); PG8_STAGE(PG8_SA(1, 0), a3, voffA);
;             PG8_WAIT_V(8); PG8_WAIT_L(0); PG8_BAR; PG8_MMA(1, 0, At, B0); PG8_MMA(1, 1, At, B1); PG8_BAR; PG8_SCHED;
	s_add_i32 s36, s67, s40
	v_lshl_add_u64 v[206:207], v[206:207], 0, s[8:9]
	s_mov_b32 m0, s36
	ds_read_b128 v[160:163], v211 offset:49152
	ds_read_b128 v[164:167], v211 offset:50176
	ds_read_b128 v[168:171], v211 offset:51200
	ds_read_b128 v[172:175], v211 offset:52224
	ds_read_b128 v[176:179], v211 offset:53248
	ds_read_b128 v[194:197], v211 offset:54272
	ds_read_b128 v[198:201], v211 offset:55296
	ds_read_b128 v[202:205], v211 offset:56320
	global_load_lds_dwordx4 v[206:207], off
	s_add_i32 m0, s36, 0x2000
	s_add_u32 s34, s34, 0x40080
	v_lshl_add_u64 v[206:207], v[212:213], 0, s[8:9]
	s_addc_u32 s35, s35, 0
	s_add_i32 s36, s68, s40
	global_load_lds_dwordx4 v[206:207], off
	v_lshl_add_u64 v[206:207], s[34:35], 0, v[184:185]
	s_mov_b32 m0, s36
	s_nop 0
	global_load_lds_dwordx4 v[206:207], off
	v_lshl_add_u64 v[206:207], s[34:35], 0, v[180:181]
	s_add_i32 m0, s36, 0x2000
	s_nop 0
	global_load_lds_dwordx4 v[206:207], off
	v_lshl_add_u64 v[206:207], v[214:215], 0, s[8:9]
	s_mov_b32 m0, s52
	s_nop 0
	global_load_lds_dwordx4 v[206:207], off
	v_lshl_add_u64 v[206:207], v[216:217], 0, s[8:9]
	s_mov_b32 m0, s53
	s_nop 0
	global_load_lds_dwordx4 v[206:207], off
	s_waitcnt vmcnt(8)
	s_waitcnt lgkmcnt(0)
	s_barrier
	s_waitcnt lgkmcnt(0)
	v_mfma_f32_16x16x32_bf16 v[60:63], v[128:131], v[160:163], v[60:63]
	v_mfma_f32_16x16x32_bf16 v[56:59], v[136:139], v[160:163], v[56:59]
	v_mfma_f32_16x16x32_bf16 v[44:47], v[128:131], v[168:171], v[44:47]
	v_mfma_f32_16x16x32_bf16 v[40:43], v[136:139], v[168:171], v[40:43]
	v_mfma_f32_16x16x32_bf16 v[28:31], v[128:131], v[176:179], v[28:31]
	v_mfma_f32_16x16x32_bf16 v[24:27], v[136:139], v[176:179], v[24:27]
	v_mfma_f32_16x16x32_bf16 v[12:15], v[128:131], v[198:201], v[12:15]
	v_mfma_f32_16x16x32_bf16 v[8:11], v[136:139], v[198:201], v[8:11]
	v_mfma_f32_16x16x32_bf16 v[60:63], v[132:135], v[164:167], v[60:63]
	v_mfma_f32_16x16x32_bf16 v[56:59], v[140:143], v[164:167], v[56:59]
	v_mfma_f32_16x16x32_bf16 v[44:47], v[132:135], v[172:175], v[44:47]
	v_mfma_f32_16x16x32_bf16 v[40:43], v[140:143], v[172:175], v[40:43]
	v_mfma_f32_16x16x32_bf16 v[28:31], v[132:135], v[194:197], v[28:31]
	v_mfma_f32_16x16x32_bf16 v[24:27], v[140:143], v[194:197], v[24:27]
	v_mfma_f32_16x16x32_bf16 v[12:15], v[132:135], v[202:205], v[12:15]
	v_mfma_f32_16x16x32_bf16 v[8:11], v[140:143], v[202:205], v[8:11]
	v_mfma_f32_16x16x32_bf16 v[52:55], v[144:147], v[160:163], v[52:55]
	v_mfma_f32_16x16x32_bf16 v[48:51], v[152:155], v[160:163], v[48:51]
	v_mfma_f32_16x16x32_bf16 v[36:39], v[144:147], v[168:171], v[36:39]
	v_mfma_f32_16x16x32_bf16 v[32:35], v[152:155], v[168:171], v[32:35]
	v_mfma_f32_16x16x32_bf16 v[20:23], v[144:147], v[176:179], v[20:23]
	v_mfma_f32_16x16x32_bf16 v[16:19], v[152:155], v[176:179], v[16:19]
	v_mfma_f32_16x16x32_bf16 v[4:7], v[144:147], v[198:201], v[4:7]
	v_mfma_f32_16x16x32_bf16 v[0:3], v[152:155], v[198:201], v[0:3]
	v_mfma_f32_16x16x32_bf16 v[52:55], v[148:151], v[164:167], v[52:55]
	v_mfma_f32_16x16x32_bf16 v[48:51], v[156:159], v[164:167], v[48:51]
	v_mfma_f32_16x16x32_bf16 v[36:39], v[148:151], v[172:175], v[36:39]
	v_mfma_f32_16x16x32_bf16 v[32:35], v[156:159], v[172:175], v[32:35]
	v_mfma_f32_16x16x32_bf16 v[20:23], v[148:151], v[194:197], v[20:23]
	v_mfma_f32_16x16x32_bf16 v[16:19], v[156:159], v[194:197], v[16:19]
	v_mfma_f32_16x16x32_bf16 v[4:7], v[148:151], v[202:205], v[4:7]
	v_mfma_f32_16x16x32_bf16 v[0:3], v[156:159], v[202:205], v[0:3]
	s_barrier
	s_add_i32 s66, s66, 2
	s_add_u32 s30, s30, 0x100
	s_addc_u32 s31, s31, 0
	s_add_u32 s64, s64, 0x100
	s_addc_u32 s65, s65, 0
	s_cmp_gt_u32 s66, 13
	s_cbranch_scc0 .LBB0_1304
	s_and_b64 vcc, exec, s[10:11]
	s_cbranch_vccz .LBB0_1307
	s_barrier

; #define PG8_LDA(dst, b, h) do { _Pragma("unroll") for (int m = 0; m < 4; ++m) _Pragma("unroll") for (int k = 0; k < 2; ++k) dst[m][k] = *(const PG8_LAS bf16x8*)(lds + PG8_SA(b, h) + aoff + m * 2048 + k * 1024); } while (0)
; #define PG8_LDB(dst, b, h) do { _Pragma("unroll") for (int n = 0; n < 2; ++n) _Pragma("unroll") for (int k = 0; k < 2; ++k) dst[n][k] = *(const PG8_LAS bf16x8*)(lds + PG8_SB(b, h) + boff + n * 2048 + k * 1024); } while (0)
; #define PG8_WAIT_V(n) asm volatile("s_waitcnt vmcnt(" #n ")" ::: "memory")
; #define PG8_WAIT_L(n) asm volatile("s_waitcnt lgkmcnt(" #n ")" ::: "memory")
; #define PG8_BAR __builtin_amdgcn_s_barrier()
; #define PG8_SCHED __builtin_amdgcn_sched_barrier(0)
; template <class Epi, class Sched, bool ALIGN_EPI = false, bool SP2 = false, bool F8 = false, bool I8 = false, bool PF = false>
; __device__ __forceinline__ void gemm_phase(PG8_LAS unsigned char* lds, const Gemm g, const Sched& S, const Epi& E, const int wave_) {
;     ...
;             PG8_LDB(B0, 0, 0); PG8_LDB(B1, 0, 1); PG8_SCHED; PG8_LDA(At, 0, 0); PG8_STAGE(PG8_SA(1, 1), a1 + hstep, voffA);
;             PG8_WAIT_V(8); PG8_WAIT_L(0); PG8_BAR; PG8_MMA(0, 0, At, B0); PG8_MMA(0, 1, At, B1); PG8_BAR; PG8_SCHED;
;             PG8_LDA(At, 0, 1); PG8_STAGE(PG8_SB(0, 0), b2, voffB); PG8_STAGE(PG8_SB(0, 1), b2 + hstep, voffB); PG8_STAGE(PG8_SA(0, 0), a2, voffA);
;             PG8_WAIT_V(8); PG8_WAIT_L(0); PG8_BAR; PG8_MMA(1, 0, At, B0); PG8_MMA(1, 1, At, B1); PG8_BAR; PG8_SCHED;
.LBB0_1540:
	ds_read_b128 v[24:27], v181
	ds_read_b128 v[28:31], v181 offset:1024
	ds_read_b128 v[16:19], v181 offset:2048
	ds_read_b128 v[20:23], v181 offset:3072
	ds_read_b128 v[8:11], v182
	ds_read_b128 v[12:15], v182 offset:1024
	ds_read_b128 v[0:3], v182 offset:2048
	ds_read_b128 v[4:7], v182 offset:3072
	s_add_u32 s34, s30, 0xfffe0080
	s_addc_u32 s35, s31, -1
	s_cmp_eq_u32 s74, 4
	s_cselect_b32 s37, s19, s35
	s_cselect_b32 s36, s21, s34
	s_cselect_b32 s35, s17, s73
	s_cselect_b32 s34, s71, s72
	v_lshl_add_u64 v[210:211], s[30:31], 0, v[168:169]
	s_add_i32 m0, s29, 0xc000
	ds_read_b128 v[172:175], v183
	ds_read_b128 v[176:179], v183 offset:1024
	ds_read_b128 v[186:189], v183 offset:2048
	ds_read_b128 v[190:193], v183 offset:3072
	ds_read_b128 v[194:197], v183 offset:4096
	ds_read_b128 v[198:201], v183 offset:5120
	ds_read_b128 v[202:205], v183 offset:6144
	ds_read_b128 v[206:209], v183 offset:7168
	global_load_lds_dwordx4 v[210:211], off
	v_lshl_add_u64 v[210:211], s[30:31], 0, v[170:171]
	s_add_i32 m0, s29, 0xe000
	s_nop 0
	global_load_lds_dwordx4 v[210:211], off
	s_waitcnt vmcnt(8)
	s_waitcnt lgkmcnt(0)
	s_barrier
	s_waitcnt lgkmcnt(0)
	v_mfma_f32_16x16x128_f8f6f4 v[156:159], v[24:31], v[172:179], v[156:159]
	v_mfma_f32_16x16x128_f8f6f4 v[148:151], v[16:23], v[172:179], v[148:151]
	v_mfma_f32_16x16x128_f8f6f4 v[140:143], v[24:31], v[186:193], v[140:143]
	v_mfma_f32_16x16x128_f8f6f4 v[132:135], v[16:23], v[186:193], v[132:135]
	v_mfma_f32_16x16x128_f8f6f4 v[124:127], v[24:31], v[194:201], v[124:127]
	v_mfma_f32_16x16x128_f8f6f4 v[116:119], v[16:23], v[194:201], v[116:119]
	v_mfma_f32_16x16x128_f8f6f4 v[108:111], v[24:31], v[202:209], v[108:111]
	v_mfma_f32_16x16x128_f8f6f4 v[100:103], v[16:23], v[202:209], v[100:103]
	v_mfma_f32_16x16x128_f8f6f4 v[152:155], v[8:15], v[172:179], v[152:155]
	v_mfma_f32_16x16x128_f8f6f4 v[144:147], v[0:7], v[172:179], v[144:147]
	v_mfma_f32_16x16x128_f8f6f4 v[136:139], v[8:15], v[186:193], v[136:139]
	v_mfma_f32_16x16x128_f8f6f4 v[128:131], v[0:7], v[186:193], v[128:131]
	v_mfma_f32_16x16x128_f8f6f4 v[120:123], v[8:15], v[194:201], v[120:123]
	v_mfma_f32_16x16x128_f8f6f4 v[112:115], v[0:7], v[194:201], v[112:115]
	v_mfma_f32_16x16x128_f8f6f4 v[104:107], v[8:15], v[202:209], v[104:107]
	v_mfma_f32_16x16x128_f8f6f4 v[96:99], v[0:7], v[202:209], v[96:99]
	s_barrier
	s_add_i32 s75, s55, s39
	v_lshl_add_u64 v[172:173], s[34:35], 0, v[160:161]
	s_mov_b32 m0, s75
	ds_read_b128 v[186:189], v183 offset:16384
	ds_read_b128 v[190:193], v183 offset:17408
	ds_read_b128 v[194:197], v183 offset:18432
	ds_read_b128 v[198:201], v183 offset:19456
	ds_read_b128 v[202:205], v183 offset:20480
	ds_read_b128 v[206:209], v183 offset:21504
	ds_read_b128 v[210:213], v183 offset:22528
	ds_read_b128 v[214:217], v183 offset:23552
	global_load_lds_dwordx4 v[172:173], off
	s_add_i32 m0, s75, 0x2000
	s_add_u32 s76, s34, 0x20000
	v_lshl_add_u64 v[174:175], s[34:35], 0, v[166:167]
	s_addc_u32 s77, s35, 0
	s_add_i32 s75, s64, s39
	global_load_lds_dwordx4 v[174:175], off
	v_lshl_add_u64 v[176:177], s[76:77], 0, v[160:161]
	s_mov_b32 m0, s75
	v_lshl_add_u64 v[178:179], s[36:37], 0, v[164:165]
	global_load_lds_dwordx4 v[176:177], off
	v_lshl_add_u64 v[176:177], s[76:77], 0, v[166:167]
	s_add_i32 m0, s75, 0x2000
	s_nop 0
	global_load_lds_dwordx4 v[176:177], off
	v_lshl_add_u64 v[176:177], s[36:37], 0, v[162:163]
	s_mov_b32 m0, s29
	s_nop 0
	global_load_lds_dwordx4 v[176:177], off
	s_mov_b32 m0, s42
	s_nop 0
	global_load_lds_dwordx4 v[178:179], off
	s_waitcnt vmcnt(8)
	s_waitcnt lgkmcnt(0)
	s_barrier
	s_waitcnt lgkmcnt(0)
	v_mfma_f32_16x16x128_f8f6f4 v[92:95], v[24:31], v[186:193], v[92:95]
	v_mfma_f32_16x16x128_f8f6f4 v[84:87], v[16:23], v[186:193], v[84:87]
	v_mfma_f32_16x16x128_f8f6f4 v[76:79], v[24:31], v[194:201], v[76:79]
	v_mfma_f32_16x16x128_f8f6f4 v[68:71], v[16:23], v[194:201], v[68:71]
	v_mfma_f32_16x16x128_f8f6f4 v[60:63], v[24:31], v[202:209], v[60:63]
	v_mfma_f32_16x16x128_f8f6f4 v[52:55], v[16:23], v[202:209], v[52:55]
	v_mfma_f32_16x16x128_f8f6f4 v[44:47], v[24:31], v[210:217], v[44:47]
	v_mfma_f32_16x16x128_f8f6f4 v[36:39], v[16:23], v[210:217], v[36:39]
	v_mfma_f32_16x16x128_f8f6f4 v[88:91], v[8:15], v[186:193], v[88:91]
	v_mfma_f32_16x16x128_f8f6f4 v[80:83], v[0:7], v[186:193], v[80:83]
	v_mfma_f32_16x16x128_f8f6f4 v[72:75], v[8:15], v[194:201], v[72:75]
	v_mfma_f32_16x16x128_f8f6f4 v[64:67], v[0:7], v[194:201], v[64:67]
	v_mfma_f32_16x16x128_f8f6f4 v[56:59], v[8:15], v[202:209], v[56:59]
	v_mfma_f32_16x16x128_f8f6f4 v[48:51], v[0:7], v[202:209], v[48:51]
	v_mfma_f32_16x16x128_f8f6f4 v[40:43], v[8:15], v[210:217], v[40:43]
	v_mfma_f32_16x16x128_f8f6f4 v[32:35], v[0:7], v[210:217], v[32:35]
	s_barrier
; #define PG8_LDA(dst, b, h) do { _Pragma("unroll") for (int m = 0; m < 4; ++m) _Pragma("unroll") for (int k = 0; k < 2; ++k) dst[m][k] = *(const PG8_LAS bf16x8*)(lds + PG8_SA(b, h) + aoff + m * 2048 + k * 1024); } while (0)
; #define PG8_LDB(dst, b, h) do { _Pragma("unroll") for (int n = 0; n < 2; ++n) _Pragma("unroll") for (int k = 0; k < 2; ++k) dst[n][k] = *(const PG8_LAS bf16x8*)(lds + PG8_SB(b, h) + boff + n * 2048 + k * 1024); } while (0)
; #define PG8_WAIT_V(n) asm volatile("s_waitcnt vmcnt(" #n ")" ::: "memory")
; #define PG8_WAIT_L(n) asm volatile("s_waitcnt lgkmcnt(" #n ")" ::: "memory")
; #define PG8_BAR __builtin_amdgcn_s_barrier()
; #define PG8_SCHED __builtin_amdgcn_sched_barrier(0)
; template <class Epi, class Sched, bool ALIGN_EPI = false, bool SP2 = false, bool F8 = false, bool I8 = false, bool PF = false>
; __device__ __forceinline__ void gemm_phase(PG8_LAS unsigned char* lds, const Gemm g, const Sched& S, const Epi& E, const int wave_) {
;     ...
;             PG8_LDB(B0, 1, 0); PG8_LDB(B1, 1, 1); PG8_SCHED; PG8_LDA(At, 1, 0); PG8_STAGE(PG8_SA(0, 1), a2 + hstep, voffA);
;             PG8_WAIT_V(8); PG8_WAIT_L(0); PG8_BAR; PG8_MMA(0, 0, At, B0); PG8_MMA(0, 1, At, B1); PG8_BAR; PG8_SCHED;
;             PG8_LDA(At, 1, 1); PG8_STAGE(PG8_SB(1, 0), b3, voffB); PG8_STAGE(PG8_SB(1, 1), b3 + hstep, voffB); PG8_STAGE(PG8_SA(1, 0), a3, voffA);
;             PG8_WAIT_V(8); PG8_WAIT_L(0); PG8_BAR; PG8_MMA(1, 0, At, B0); PG8_MMA(1, 1, At, B1); PG8_BAR; PG8_SCHED;
	s_add_i32 s75, 0, 0x18000
	s_add_i32 s76, 0, 0x1c000
	v_add_u32_e32 v12, s75, v180
	v_add_u32_e32 v28, s76, v180
	ds_read_b128 v[0:3], v12
	ds_read_b128 v[4:7], v12 offset:1024
	ds_read_b128 v[8:11], v12 offset:2048
	ds_read_b128 v[12:15], v12 offset:3072
	ds_read_b128 v[16:19], v28
	ds_read_b128 v[20:23], v28 offset:1024
	ds_read_b128 v[24:27], v28 offset:2048
	ds_read_b128 v[28:31], v28 offset:3072
	s_add_u32 s36, s36, 0x20000
	s_addc_u32 s37, s37, 0
	s_mov_b32 m0, s43
	v_lshl_add_u64 v[218:219], s[36:37], 0, v[162:163]
	ds_read_b128 v[186:189], v183 offset:32768
	ds_read_b128 v[190:193], v183 offset:33792
	ds_read_b128 v[194:197], v183 offset:34816
	ds_read_b128 v[198:201], v183 offset:35840
	ds_read_b128 v[202:205], v183 offset:36864
	ds_read_b128 v[206:209], v183 offset:37888
	ds_read_b128 v[210:213], v183 offset:38912
	ds_read_b128 v[214:217], v183 offset:39936
	global_load_lds_dwordx4 v[218:219], off
	v_lshl_add_u64 v[218:219], s[36:37], 0, v[164:165]
	s_mov_b32 m0, s44
	s_nop 0
	global_load_lds_dwordx4 v[218:219], off
	s_waitcnt vmcnt(8)
	s_waitcnt lgkmcnt(0)
	s_barrier
	s_waitcnt lgkmcnt(0)
	v_mfma_f32_16x16x128_f8f6f4 v[156:159], v[0:7], v[186:193], v[156:159]
	v_mfma_f32_16x16x128_f8f6f4 v[148:151], v[8:15], v[186:193], v[148:151]
	v_mfma_f32_16x16x128_f8f6f4 v[140:143], v[0:7], v[194:201], v[140:143]
	v_mfma_f32_16x16x128_f8f6f4 v[132:135], v[8:15], v[194:201], v[132:135]
	v_mfma_f32_16x16x128_f8f6f4 v[124:127], v[0:7], v[202:209], v[124:127]
	v_mfma_f32_16x16x128_f8f6f4 v[116:119], v[8:15], v[202:209], v[116:119]
	v_mfma_f32_16x16x128_f8f6f4 v[108:111], v[0:7], v[210:217], v[108:111]
	v_mfma_f32_16x16x128_f8f6f4 v[100:103], v[8:15], v[210:217], v[100:103]
	v_mfma_f32_16x16x128_f8f6f4 v[152:155], v[16:23], v[186:193], v[152:155]
	v_mfma_f32_16x16x128_f8f6f4 v[144:147], v[24:31], v[186:193], v[144:147]
	v_mfma_f32_16x16x128_f8f6f4 v[136:139], v[16:23], v[194:201], v[136:139]
	v_mfma_f32_16x16x128_f8f6f4 v[128:131], v[24:31], v[194:201], v[128:131]
	v_mfma_f32_16x16x128_f8f6f4 v[120:123], v[16:23], v[202:209], v[120:123]
	v_mfma_f32_16x16x128_f8f6f4 v[112:115], v[24:31], v[202:209], v[112:115]
	v_mfma_f32_16x16x128_f8f6f4 v[104:107], v[16:23], v[210:217], v[104:107]
	v_mfma_f32_16x16x128_f8f6f4 v[96:99], v[24:31], v[210:217], v[96:99]
	s_barrier
	s_add_i32 s36, s75, s39
	v_lshl_add_u64 v[172:173], v[172:173], 0, s[8:9]
	s_mov_b32 m0, s36
	ds_read_b128 v[186:189], v183 offset:49152
	ds_read_b128 v[190:193], v183 offset:50176
	ds_read_b128 v[194:197], v183 offset:51200
	ds_read_b128 v[198:201], v183 offset:52224
	ds_read_b128 v[202:205], v183 offset:53248
	ds_read_b128 v[206:209], v183 offset:54272
	ds_read_b128 v[210:213], v183 offset:55296
	ds_read_b128 v[214:217], v183 offset:56320
	global_load_lds_dwordx4 v[172:173], off
	s_add_i32 m0, s36, 0x2000
	s_add_u32 s34, s34, 0x20080
	v_lshl_add_u64 v[172:173], v[174:175], 0, s[8:9]
	s_addc_u32 s35, s35, 0
	s_add_i32 s36, s76, s39
	global_load_lds_dwordx4 v[172:173], off
	v_lshl_add_u64 v[172:173], s[34:35], 0, v[160:161]
	s_mov_b32 m0, s36
	s_nop 0
	global_load_lds_dwordx4 v[172:173], off
	v_lshl_add_u64 v[172:173], s[34:35], 0, v[166:167]
	s_add_i32 m0, s36, 0x2000
	s_nop 0
	global_load_lds_dwordx4 v[172:173], off
	v_lshl_add_u64 v[172:173], v[176:177], 0, s[8:9]
	s_mov_b32 m0, s48
	s_nop 0
	global_load_lds_dwordx4 v[172:173], off
	v_lshl_add_u64 v[172:173], v[178:179], 0, s[8:9]
	s_mov_b32 m0, s49
	s_nop 0
	global_load_lds_dwordx4 v[172:173], off
	s_waitcnt vmcnt(8)
	s_waitcnt lgkmcnt(0)
	s_barrier
	s_waitcnt lgkmcnt(0)
	v_mfma_f32_16x16x128_f8f6f4 v[92:95], v[0:7], v[186:193], v[92:95]
	v_mfma_f32_16x16x128_f8f6f4 v[84:87], v[8:15], v[186:193], v[84:87]
	v_mfma_f32_16x16x128_f8f6f4 v[76:79], v[0:7], v[194:201], v[76:79]
	v_mfma_f32_16x16x128_f8f6f4 v[68:71], v[8:15], v[194:201], v[68:71]
	v_mfma_f32_16x16x128_f8f6f4 v[60:63], v[0:7], v[202:209], v[60:63]
	v_mfma_f32_16x16x128_f8f6f4 v[52:55], v[8:15], v[202:209], v[52:55]
	v_mfma_f32_16x16x128_f8f6f4 v[44:47], v[0:7], v[210:217], v[44:47]
	v_mfma_f32_16x16x128_f8f6f4 v[36:39], v[8:15], v[210:217], v[36:39]
	v_mfma_f32_16x16x128_f8f6f4 v[88:91], v[16:23], v[186:193], v[88:91]
	v_mfma_f32_16x16x128_f8f6f4 v[80:83], v[24:31], v[186:193], v[80:83]
	v_mfma_f32_16x16x128_f8f6f4 v[72:75], v[16:23], v[194:201], v[72:75]
	v_mfma_f32_16x16x128_f8f6f4 v[64:67], v[24:31], v[194:201], v[64:67]
	v_mfma_f32_16x16x128_f8f6f4 v[56:59], v[16:23], v[202:209], v[56:59]
	v_mfma_f32_16x16x128_f8f6f4 v[48:51], v[24:31], v[202:209], v[48:51]
	v_mfma_f32_16x16x128_f8f6f4 v[40:43], v[16:23], v[210:217], v[40:43]
	v_mfma_f32_16x16x128_f8f6f4 v[32:35], v[24:31], v[210:217], v[32:35]
	s_barrier
	s_add_i32 s74, s74, 2
	s_add_u32 s30, s30, 0x100
	s_addc_u32 s31, s31, 0
	s_add_u32 s72, s72, 0x100
	s_addc_u32 s73, s73, 0
	s_cmp_gt_u32 s74, 5
	s_cbranch_scc0 .LBB0_1540
	s_and_b64 vcc, exec, s[10:11]
	s_cbranch_vccz .LBB0_1543
	s_barrier

; #define PG8_LDA(dst, b, h) do { _Pragma("unroll") for (int m = 0; m < 4; ++m) _Pragma("unroll") for (int k = 0; k < 2; ++k) dst[m][k] = *(const PG8_LAS bf16x8*)(lds + PG8_SA(b, h) + aoff + m * 2048 + k * 1024); } while (0)
; #define PG8_LDB(dst, b, h) do { _Pragma("unroll") for (int n = 0; n < 2; ++n) _Pragma("unroll") for (int k = 0; k < 2; ++k) dst[n][k] = *(const PG8_LAS bf16x8*)(lds + PG8_SB(b, h) + boff + n * 2048 + k * 1024); } while (0)
; #define PG8_WAIT_V(n) asm volatile("s_waitcnt vmcnt(" #n ")" ::: "memory")
; #define PG8_WAIT_L(n) asm volatile("s_waitcnt lgkmcnt(" #n ")" ::: "memory")
; #define PG8_BAR __builtin_amdgcn_s_barrier()
; #define PG8_SCHED __builtin_amdgcn_sched_barrier(0)
; template <class Epi, class Sched, bool ALIGN_EPI = false, bool SP2 = false, bool F8 = false, bool I8 = false, bool PF = false>
; __device__ __forceinline__ void gemm_phase(PG8_LAS unsigned char* lds, const Gemm g, const Sched& S, const Epi& E, const int wave_) {
;     ...
;             PG8_LDB(B0, 0, 0); PG8_LDB(B1, 0, 1); PG8_SCHED; PG8_LDA(At, 0, 0); PG8_STAGE(PG8_SA(1, 1), a1 + hstep, voffA);
;             PG8_WAIT_V(8); PG8_WAIT_L(0); PG8_BAR; PG8_MMA(0, 0, At, B0); PG8_MMA(0, 1, At, B1); PG8_BAR; PG8_SCHED;
;             PG8_LDA(At, 0, 1); PG8_STAGE(PG8_SB(0, 0), b2, voffB); PG8_STAGE(PG8_SB(0, 1), b2 + hstep, voffB); PG8_STAGE(PG8_SA(0, 0), a2, voffA);
;             PG8_WAIT_V(8); PG8_WAIT_L(0); PG8_BAR; PG8_MMA(1, 0, At, B0); PG8_MMA(1, 1, At, B1); PG8_BAR; PG8_SCHED;
.LBB0_1621:
	ds_read_b128 v[24:27], v181
	ds_read_b128 v[28:31], v181 offset:1024
	ds_read_b128 v[16:19], v181 offset:2048
	ds_read_b128 v[20:23], v181 offset:3072
	ds_read_b128 v[8:11], v182
	ds_read_b128 v[12:15], v182 offset:1024
	ds_read_b128 v[0:3], v182 offset:2048
	ds_read_b128 v[4:7], v182 offset:3072
	s_add_u32 s30, s34, 0x100
	s_addc_u32 s31, s35, 0
	s_cmp_eq_u32 s73, 24
	s_cselect_b32 s39, s25, s31
	s_cselect_b32 s38, s24, s30
	s_cselect_b32 s37, s27, s72
	s_cselect_b32 s36, s26, s71
	v_lshl_add_u64 v[208:209], s[34:35], 0, v[168:169]
	s_add_i32 m0, s29, 0xc000
	ds_read_b128 v[172:175], v183
	ds_read_b128 v[176:179], v183 offset:1024
	ds_read_b128 v[184:187], v183 offset:2048
	ds_read_b128 v[188:191], v183 offset:3072
	ds_read_b128 v[192:195], v183 offset:4096
	ds_read_b128 v[196:199], v183 offset:5120
	ds_read_b128 v[200:203], v183 offset:6144
	ds_read_b128 v[204:207], v183 offset:7168
	global_load_lds_dwordx4 v[208:209], off
	v_lshl_add_u64 v[208:209], s[34:35], 0, v[170:171]
	s_add_i32 m0, s29, 0xe000
	s_nop 0
	global_load_lds_dwordx4 v[208:209], off
	s_waitcnt vmcnt(8)
	s_waitcnt lgkmcnt(0)
	s_barrier
	s_waitcnt lgkmcnt(0)
	v_mfma_f32_16x16x128_f8f6f4 v[156:159], v[24:31], v[172:179], v[156:159]
	v_mfma_f32_16x16x128_f8f6f4 v[152:155], v[16:23], v[172:179], v[152:155]
	v_mfma_f32_16x16x128_f8f6f4 v[144:147], v[24:31], v[184:191], v[144:147]
	v_mfma_f32_16x16x128_f8f6f4 v[136:139], v[16:23], v[184:191], v[136:139]
	v_mfma_f32_16x16x128_f8f6f4 v[128:131], v[24:31], v[192:199], v[128:131]
	v_mfma_f32_16x16x128_f8f6f4 v[120:123], v[16:23], v[192:199], v[120:123]
	v_mfma_f32_16x16x128_f8f6f4 v[112:115], v[24:31], v[200:207], v[112:115]
	v_mfma_f32_16x16x128_f8f6f4 v[104:107], v[16:23], v[200:207], v[104:107]
	v_mfma_f32_16x16x128_f8f6f4 v[148:151], v[8:15], v[172:179], v[148:151]
	v_mfma_f32_16x16x128_f8f6f4 v[140:143], v[0:7], v[172:179], v[140:143]
	v_mfma_f32_16x16x128_f8f6f4 v[132:135], v[8:15], v[184:191], v[132:135]
	v_mfma_f32_16x16x128_f8f6f4 v[124:127], v[0:7], v[184:191], v[124:127]
	v_mfma_f32_16x16x128_f8f6f4 v[116:119], v[8:15], v[192:199], v[116:119]
	v_mfma_f32_16x16x128_f8f6f4 v[108:111], v[0:7], v[192:199], v[108:111]
	v_mfma_f32_16x16x128_f8f6f4 v[100:103], v[8:15], v[200:207], v[100:103]
	v_mfma_f32_16x16x128_f8f6f4 v[96:99], v[0:7], v[200:207], v[96:99]
	s_barrier
	s_add_i32 s34, s53, s42
	v_lshl_add_u64 v[172:173], s[36:37], 0, v[160:161]
	s_mov_b32 m0, s34
	ds_read_b128 v[184:187], v183 offset:16384
	ds_read_b128 v[188:191], v183 offset:17408
	ds_read_b128 v[192:195], v183 offset:18432
	ds_read_b128 v[196:199], v183 offset:19456
	ds_read_b128 v[200:203], v183 offset:20480
	ds_read_b128 v[204:207], v183 offset:21504
	ds_read_b128 v[208:211], v183 offset:22528
	ds_read_b128 v[212:215], v183 offset:23552
	global_load_lds_dwordx4 v[172:173], off
	s_add_i32 m0, s34, 0x2000
	s_add_u32 s34, s36, 0x70000
	v_lshl_add_u64 v[174:175], s[36:37], 0, v[166:167]
	s_addc_u32 s35, s37, 0
	s_add_i32 s74, s54, s42
	global_load_lds_dwordx4 v[174:175], off
	v_lshl_add_u64 v[176:177], s[34:35], 0, v[160:161]
	s_mov_b32 m0, s74
	v_lshl_add_u64 v[178:179], s[38:39], 0, v[164:165]
	global_load_lds_dwordx4 v[176:177], off
	v_lshl_add_u64 v[176:177], s[34:35], 0, v[166:167]
	s_add_i32 m0, s74, 0x2000
	s_nop 0
	global_load_lds_dwordx4 v[176:177], off
	v_lshl_add_u64 v[176:177], s[38:39], 0, v[162:163]
	s_mov_b32 m0, s29
	s_nop 0
	global_load_lds_dwordx4 v[176:177], off
	s_mov_b32 m0, s45
	s_nop 0
	global_load_lds_dwordx4 v[178:179], off
	s_waitcnt vmcnt(8)
	s_waitcnt lgkmcnt(0)
	s_barrier
	s_waitcnt lgkmcnt(0)
	v_mfma_f32_16x16x128_f8f6f4 v[92:95], v[24:31], v[184:191], v[92:95]
	v_mfma_f32_16x16x128_f8f6f4 v[88:91], v[16:23], v[184:191], v[88:91]
	v_mfma_f32_16x16x128_f8f6f4 v[80:83], v[24:31], v[192:199], v[80:83]
	v_mfma_f32_16x16x128_f8f6f4 v[72:75], v[16:23], v[192:199], v[72:75]
	v_mfma_f32_16x16x128_f8f6f4 v[64:67], v[24:31], v[200:207], v[64:67]
	v_mfma_f32_16x16x128_f8f6f4 v[56:59], v[16:23], v[200:207], v[56:59]
	v_mfma_f32_16x16x128_f8f6f4 v[48:51], v[24:31], v[208:215], v[48:51]
	v_mfma_f32_16x16x128_f8f6f4 v[40:43], v[16:23], v[208:215], v[40:43]
	v_mfma_f32_16x16x128_f8f6f4 v[84:87], v[8:15], v[184:191], v[84:87]
	v_mfma_f32_16x16x128_f8f6f4 v[76:79], v[0:7], v[184:191], v[76:79]
	v_mfma_f32_16x16x128_f8f6f4 v[68:71], v[8:15], v[192:199], v[68:71]
	v_mfma_f32_16x16x128_f8f6f4 v[60:63], v[0:7], v[192:199], v[60:63]
	v_mfma_f32_16x16x128_f8f6f4 v[52:55], v[8:15], v[200:207], v[52:55]
	v_mfma_f32_16x16x128_f8f6f4 v[44:47], v[0:7], v[200:207], v[44:47]
	v_mfma_f32_16x16x128_f8f6f4 v[36:39], v[8:15], v[208:215], v[36:39]
	v_mfma_f32_16x16x128_f8f6f4 v[32:35], v[0:7], v[208:215], v[32:35]
	s_barrier
; #define PG8_LDA(dst, b, h) do { _Pragma("unroll") for (int m = 0; m < 4; ++m) _Pragma("unroll") for (int k = 0; k < 2; ++k) dst[m][k] = *(const PG8_LAS bf16x8*)(lds + PG8_SA(b, h) + aoff + m * 2048 + k * 1024); } while (0)
; #define PG8_LDB(dst, b, h) do { _Pragma("unroll") for (int n = 0; n < 2; ++n) _Pragma("unroll") for (int k = 0; k < 2; ++k) dst[n][k] = *(const PG8_LAS bf16x8*)(lds + PG8_SB(b, h) + boff + n * 2048 + k * 1024); } while (0)
; #define PG8_WAIT_V(n) asm volatile("s_waitcnt vmcnt(" #n ")" ::: "memory")
; #define PG8_WAIT_L(n) asm volatile("s_waitcnt lgkmcnt(" #n ")" ::: "memory")
; #define PG8_BAR __builtin_amdgcn_s_barrier()
; #define PG8_SCHED __builtin_amdgcn_sched_barrier(0)
; template <class Epi, class Sched, bool ALIGN_EPI = false, bool SP2 = false, bool F8 = false, bool I8 = false, bool PF = false>
; __device__ __forceinline__ void gemm_phase(PG8_LAS unsigned char* lds, const Gemm g, const Sched& S, const Epi& E, const int wave_) {
;     ...
;             if constexpr (SP2) {
;             PG8_LDB(B0, 0, 0); PG8_LDB(B1, 0, 1); PG8_SCHED; PG8_LDA(At, 0, 0); PG8_STAGE(PG8_SA(1, 1), a1 + hstep, voffA);
;             PG8_WAIT_V(8); PG8_WAIT_L(0); PG8_BAR; PG8_MMA(0, 0, At, B0); PG8_MMA(0, 1, At, B1); PG8_BAR; PG8_SCHED;
;             PG8_LDA(At, 0, 1); PG8_STAGE(PG8_SB(0, 0), b2, voffB); PG8_STAGE(PG8_SB(0, 1), b2 + hstep, voffB); PG8_STAGE(PG8_SA(0, 0), a2, voffA);
;             PG8_WAIT_V(8); PG8_WAIT_L(0); PG8_BAR; PG8_MMA(1, 0, At, B0); PG8_MMA(1, 1, At, B1); PG8_BAR; PG8_SCHED;
;             PG8_LDB(B0, 1, 0); PG8_LDB(B1, 1, 1); PG8_SCHED; PG8_LDA(At, 1, 0); PG8_STAGE(PG8_SA(0, 1), a2 + hstep, voffA);
;             PG8_WAIT_V(8); PG8_WAIT_L(0); PG8_BAR; PG8_MMA(0, 0, At, B0); PG8_MMA(0, 1, At, B1); PG8_BAR; PG8_SCHED;
;             PG8_LDA(At, 1, 1); PG8_STAGE(PG8_SB(1, 0), b3, voffB); PG8_STAGE(PG8_SB(1, 1), b3 + hstep, voffB); PG8_STAGE(PG8_SA(1, 0), a3, voffA);
;             PG8_WAIT_V(8); PG8_WAIT_L(0); PG8_BAR; PG8_MMA(1, 0, At, B0); PG8_MMA(1, 1, At, B1); PG8_BAR; PG8_SCHED;
	s_add_i32 s74, 0, 0x18000
	s_add_i32 s75, 0, 0x1c000
	v_add_u32_e32 v12, s74, v180
	v_add_u32_e32 v28, s75, v180
	ds_read_b128 v[0:3], v12
	ds_read_b128 v[4:7], v12 offset:1024
	ds_read_b128 v[8:11], v12 offset:2048
	ds_read_b128 v[12:15], v12 offset:3072
	ds_read_b128 v[16:19], v28
	ds_read_b128 v[20:23], v28 offset:1024
	ds_read_b128 v[24:27], v28 offset:2048
	ds_read_b128 v[28:31], v28 offset:3072
	s_add_u32 s34, s38, 0x70000
	s_addc_u32 s35, s39, 0
	s_mov_b32 m0, s46
	v_lshl_add_u64 v[216:217], s[34:35], 0, v[162:163]
	ds_read_b128 v[184:187], v183 offset:32768
	ds_read_b128 v[188:191], v183 offset:33792
	ds_read_b128 v[192:195], v183 offset:34816
	ds_read_b128 v[196:199], v183 offset:35840
	ds_read_b128 v[200:203], v183 offset:36864
	ds_read_b128 v[204:207], v183 offset:37888
	ds_read_b128 v[208:211], v183 offset:38912
	ds_read_b128 v[212:215], v183 offset:39936
	global_load_lds_dwordx4 v[216:217], off
	v_lshl_add_u64 v[216:217], s[34:35], 0, v[164:165]
	s_mov_b32 m0, s47
	s_nop 0
	global_load_lds_dwordx4 v[216:217], off
	s_waitcnt vmcnt(8)
	s_waitcnt lgkmcnt(0)
	s_barrier
	s_waitcnt lgkmcnt(0)
	v_mfma_f32_16x16x128_f8f6f4 v[156:159], v[0:7], v[184:191], v[156:159]
	v_mfma_f32_16x16x128_f8f6f4 v[152:155], v[8:15], v[184:191], v[152:155]
	v_mfma_f32_16x16x128_f8f6f4 v[144:147], v[0:7], v[192:199], v[144:147]
	v_mfma_f32_16x16x128_f8f6f4 v[136:139], v[8:15], v[192:199], v[136:139]
	v_mfma_f32_16x16x128_f8f6f4 v[128:131], v[0:7], v[200:207], v[128:131]
	v_mfma_f32_16x16x128_f8f6f4 v[120:123], v[8:15], v[200:207], v[120:123]
	v_mfma_f32_16x16x128_f8f6f4 v[112:115], v[0:7], v[208:215], v[112:115]
	v_mfma_f32_16x16x128_f8f6f4 v[104:107], v[8:15], v[208:215], v[104:107]
	v_mfma_f32_16x16x128_f8f6f4 v[148:151], v[16:23], v[184:191], v[148:151]
	v_mfma_f32_16x16x128_f8f6f4 v[140:143], v[24:31], v[184:191], v[140:143]
	v_mfma_f32_16x16x128_f8f6f4 v[132:135], v[16:23], v[192:199], v[132:135]
	v_mfma_f32_16x16x128_f8f6f4 v[124:127], v[24:31], v[192:199], v[124:127]
	v_mfma_f32_16x16x128_f8f6f4 v[116:119], v[16:23], v[200:207], v[116:119]
	v_mfma_f32_16x16x128_f8f6f4 v[108:111], v[24:31], v[200:207], v[108:111]
	v_mfma_f32_16x16x128_f8f6f4 v[100:103], v[16:23], v[208:215], v[100:103]
	v_mfma_f32_16x16x128_f8f6f4 v[96:99], v[24:31], v[208:215], v[96:99]
	s_barrier
	s_add_i32 s34, s74, s42
	v_lshl_add_u64 v[172:173], v[172:173], 0, s[8:9]
	s_mov_b32 m0, s34
	ds_read_b128 v[184:187], v183 offset:49152
	ds_read_b128 v[188:191], v183 offset:50176
	ds_read_b128 v[192:195], v183 offset:51200
	ds_read_b128 v[196:199], v183 offset:52224
	ds_read_b128 v[200:203], v183 offset:53248
	ds_read_b128 v[204:207], v183 offset:54272
	ds_read_b128 v[208:211], v183 offset:55296
	ds_read_b128 v[212:215], v183 offset:56320
	global_load_lds_dwordx4 v[172:173], off
	s_add_i32 m0, s34, 0x2000
	s_add_u32 s34, s36, 0x70080
	v_lshl_add_u64 v[172:173], v[174:175], 0, s[8:9]
	s_addc_u32 s35, s37, 0
	s_add_i32 s36, s75, s42
	global_load_lds_dwordx4 v[172:173], off
	v_lshl_add_u64 v[172:173], s[34:35], 0, v[160:161]
	s_mov_b32 m0, s36
	s_nop 0
	global_load_lds_dwordx4 v[172:173], off
	v_lshl_add_u64 v[172:173], s[34:35], 0, v[166:167]
	s_add_i32 m0, s36, 0x2000
	s_nop 0
	global_load_lds_dwordx4 v[172:173], off
	v_lshl_add_u64 v[172:173], v[176:177], 0, s[8:9]
	s_mov_b32 m0, s51
	s_nop 0
	global_load_lds_dwordx4 v[172:173], off
	v_lshl_add_u64 v[172:173], v[178:179], 0, s[8:9]
	s_mov_b32 m0, s52
	s_nop 0
	global_load_lds_dwordx4 v[172:173], off
	s_waitcnt vmcnt(8)
	s_waitcnt lgkmcnt(0)
	s_barrier
	s_waitcnt lgkmcnt(0)
	v_mfma_f32_16x16x128_f8f6f4 v[92:95], v[0:7], v[184:191], v[92:95]
	v_mfma_f32_16x16x128_f8f6f4 v[88:91], v[8:15], v[184:191], v[88:91]
	v_mfma_f32_16x16x128_f8f6f4 v[80:83], v[0:7], v[192:199], v[80:83]
	v_mfma_f32_16x16x128_f8f6f4 v[72:75], v[8:15], v[192:199], v[72:75]
	v_mfma_f32_16x16x128_f8f6f4 v[64:67], v[0:7], v[200:207], v[64:67]
	v_mfma_f32_16x16x128_f8f6f4 v[56:59], v[8:15], v[200:207], v[56:59]
	v_mfma_f32_16x16x128_f8f6f4 v[48:51], v[0:7], v[208:215], v[48:51]
	v_mfma_f32_16x16x128_f8f6f4 v[40:43], v[8:15], v[208:215], v[40:43]
	v_mfma_f32_16x16x128_f8f6f4 v[84:87], v[16:23], v[184:191], v[84:87]
	v_mfma_f32_16x16x128_f8f6f4 v[76:79], v[24:31], v[184:191], v[76:79]
	v_mfma_f32_16x16x128_f8f6f4 v[68:71], v[16:23], v[192:199], v[68:71]
	v_mfma_f32_16x16x128_f8f6f4 v[60:63], v[24:31], v[192:199], v[60:63]
	v_mfma_f32_16x16x128_f8f6f4 v[52:55], v[16:23], v[200:207], v[52:55]
	v_mfma_f32_16x16x128_f8f6f4 v[44:47], v[24:31], v[200:207], v[44:47]
	v_mfma_f32_16x16x128_f8f6f4 v[36:39], v[16:23], v[208:215], v[36:39]
	v_mfma_f32_16x16x128_f8f6f4 v[32:35], v[24:31], v[208:215], v[32:35]
	s_barrier
	s_add_i32 s73, s73, 2
	s_add_u32 s71, s71, 0x100
	s_addc_u32 s72, s72, 0
	s_cmp_gt_u32 s73, 25
	s_mov_b64 s[34:35], s[30:31]
	s_cbranch_scc0 .LBB0_1621
	s_and_b64 vcc, exec, s[10:11]
	s_cbranch_vccz .LBB0_1624
	s_barrier

; #define PG8_LDA(dst, b, h) do { _Pragma("unroll") for (int m = 0; m < 4; ++m) _Pragma("unroll") for (int k = 0; k < 2; ++k) dst[m][k] = *(const PG8_LAS bf16x8*)(lds + PG8_SA(b, h) + aoff + m * 2048 + k * 1024); } while (0)
; #define PG8_LDB(dst, b, h) do { _Pragma("unroll") for (int n = 0; n < 2; ++n) _Pragma("unroll") for (int k = 0; k < 2; ++k) dst[n][k] = *(const PG8_LAS bf16x8*)(lds + PG8_SB(b, h) + boff + n * 2048 + k * 1024); } while (0)
; #define PG8_WAIT_V(n) asm volatile("s_waitcnt vmcnt(" #n ")" ::: "memory")
; #define PG8_WAIT_L(n) asm volatile("s_waitcnt lgkmcnt(" #n ")" ::: "memory")
; #define PG8_BAR __builtin_amdgcn_s_barrier()
; #define PG8_SCHED __builtin_amdgcn_sched_barrier(0)
; template <class Epi, class Sched, bool ALIGN_EPI = false, bool SP2 = false, bool F8 = false, bool I8 = false, bool PF = false>
; __device__ __forceinline__ void gemm_phase(PG8_LAS unsigned char* lds, const Gemm g, const Sched& S, const Epi& E, const int wave_) {
;     ...
;             if constexpr (SP2) {
;             PG8_LDB(B0, 0, 0); PG8_LDB(B1, 0, 1); PG8_SCHED; PG8_LDA(At, 0, 0); PG8_STAGE(PG8_SA(1, 1), a1 + hstep, voffA);
;             PG8_WAIT_V(8); PG8_WAIT_L(0); PG8_BAR; PG8_MMA(0, 0, At, B0); PG8_MMA(0, 1, At, B1); PG8_BAR; PG8_SCHED;
;             PG8_LDA(At, 0, 1); PG8_STAGE(PG8_SB(0, 0), b2, voffB); PG8_STAGE(PG8_SB(0, 1), b2 + hstep, voffB); PG8_STAGE(PG8_SA(0, 0), a2, voffA);
;             PG8_WAIT_V(8); PG8_WAIT_L(0); PG8_BAR; PG8_MMA(1, 0, At, B0); PG8_MMA(1, 1, At, B1); PG8_BAR; PG8_SCHED;
;             PG8_LDB(B0, 1, 0); PG8_LDB(B1, 1, 1); PG8_SCHED; PG8_LDA(At, 1, 0); PG8_STAGE(PG8_SA(0, 1), a2 + hstep, voffA);
;             PG8_WAIT_V(8); PG8_WAIT_L(0); PG8_BAR; PG8_MMA(0, 0, At, B0); PG8_MMA(0, 1, At, B1); PG8_BAR; PG8_SCHED;
;             PG8_LDA(At, 1, 1); PG8_STAGE(PG8_SB(1, 0), b3, voffB); PG8_STAGE(PG8_SB(1, 1), b3 + hstep, voffB); PG8_STAGE(PG8_SA(1, 0), a3, voffA);
;             PG8_WAIT_V(8); PG8_WAIT_L(0); PG8_BAR; PG8_MMA(1, 0, At, B0); PG8_MMA(1, 1, At, B1); PG8_BAR; PG8_SCHED;
.LBB0_1718:
	ds_read_b128 v[24:27], v181
	ds_read_b128 v[28:31], v181 offset:1024
	ds_read_b128 v[16:19], v181 offset:2048
	ds_read_b128 v[20:23], v181 offset:3072
	ds_read_b128 v[8:11], v182
	ds_read_b128 v[12:15], v182 offset:1024
	ds_read_b128 v[0:3], v182 offset:2048
	ds_read_b128 v[4:7], v182 offset:3072
	s_add_u32 s30, s34, 0x100
	s_addc_u32 s31, s35, 0
	s_cmp_eq_u32 s73, 24
	s_cselect_b32 s39, s25, s31
	s_cselect_b32 s38, s24, s30
	s_cselect_b32 s37, s27, s72
	s_cselect_b32 s36, s26, s71
	v_lshl_add_u64 v[208:209], s[34:35], 0, v[168:169]
	s_add_i32 m0, s29, 0xc000
	ds_read_b128 v[172:175], v183
	ds_read_b128 v[176:179], v183 offset:1024
	ds_read_b128 v[184:187], v183 offset:2048
	ds_read_b128 v[188:191], v183 offset:3072
	ds_read_b128 v[192:195], v183 offset:4096
	ds_read_b128 v[196:199], v183 offset:5120
	ds_read_b128 v[200:203], v183 offset:6144
	ds_read_b128 v[204:207], v183 offset:7168
	global_load_lds_dwordx4 v[208:209], off
	v_lshl_add_u64 v[208:209], s[34:35], 0, v[170:171]
	s_add_i32 m0, s29, 0xe000
	s_nop 0
	global_load_lds_dwordx4 v[208:209], off
	s_waitcnt vmcnt(8)
	s_waitcnt lgkmcnt(0)
	s_barrier
	s_waitcnt lgkmcnt(0)
	v_mfma_f32_16x16x128_f8f6f4 v[156:159], v[24:31], v[172:179], v[156:159]
	v_mfma_f32_16x16x128_f8f6f4 v[152:155], v[16:23], v[172:179], v[152:155]
	v_mfma_f32_16x16x128_f8f6f4 v[144:147], v[24:31], v[184:191], v[144:147]
	v_mfma_f32_16x16x128_f8f6f4 v[136:139], v[16:23], v[184:191], v[136:139]
	v_mfma_f32_16x16x128_f8f6f4 v[128:131], v[24:31], v[192:199], v[128:131]
	v_mfma_f32_16x16x128_f8f6f4 v[120:123], v[16:23], v[192:199], v[120:123]
	v_mfma_f32_16x16x128_f8f6f4 v[112:115], v[24:31], v[200:207], v[112:115]
	v_mfma_f32_16x16x128_f8f6f4 v[104:107], v[16:23], v[200:207], v[104:107]
	v_mfma_f32_16x16x128_f8f6f4 v[148:151], v[8:15], v[172:179], v[148:151]
	v_mfma_f32_16x16x128_f8f6f4 v[140:143], v[0:7], v[172:179], v[140:143]
	v_mfma_f32_16x16x128_f8f6f4 v[132:135], v[8:15], v[184:191], v[132:135]
	v_mfma_f32_16x16x128_f8f6f4 v[124:127], v[0:7], v[184:191], v[124:127]
	v_mfma_f32_16x16x128_f8f6f4 v[116:119], v[8:15], v[192:199], v[116:119]
	v_mfma_f32_16x16x128_f8f6f4 v[108:111], v[0:7], v[192:199], v[108:111]
	v_mfma_f32_16x16x128_f8f6f4 v[100:103], v[8:15], v[200:207], v[100:103]
	v_mfma_f32_16x16x128_f8f6f4 v[96:99], v[0:7], v[200:207], v[96:99]
	s_barrier
	s_add_i32 s34, s53, s43
	v_lshl_add_u64 v[172:173], s[36:37], 0, v[160:161]
	s_mov_b32 m0, s34
	ds_read_b128 v[184:187], v183 offset:16384
	ds_read_b128 v[188:191], v183 offset:17408
	ds_read_b128 v[192:195], v183 offset:18432
	ds_read_b128 v[196:199], v183 offset:19456
	ds_read_b128 v[200:203], v183 offset:20480
	ds_read_b128 v[204:207], v183 offset:21504
	ds_read_b128 v[208:211], v183 offset:22528
	ds_read_b128 v[212:215], v183 offset:23552
	global_load_lds_dwordx4 v[172:173], off
	s_add_i32 m0, s34, 0x2000
	s_add_u32 s34, s36, 0x70000
	v_lshl_add_u64 v[174:175], s[36:37], 0, v[162:163]
	s_addc_u32 s35, s37, 0
	s_add_i32 s74, s54, s43
	global_load_lds_dwordx4 v[174:175], off
	v_lshl_add_u64 v[176:177], s[34:35], 0, v[160:161]
	s_mov_b32 m0, s74
	v_lshl_add_u64 v[178:179], s[38:39], 0, v[164:165]
	global_load_lds_dwordx4 v[176:177], off
	v_lshl_add_u64 v[176:177], s[34:35], 0, v[162:163]
	s_add_i32 m0, s74, 0x2000
	s_nop 0
	global_load_lds_dwordx4 v[176:177], off
	v_lshl_add_u64 v[176:177], s[38:39], 0, v[166:167]
	s_mov_b32 m0, s29
	s_nop 0
	global_load_lds_dwordx4 v[176:177], off
	s_mov_b32 m0, s45
	s_nop 0
	global_load_lds_dwordx4 v[178:179], off
	s_waitcnt vmcnt(8)
	s_waitcnt lgkmcnt(0)
	s_barrier
	s_waitcnt lgkmcnt(0)
	v_mfma_f32_16x16x128_f8f6f4 v[92:95], v[24:31], v[184:191], v[92:95]
	v_mfma_f32_16x16x128_f8f6f4 v[88:91], v[16:23], v[184:191], v[88:91]
	v_mfma_f32_16x16x128_f8f6f4 v[80:83], v[24:31], v[192:199], v[80:83]
	v_mfma_f32_16x16x128_f8f6f4 v[72:75], v[16:23], v[192:199], v[72:75]
	v_mfma_f32_16x16x128_f8f6f4 v[64:67], v[24:31], v[200:207], v[64:67]
	v_mfma_f32_16x16x128_f8f6f4 v[56:59], v[16:23], v[200:207], v[56:59]
	v_mfma_f32_16x16x128_f8f6f4 v[48:51], v[24:31], v[208:215], v[48:51]
	v_mfma_f32_16x16x128_f8f6f4 v[40:43], v[16:23], v[208:215], v[40:43]
	v_mfma_f32_16x16x128_f8f6f4 v[84:87], v[8:15], v[184:191], v[84:87]
	v_mfma_f32_16x16x128_f8f6f4 v[76:79], v[0:7], v[184:191], v[76:79]
	v_mfma_f32_16x16x128_f8f6f4 v[68:71], v[8:15], v[192:199], v[68:71]
	v_mfma_f32_16x16x128_f8f6f4 v[60:63], v[0:7], v[192:199], v[60:63]
	v_mfma_f32_16x16x128_f8f6f4 v[52:55], v[8:15], v[200:207], v[52:55]
	v_mfma_f32_16x16x128_f8f6f4 v[44:47], v[0:7], v[200:207], v[44:47]
	v_mfma_f32_16x16x128_f8f6f4 v[36:39], v[8:15], v[208:215], v[36:39]
	v_mfma_f32_16x16x128_f8f6f4 v[32:35], v[0:7], v[208:215], v[32:35]
	s_barrier
; #define PG8_LDA(dst, b, h) do { _Pragma("unroll") for (int m = 0; m < 4; ++m) _Pragma("unroll") for (int k = 0; k < 2; ++k) dst[m][k] = *(const PG8_LAS bf16x8*)(lds + PG8_SA(b, h) + aoff + m * 2048 + k * 1024); } while (0)
; #define PG8_LDB(dst, b, h) do { _Pragma("unroll") for (int n = 0; n < 2; ++n) _Pragma("unroll") for (int k = 0; k < 2; ++k) dst[n][k] = *(const PG8_LAS bf16x8*)(lds + PG8_SB(b, h) + boff + n * 2048 + k * 1024); } while (0)
; #define PG8_WAIT_V(n) asm volatile("s_waitcnt vmcnt(" #n ")" ::: "memory")
; #define PG8_WAIT_L(n) asm volatile("s_waitcnt lgkmcnt(" #n ")" ::: "memory")
; #define PG8_BAR __builtin_amdgcn_s_barrier()
; #define PG8_SCHED __builtin_amdgcn_sched_barrier(0)
; template <class Epi, class Sched, bool ALIGN_EPI = false, bool SP2 = false, bool F8 = false, bool I8 = false, bool PF = false>
; __device__ __forceinline__ void gemm_phase(PG8_LAS unsigned char* lds, const Gemm g, const Sched& S, const Epi& E, const int wave_) {
;     ...
;             if constexpr (SP2) {
;             PG8_LDB(B0, 0, 0); PG8_LDB(B1, 0, 1); PG8_SCHED; PG8_LDA(At, 0, 0); PG8_STAGE(PG8_SA(1, 1), a1 + hstep, voffA);
;             PG8_WAIT_V(8); PG8_WAIT_L(0); PG8_BAR; PG8_MMA(0, 0, At, B0); PG8_MMA(0, 1, At, B1); PG8_BAR; PG8_SCHED;
;             PG8_LDA(At, 0, 1); PG8_STAGE(PG8_SB(0, 0), b2, voffB); PG8_STAGE(PG8_SB(0, 1), b2 + hstep, voffB); PG8_STAGE(PG8_SA(0, 0), a2, voffA);
;             PG8_WAIT_V(8); PG8_WAIT_L(0); PG8_BAR; PG8_MMA(1, 0, At, B0); PG8_MMA(1, 1, At, B1); PG8_BAR; PG8_SCHED;
;             PG8_LDB(B0, 1, 0); PG8_LDB(B1, 1, 1); PG8_SCHED; PG8_LDA(At, 1, 0); PG8_STAGE(PG8_SA(0, 1), a2 + hstep, voffA);
;             PG8_WAIT_V(8); PG8_WAIT_L(0); PG8_BAR; PG8_MMA(0, 0, At, B0); PG8_MMA(0, 1, At, B1); PG8_BAR; PG8_SCHED;
;             PG8_LDA(At, 1, 1); PG8_STAGE(PG8_SB(1, 0), b3, voffB); PG8_STAGE(PG8_SB(1, 1), b3 + hstep, voffB); PG8_STAGE(PG8_SA(1, 0), a3, voffA);
;             PG8_WAIT_V(8); PG8_WAIT_L(0); PG8_BAR; PG8_MMA(1, 0, At, B0); PG8_MMA(1, 1, At, B1); PG8_BAR; PG8_SCHED;
	s_add_i32 s74, 0, 0x18000
	s_add_i32 s75, 0, 0x1c000
	v_add_u32_e32 v12, s74, v180
	v_add_u32_e32 v28, s75, v180
	ds_read_b128 v[0:3], v12
	ds_read_b128 v[4:7], v12 offset:1024
	ds_read_b128 v[8:11], v12 offset:2048
	ds_read_b128 v[12:15], v12 offset:3072
	ds_read_b128 v[16:19], v28
	ds_read_b128 v[20:23], v28 offset:1024
	ds_read_b128 v[24:27], v28 offset:2048
	ds_read_b128 v[28:31], v28 offset:3072
	s_add_u32 s34, s38, 0x70000
	s_addc_u32 s35, s39, 0
	s_mov_b32 m0, s46
	v_lshl_add_u64 v[216:217], s[34:35], 0, v[166:167]
	ds_read_b128 v[184:187], v183 offset:32768
	ds_read_b128 v[188:191], v183 offset:33792
	ds_read_b128 v[192:195], v183 offset:34816
	ds_read_b128 v[196:199], v183 offset:35840
	ds_read_b128 v[200:203], v183 offset:36864
	ds_read_b128 v[204:207], v183 offset:37888
	ds_read_b128 v[208:211], v183 offset:38912
	ds_read_b128 v[212:215], v183 offset:39936
	global_load_lds_dwordx4 v[216:217], off
	v_lshl_add_u64 v[216:217], s[34:35], 0, v[164:165]
	s_mov_b32 m0, s47
	s_nop 0
	global_load_lds_dwordx4 v[216:217], off
	s_waitcnt vmcnt(8)
	s_waitcnt lgkmcnt(0)
	s_barrier
	s_waitcnt lgkmcnt(0)
	v_mfma_f32_16x16x128_f8f6f4 v[156:159], v[0:7], v[184:191], v[156:159]
	v_mfma_f32_16x16x128_f8f6f4 v[152:155], v[8:15], v[184:191], v[152:155]
	v_mfma_f32_16x16x128_f8f6f4 v[144:147], v[0:7], v[192:199], v[144:147]
	v_mfma_f32_16x16x128_f8f6f4 v[136:139], v[8:15], v[192:199], v[136:139]
	v_mfma_f32_16x16x128_f8f6f4 v[128:131], v[0:7], v[200:207], v[128:131]
	v_mfma_f32_16x16x128_f8f6f4 v[120:123], v[8:15], v[200:207], v[120:123]
	v_mfma_f32_16x16x128_f8f6f4 v[112:115], v[0:7], v[208:215], v[112:115]
	v_mfma_f32_16x16x128_f8f6f4 v[104:107], v[8:15], v[208:215], v[104:107]
	v_mfma_f32_16x16x128_f8f6f4 v[148:151], v[16:23], v[184:191], v[148:151]
	v_mfma_f32_16x16x128_f8f6f4 v[140:143], v[24:31], v[184:191], v[140:143]
	v_mfma_f32_16x16x128_f8f6f4 v[132:135], v[16:23], v[192:199], v[132:135]
	v_mfma_f32_16x16x128_f8f6f4 v[124:127], v[24:31], v[192:199], v[124:127]
	v_mfma_f32_16x16x128_f8f6f4 v[116:119], v[16:23], v[200:207], v[116:119]
	v_mfma_f32_16x16x128_f8f6f4 v[108:111], v[24:31], v[200:207], v[108:111]
	v_mfma_f32_16x16x128_f8f6f4 v[100:103], v[16:23], v[208:215], v[100:103]
	v_mfma_f32_16x16x128_f8f6f4 v[96:99], v[24:31], v[208:215], v[96:99]
	s_barrier
	s_add_i32 s34, s74, s43
	v_lshl_add_u64 v[172:173], v[172:173], 0, s[8:9]
	s_mov_b32 m0, s34
	ds_read_b128 v[184:187], v183 offset:49152
	ds_read_b128 v[188:191], v183 offset:50176
	ds_read_b128 v[192:195], v183 offset:51200
	ds_read_b128 v[196:199], v183 offset:52224
	ds_read_b128 v[200:203], v183 offset:53248
	ds_read_b128 v[204:207], v183 offset:54272
	ds_read_b128 v[208:211], v183 offset:55296
	ds_read_b128 v[212:215], v183 offset:56320
	global_load_lds_dwordx4 v[172:173], off
	s_add_i32 m0, s34, 0x2000
	s_add_u32 s34, s36, 0x70080
	v_lshl_add_u64 v[172:173], v[174:175], 0, s[8:9]
	s_addc_u32 s35, s37, 0
	s_add_i32 s36, s75, s43
	global_load_lds_dwordx4 v[172:173], off
	v_lshl_add_u64 v[172:173], s[34:35], 0, v[160:161]
	s_mov_b32 m0, s36
	s_nop 0
	global_load_lds_dwordx4 v[172:173], off
	v_lshl_add_u64 v[172:173], s[34:35], 0, v[162:163]
	s_add_i32 m0, s36, 0x2000
	s_nop 0
	global_load_lds_dwordx4 v[172:173], off
	v_lshl_add_u64 v[172:173], v[176:177], 0, s[8:9]
	s_mov_b32 m0, s51
	s_nop 0
	global_load_lds_dwordx4 v[172:173], off
	v_lshl_add_u64 v[172:173], v[178:179], 0, s[8:9]
	s_mov_b32 m0, s52
	s_nop 0
	global_load_lds_dwordx4 v[172:173], off
	s_waitcnt vmcnt(8)
	s_waitcnt lgkmcnt(0)
	s_barrier
	s_waitcnt lgkmcnt(0)
	v_mfma_f32_16x16x128_f8f6f4 v[92:95], v[0:7], v[184:191], v[92:95]
	v_mfma_f32_16x16x128_f8f6f4 v[88:91], v[8:15], v[184:191], v[88:91]
	v_mfma_f32_16x16x128_f8f6f4 v[80:83], v[0:7], v[192:199], v[80:83]
	v_mfma_f32_16x16x128_f8f6f4 v[72:75], v[8:15], v[192:199], v[72:75]
	v_mfma_f32_16x16x128_f8f6f4 v[64:67], v[0:7], v[200:207], v[64:67]
	v_mfma_f32_16x16x128_f8f6f4 v[56:59], v[8:15], v[200:207], v[56:59]
	v_mfma_f32_16x16x128_f8f6f4 v[48:51], v[0:7], v[208:215], v[48:51]
	v_mfma_f32_16x16x128_f8f6f4 v[40:43], v[8:15], v[208:215], v[40:43]
	v_mfma_f32_16x16x128_f8f6f4 v[84:87], v[16:23], v[184:191], v[84:87]
	v_mfma_f32_16x16x128_f8f6f4 v[76:79], v[24:31], v[184:191], v[76:79]
	v_mfma_f32_16x16x128_f8f6f4 v[68:71], v[16:23], v[192:199], v[68:71]
	v_mfma_f32_16x16x128_f8f6f4 v[60:63], v[24:31], v[192:199], v[60:63]
	v_mfma_f32_16x16x128_f8f6f4 v[52:55], v[16:23], v[200:207], v[52:55]
	v_mfma_f32_16x16x128_f8f6f4 v[44:47], v[24:31], v[200:207], v[44:47]
	v_mfma_f32_16x16x128_f8f6f4 v[36:39], v[16:23], v[208:215], v[36:39]
	v_mfma_f32_16x16x128_f8f6f4 v[32:35], v[24:31], v[208:215], v[32:35]
	s_barrier
	s_add_i32 s73, s73, 2
	s_add_u32 s71, s71, 0x100
	s_addc_u32 s72, s72, 0
	s_cmp_gt_u32 s73, 25
	s_mov_b64 s[34:35], s[30:31]
	s_cbranch_scc0 .LBB0_1718
	s_and_b64 vcc, exec, s[10:11]
	s_cbranch_vccz .LBB0_1721
	s_barrier
